# PEER up re-timed like down: second row buffer in unused registers, rows of the token two ahead refilled right after a buffer's last access, one counted wait per token block
# speedup vs baseline: 1.0275x; 1.0020x over previous
; DI int tidx() { int t = threadIdx.x & 255; asm volatile("" : "+v"(t)); return t; }
; DI int ftid() { int t = threadIdx.x; asm volatile("" : "+v"(t)); return t; }
; #define PU_IDX(t, E, C) do { const char* eb_ = eiu + (size_t)(t) * 512; const char* cb_ = cfu + (size_t)(t) * 512; \
;     _Pragma("unroll") for (int q = 0; q < 4; ++q) { E[q] = *(const i32x4_t*)(eb_ + (eio + 16u * q)); C[q] = *(const f32x4*)(cb_ + (eio + 16u * q)); } } while (0)
; #define PU_TAB(E, W) do { _Pragma("unroll") for (int q = 0; q < 16; ++q) W[q] = *(const u32x4*)(tabu + ((unsigned)E[q >> 2][q & 3] * 128u + tabo)); } while (0)
; DI void phase_peerup(const Params& p, int bid, int nb) {
;   const int lane = tidx() & 63, wid = __builtin_amdgcn_readfirstlane(ftid() >> 6), e8 = lane >> 3, c = lane & 7;
;   const int x = bid & 7, gw = (bid >> 3) * 8 + wid, nw = (nb >> 3) * 8;
;   const char* tabu = p.ws + WS_PV + (size_t)x * 16384 * 128; const unsigned tabo = 16u * c;
;   const char* eiu = p.ws + WS_EIDX; const char* cfu = p.ws + WS_COEF; const unsigned eio = 64u * e8;
;   bf16_t* y2 = (bf16_t*)(p.ws + WS_Y2) + 128 * x + 16 * c; float* ssq = (float*)(p.ws + WS_SSQ) + (size_t)x * T_;
;   const bool b3 = (lane & 8) != 0;
;     ...
;   i32x4_t eA[4], eB[4]; f32x4 cA[4], cB[4]; u32x4 w[16];
;   int t = gw; if (t >= T_) return;
;   PU_IDX(t, eA, cA);
;   for (;;) {
;     PU_TAB(eA, w);
;     const int t1 = t + nw; if (t1 < T_) PU_IDX(t1, eB, cB);
.LBB0_1876:
	s_or_b64 exec, exec, s[0:1]
	s_waitcnt vmcnt(14)
	v_mov_b32_e32 v32, v206
	s_waitcnt lgkmcnt(0)
	s_barrier
	s_nop 0
	v_readfirstlane_b32 s0, v207
	s_ashr_i32 s0, s0, 6
	s_add_i32 s8, s0, s49
	s_cmpk_gt_i32 s8, 0x7fff
	s_cbranch_scc1 .LBB0_1889
	s_add_u32 s0, s84, s48
	s_addc_u32 s1, s85, 0
	s_add_u32 s4, s0, 0xf000000
	s_addc_u32 s5, s1, 0
	s_lshl_b32 s0, s19, 17
	s_add_u32 s0, s84, s0
	s_addc_u32 s1, s85, 0
	s_add_u32 s12, s0, 0x3000000
	v_lshlrev_b32_e32 v0, 4, v32
	s_addc_u32 s13, s1, 0
	s_lshl_b32 s0, s19, 8
	v_and_b32_e32 v136, 0x70, v0
	s_add_u32 s0, s58, s0
	s_addc_u32 s1, s59, 0
	v_lshlrev_b32_e32 v128, 1, v136
	v_mov_b32_e32 v129, 0
	s_ashr_i32 s9, s8, 31
	v_lshl_add_u64 v[34:35], s[0:1], 0, v[128:129]
	s_lshl_b64 s[0:1], s[8:9], 9
	s_add_u32 s2, s16, s0
	v_bfe_u32 v33, v32, 3, 3
	s_addc_u32 s3, s17, s1
	v_lshlrev_b32_e32 v128, 6, v33
	s_add_u32 s0, s56, s0
	s_addc_u32 s1, s57, s1
	v_and_b32_e32 v36, 8, v32
	v_cmp_eq_u32_e64 s[0:1], 0, v36
	v_and_b32_e32 v36, 63, v32
	v_lshlrev_b32_e32 v32, 2, v33
	v_mov_b32_e32 v33, v129
	v_lshl_add_u64 v[130:131], v[34:35], 0, v[32:33]
	v_cmp_eq_u32_e64 s[2:3], 0, v36
	v_lshl_add_u64 v[132:133], s[16:17], 0, v[128:129]
	v_lshl_add_u64 v[134:135], s[56:57], 0, v[128:129]
	s_and_b32 s14, s90, -16
	s_mov_b32 s20, s8
	s_mov_b32 s23, 0
	s_add_u32 s22, s20, 0x0
	s_lshl_b32 s22, s22, 9
	v_lshl_add_u64 v[12:13], v[132:133], 0, s[22:23]
	global_load_dwordx4 v[0:3], v[12:13], off offset:48
	global_load_dwordx4 v[4:7], v[12:13], off offset:32
	global_load_dwordx4 v[8:11], v[12:13], off offset:16
	s_nop 0
	global_load_dwordx4 v[12:15], v[12:13], off
	s_add_u32 s22, s20, 0x0
	s_lshl_b32 s22, s22, 9
	v_lshl_add_u64 v[28:29], v[134:135], 0, s[22:23]
	global_load_dwordx4 v[16:19], v[28:29], off offset:48
	global_load_dwordx4 v[20:23], v[28:29], off offset:32
	global_load_dwordx4 v[24:27], v[28:29], off offset:16
	s_nop 0
	global_load_dwordx4 v[28:31], v[28:29], off
	s_add_u32 s22, s20, 0x100
	s_lshl_b32 s22, s22, 9
	v_lshl_add_u64 v[32:33], v[132:133], 0, s[22:23]
	global_load_dwordx4 v[44:47], v[32:33], off offset:48
	global_load_dwordx4 v[40:43], v[32:33], off offset:32
	global_load_dwordx4 v[36:39], v[32:33], off offset:16
	s_nop 0
	global_load_dwordx4 v[32:35], v[32:33], off
	s_add_u32 s22, s20, 0x100
	s_lshl_b32 s22, s22, 9
	v_lshl_add_u64 v[48:49], v[134:135], 0, s[22:23]
	global_load_dwordx4 v[60:63], v[48:49], off offset:48
	global_load_dwordx4 v[56:59], v[48:49], off offset:32
	global_load_dwordx4 v[52:55], v[48:49], off offset:16
	s_nop 0
	global_load_dwordx4 v[48:51], v[48:49], off
	s_waitcnt vmcnt(12)
	v_lshl_or_b32 v12, v12, 7, v136
	global_load_dwordx4 v[124:127], v12, s[4:5]
	v_lshl_or_b32 v13, v13, 7, v136
	global_load_dwordx4 v[120:123], v13, s[4:5]
	v_lshl_or_b32 v14, v14, 7, v136
	global_load_dwordx4 v[116:119], v14, s[4:5]
	v_lshl_or_b32 v15, v15, 7, v136
	global_load_dwordx4 v[112:115], v15, s[4:5]
	v_lshl_or_b32 v8, v8, 7, v136
	global_load_dwordx4 v[108:111], v8, s[4:5]
	v_lshl_or_b32 v9, v9, 7, v136
	global_load_dwordx4 v[104:107], v9, s[4:5]
	v_lshl_or_b32 v10, v10, 7, v136
	global_load_dwordx4 v[100:103], v10, s[4:5]
	v_lshl_or_b32 v11, v11, 7, v136
	global_load_dwordx4 v[96:99], v11, s[4:5]
	v_lshl_or_b32 v4, v4, 7, v136
	global_load_dwordx4 v[92:95], v4, s[4:5]
	v_lshl_or_b32 v5, v5, 7, v136
	global_load_dwordx4 v[88:91], v5, s[4:5]
	v_lshl_or_b32 v6, v6, 7, v136
	global_load_dwordx4 v[84:87], v6, s[4:5]
	v_lshl_or_b32 v7, v7, 7, v136
	global_load_dwordx4 v[80:83], v7, s[4:5]
	v_lshl_or_b32 v0, v0, 7, v136
	global_load_dwordx4 v[76:79], v0, s[4:5]
	v_lshl_or_b32 v1, v1, 7, v136
	global_load_dwordx4 v[72:75], v1, s[4:5]
	v_lshl_or_b32 v2, v2, 7, v136
	global_load_dwordx4 v[68:71], v2, s[4:5]
	v_lshl_or_b32 v3, v3, 7, v136
	global_load_dwordx4 v[64:67], v3, s[4:5]
	s_add_u32 s22, s20, 0x200
	s_lshl_b32 s22, s22, 9
	v_lshl_add_u64 v[12:13], v[132:133], 0, s[22:23]
	global_load_dwordx4 v[0:3], v[12:13], off offset:48
	global_load_dwordx4 v[4:7], v[12:13], off offset:32
	global_load_dwordx4 v[8:11], v[12:13], off offset:16
	s_nop 0
	global_load_dwordx4 v[12:15], v[12:13], off
	s_waitcnt vmcnt(24)
	v_lshl_or_b32 v32, v32, 7, v136
	global_load_dwordx4 v[240:243], v32, s[4:5]
	v_lshl_or_b32 v33, v33, 7, v136
	global_load_dwordx4 v[236:239], v33, s[4:5]
	v_lshl_or_b32 v34, v34, 7, v136
	global_load_dwordx4 v[232:235], v34, s[4:5]
	v_lshl_or_b32 v35, v35, 7, v136
	global_load_dwordx4 v[228:231], v35, s[4:5]
	v_lshl_or_b32 v36, v36, 7, v136
	global_load_dwordx4 v[224:227], v36, s[4:5]
	v_lshl_or_b32 v37, v37, 7, v136
	global_load_dwordx4 v[220:223], v37, s[4:5]
	v_lshl_or_b32 v38, v38, 7, v136
	global_load_dwordx4 v[216:219], v38, s[4:5]
	v_lshl_or_b32 v39, v39, 7, v136
	global_load_dwordx4 v[212:215], v39, s[4:5]
	v_lshl_or_b32 v40, v40, 7, v136
	global_load_dwordx4 v[200:203], v40, s[4:5]
	v_lshl_or_b32 v41, v41, 7, v136
	global_load_dwordx4 v[196:199], v41, s[4:5]
	v_lshl_or_b32 v42, v42, 7, v136
	global_load_dwordx4 v[192:195], v42, s[4:5]
	v_lshl_or_b32 v43, v43, 7, v136
	global_load_dwordx4 v[184:187], v43, s[4:5]
	v_lshl_or_b32 v44, v44, 7, v136
	global_load_dwordx4 v[180:183], v44, s[4:5]
	v_lshl_or_b32 v45, v45, 7, v136
	global_load_dwordx4 v[172:175], v45, s[4:5]
	v_lshl_or_b32 v46, v46, 7, v136
	global_load_dwordx4 v[168:171], v46, s[4:5]
	v_lshl_or_b32 v47, v47, 7, v136
	global_load_dwordx4 v[164:167], v47, s[4:5]
	s_add_u32 s22, s20, 0x300
	s_lshl_b32 s22, s22, 9
	v_lshl_add_u64 v[32:33], v[132:133], 0, s[22:23]
	global_load_dwordx4 v[44:47], v[32:33], off offset:48
	global_load_dwordx4 v[40:43], v[32:33], off offset:32
	global_load_dwordx4 v[36:39], v[32:33], off offset:16
	s_nop 0
	global_load_dwordx4 v[32:35], v[32:33], off
	s_mov_b32 s8, s20
	s_waitcnt vmcnt(20)
	v_cvt_pk_f32_fp8_e32 v[138:139], v124
	v_cvt_pk_f32_fp8_sdwa v[140:141], v124 src0_sel:WORD_1
	v_cvt_pk_f32_fp8_e32 v[142:143], v125
	v_cvt_pk_f32_fp8_sdwa v[124:125], v125 src0_sel:WORD_1
	v_cvt_pk_f32_fp8_e32 v[144:145], v126
	v_cvt_pk_f32_fp8_sdwa v[146:147], v126 src0_sel:WORD_1
	v_cvt_pk_f32_fp8_e32 v[148:149], v127
	v_cvt_pk_f32_fp8_sdwa v[126:127], v127 src0_sel:WORD_1
	v_cvt_pk_f32_fp8_e32 v[150:151], v120
	v_cvt_pk_f32_fp8_sdwa v[152:153], v120 src0_sel:WORD_1
	v_cvt_pk_f32_fp8_e32 v[154:155], v121
	v_cvt_pk_f32_fp8_sdwa v[120:121], v121 src0_sel:WORD_1
	v_cvt_pk_f32_fp8_e32 v[156:157], v122
	v_cvt_pk_f32_fp8_sdwa v[158:159], v122 src0_sel:WORD_1
	v_cvt_pk_f32_fp8_e32 v[160:161], v123
	v_cvt_pk_f32_fp8_sdwa v[122:123], v123 src0_sel:WORD_1
	v_pk_fma_f32 v[138:139], v[138:139], v[28:29], 0 op_sel_hi:[1,0,0]
	v_pk_fma_f32 v[140:141], v[140:141], v[28:29], 0 op_sel_hi:[1,0,0]
	v_pk_fma_f32 v[142:143], v[142:143], v[28:29], 0 op_sel_hi:[1,0,0]
	v_pk_fma_f32 v[124:125], v[124:125], v[28:29], 0 op_sel_hi:[1,0,0]
	v_pk_fma_f32 v[144:145], v[144:145], v[28:29], 0 op_sel_hi:[1,0,0]
	v_pk_fma_f32 v[146:147], v[146:147], v[28:29], 0 op_sel_hi:[1,0,0]
	v_pk_fma_f32 v[148:149], v[148:149], v[28:29], 0 op_sel_hi:[1,0,0]
	v_pk_fma_f32 v[126:127], v[126:127], v[28:29], 0 op_sel_hi:[1,0,0]
	v_pk_fma_f32 v[138:139], v[150:151], v[28:29], v[138:139] op_sel:[0,1,0]
	v_pk_fma_f32 v[140:141], v[152:153], v[28:29], v[140:141] op_sel:[0,1,0]
	v_pk_fma_f32 v[142:143], v[154:155], v[28:29], v[142:143] op_sel:[0,1,0]
	v_pk_fma_f32 v[120:121], v[120:121], v[28:29], v[124:125] op_sel:[0,1,0]
	v_pk_fma_f32 v[124:125], v[156:157], v[28:29], v[144:145] op_sel:[0,1,0]
	v_pk_fma_f32 v[144:145], v[158:159], v[28:29], v[146:147] op_sel:[0,1,0]
	v_pk_fma_f32 v[146:147], v[160:161], v[28:29], v[148:149] op_sel:[0,1,0]
	v_pk_fma_f32 v[122:123], v[122:123], v[28:29], v[126:127] op_sel:[0,1,0]
	v_cvt_pk_f32_fp8_e32 v[126:127], v116
	v_cvt_pk_f32_fp8_sdwa v[148:149], v116 src0_sel:WORD_1
	v_cvt_pk_f32_fp8_e32 v[150:151], v117
	v_cvt_pk_f32_fp8_sdwa v[116:117], v117 src0_sel:WORD_1
	v_cvt_pk_f32_fp8_e32 v[152:153], v118
	v_cvt_pk_f32_fp8_sdwa v[154:155], v118 src0_sel:WORD_1
	v_cvt_pk_f32_fp8_e32 v[156:157], v119
	v_cvt_pk_f32_fp8_sdwa v[118:119], v119 src0_sel:WORD_1
	v_pk_fma_f32 v[126:127], v[126:127], v[30:31], v[138:139] op_sel_hi:[1,0,1]
	v_pk_fma_f32 v[138:139], v[148:149], v[30:31], v[140:141] op_sel_hi:[1,0,1]
	v_pk_fma_f32 v[140:141], v[150:151], v[30:31], v[142:143] op_sel_hi:[1,0,1]
	v_pk_fma_f32 v[116:117], v[116:117], v[30:31], v[120:121] op_sel_hi:[1,0,1]
	v_pk_fma_f32 v[120:121], v[152:153], v[30:31], v[124:125] op_sel_hi:[1,0,1]
	v_pk_fma_f32 v[124:125], v[154:155], v[30:31], v[144:145] op_sel_hi:[1,0,1]
	v_pk_fma_f32 v[142:143], v[156:157], v[30:31], v[146:147] op_sel_hi:[1,0,1]
	v_pk_fma_f32 v[118:119], v[118:119], v[30:31], v[122:123] op_sel_hi:[1,0,1]
	v_cvt_pk_f32_fp8_e32 v[122:123], v112
	v_cvt_pk_f32_fp8_sdwa v[144:145], v112 src0_sel:WORD_1
	v_cvt_pk_f32_fp8_e32 v[146:147], v113
	v_cvt_pk_f32_fp8_sdwa v[112:113], v113 src0_sel:WORD_1
	v_cvt_pk_f32_fp8_e32 v[148:149], v114
	v_cvt_pk_f32_fp8_sdwa v[150:151], v114 src0_sel:WORD_1
	v_cvt_pk_f32_fp8_e32 v[152:153], v115
	v_cvt_pk_f32_fp8_sdwa v[114:115], v115 src0_sel:WORD_1
	v_mov_b32_e32 v128, v31
	v_pk_fma_f32 v[122:123], v[122:123], v[128:129], v[126:127] op_sel_hi:[1,0,1]
	v_pk_fma_f32 v[126:127], v[144:145], v[128:129], v[138:139] op_sel_hi:[1,0,1]
	v_pk_fma_f32 v[138:139], v[146:147], v[128:129], v[140:141] op_sel_hi:[1,0,1]
	v_pk_fma_f32 v[112:113], v[112:113], v[128:129], v[116:117] op_sel_hi:[1,0,1]
	v_pk_fma_f32 v[116:117], v[148:149], v[128:129], v[120:121] op_sel_hi:[1,0,1]
	v_pk_fma_f32 v[120:121], v[150:151], v[128:129], v[124:125] op_sel_hi:[1,0,1]
	v_pk_fma_f32 v[124:125], v[152:153], v[128:129], v[142:143] op_sel_hi:[1,0,1]
	v_pk_fma_f32 v[114:115], v[114:115], v[128:129], v[118:119] op_sel_hi:[1,0,1]
	v_cvt_pk_f32_fp8_e32 v[118:119], v108
	v_cvt_pk_f32_fp8_sdwa v[140:141], v108 src0_sel:WORD_1
	v_cvt_pk_f32_fp8_e32 v[142:143], v109
	v_cvt_pk_f32_fp8_sdwa v[108:109], v109 src0_sel:WORD_1
	v_cvt_pk_f32_fp8_e32 v[144:145], v110
	v_cvt_pk_f32_fp8_sdwa v[146:147], v110 src0_sel:WORD_1
	v_cvt_pk_f32_fp8_e32 v[148:149], v111
	v_cvt_pk_f32_fp8_sdwa v[110:111], v111 src0_sel:WORD_1
	v_pk_fma_f32 v[118:119], v[118:119], v[24:25], v[122:123] op_sel_hi:[1,0,1]
	v_pk_fma_f32 v[122:123], v[140:141], v[24:25], v[126:127] op_sel_hi:[1,0,1]
	v_pk_fma_f32 v[126:127], v[142:143], v[24:25], v[138:139] op_sel_hi:[1,0,1]
	v_pk_fma_f32 v[108:109], v[108:109], v[24:25], v[112:113] op_sel_hi:[1,0,1]
	v_pk_fma_f32 v[112:113], v[144:145], v[24:25], v[116:117] op_sel_hi:[1,0,1]
	v_pk_fma_f32 v[116:117], v[146:147], v[24:25], v[120:121] op_sel_hi:[1,0,1]
	v_pk_fma_f32 v[120:121], v[148:149], v[24:25], v[124:125] op_sel_hi:[1,0,1]
	v_pk_fma_f32 v[110:111], v[110:111], v[24:25], v[114:115] op_sel_hi:[1,0,1]
	v_cvt_pk_f32_fp8_e32 v[114:115], v104
	v_cvt_pk_f32_fp8_sdwa v[124:125], v104 src0_sel:WORD_1
	v_cvt_pk_f32_fp8_e32 v[138:139], v105
	v_cvt_pk_f32_fp8_sdwa v[104:105], v105 src0_sel:WORD_1
	v_cvt_pk_f32_fp8_e32 v[140:141], v106
	v_cvt_pk_f32_fp8_sdwa v[142:143], v106 src0_sel:WORD_1
	v_cvt_pk_f32_fp8_e32 v[144:145], v107
	v_cvt_pk_f32_fp8_sdwa v[106:107], v107 src0_sel:WORD_1
	v_pk_fma_f32 v[114:115], v[114:115], v[24:25], v[118:119] op_sel:[0,1,0]
	v_pk_fma_f32 v[118:119], v[124:125], v[24:25], v[122:123] op_sel:[0,1,0]
	v_pk_fma_f32 v[122:123], v[138:139], v[24:25], v[126:127] op_sel:[0,1,0]
	v_pk_fma_f32 v[104:105], v[104:105], v[24:25], v[108:109] op_sel:[0,1,0]
	v_pk_fma_f32 v[108:109], v[140:141], v[24:25], v[112:113] op_sel:[0,1,0]
	v_pk_fma_f32 v[112:113], v[142:143], v[24:25], v[116:117] op_sel:[0,1,0]
	v_pk_fma_f32 v[116:117], v[144:145], v[24:25], v[120:121] op_sel:[0,1,0]
	v_pk_fma_f32 v[106:107], v[106:107], v[24:25], v[110:111] op_sel:[0,1,0]
	v_cvt_pk_f32_fp8_e32 v[110:111], v100
	v_cvt_pk_f32_fp8_sdwa v[120:121], v100 src0_sel:WORD_1
	v_cvt_pk_f32_fp8_e32 v[124:125], v101
	v_cvt_pk_f32_fp8_sdwa v[100:101], v101 src0_sel:WORD_1
	v_cvt_pk_f32_fp8_e32 v[126:127], v102
	v_cvt_pk_f32_fp8_sdwa v[138:139], v102 src0_sel:WORD_1
	v_cvt_pk_f32_fp8_e32 v[140:141], v103
	v_cvt_pk_f32_fp8_sdwa v[102:103], v103 src0_sel:WORD_1
	v_pk_fma_f32 v[110:111], v[110:111], v[26:27], v[114:115] op_sel_hi:[1,0,1]
	v_pk_fma_f32 v[114:115], v[120:121], v[26:27], v[118:119] op_sel_hi:[1,0,1]
	v_pk_fma_f32 v[118:119], v[124:125], v[26:27], v[122:123] op_sel_hi:[1,0,1]
	v_pk_fma_f32 v[100:101], v[100:101], v[26:27], v[104:105] op_sel_hi:[1,0,1]
	v_pk_fma_f32 v[104:105], v[126:127], v[26:27], v[108:109] op_sel_hi:[1,0,1]
	v_pk_fma_f32 v[108:109], v[138:139], v[26:27], v[112:113] op_sel_hi:[1,0,1]
	v_pk_fma_f32 v[112:113], v[140:141], v[26:27], v[116:117] op_sel_hi:[1,0,1]
	v_pk_fma_f32 v[102:103], v[102:103], v[26:27], v[106:107] op_sel_hi:[1,0,1]
	v_cvt_pk_f32_fp8_e32 v[106:107], v96
	v_cvt_pk_f32_fp8_sdwa v[116:117], v96 src0_sel:WORD_1
	v_cvt_pk_f32_fp8_e32 v[120:121], v97
	v_cvt_pk_f32_fp8_sdwa v[96:97], v97 src0_sel:WORD_1
	v_cvt_pk_f32_fp8_e32 v[122:123], v98
	v_cvt_pk_f32_fp8_sdwa v[124:125], v98 src0_sel:WORD_1
	v_cvt_pk_f32_fp8_e32 v[126:127], v99
	v_cvt_pk_f32_fp8_sdwa v[98:99], v99 src0_sel:WORD_1
	v_mov_b32_e32 v128, v27
	v_pk_fma_f32 v[106:107], v[106:107], v[128:129], v[110:111] op_sel_hi:[1,0,1]
	v_pk_fma_f32 v[110:111], v[116:117], v[128:129], v[114:115] op_sel_hi:[1,0,1]
	v_pk_fma_f32 v[114:115], v[120:121], v[128:129], v[118:119] op_sel_hi:[1,0,1]
	v_pk_fma_f32 v[96:97], v[96:97], v[128:129], v[100:101] op_sel_hi:[1,0,1]
	v_pk_fma_f32 v[100:101], v[122:123], v[128:129], v[104:105] op_sel_hi:[1,0,1]
	v_pk_fma_f32 v[104:105], v[124:125], v[128:129], v[108:109] op_sel_hi:[1,0,1]
	v_pk_fma_f32 v[108:109], v[126:127], v[128:129], v[112:113] op_sel_hi:[1,0,1]
	v_lshl_or_b32 v12, v12, 7, v136
	global_load_dwordx4 v[124:127], v12, s[4:5]
	v_pk_fma_f32 v[98:99], v[98:99], v[128:129], v[102:103] op_sel_hi:[1,0,1]
	v_cvt_pk_f32_fp8_e32 v[102:103], v92
	v_cvt_pk_f32_fp8_sdwa v[112:113], v92 src0_sel:WORD_1
	v_cvt_pk_f32_fp8_e32 v[116:117], v93
	v_cvt_pk_f32_fp8_sdwa v[92:93], v93 src0_sel:WORD_1
	v_cvt_pk_f32_fp8_e32 v[118:119], v94
	v_cvt_pk_f32_fp8_sdwa v[120:121], v94 src0_sel:WORD_1
	v_cvt_pk_f32_fp8_e32 v[122:123], v95
	v_cvt_pk_f32_fp8_sdwa v[94:95], v95 src0_sel:WORD_1
	v_pk_fma_f32 v[102:103], v[102:103], v[20:21], v[106:107] op_sel_hi:[1,0,1]
	v_pk_fma_f32 v[106:107], v[112:113], v[20:21], v[110:111] op_sel_hi:[1,0,1]
	v_pk_fma_f32 v[110:111], v[116:117], v[20:21], v[114:115] op_sel_hi:[1,0,1]
	v_pk_fma_f32 v[92:93], v[92:93], v[20:21], v[96:97] op_sel_hi:[1,0,1]
	v_pk_fma_f32 v[96:97], v[118:119], v[20:21], v[100:101] op_sel_hi:[1,0,1]
	v_pk_fma_f32 v[100:101], v[120:121], v[20:21], v[104:105] op_sel_hi:[1,0,1]
	v_pk_fma_f32 v[104:105], v[122:123], v[20:21], v[108:109] op_sel_hi:[1,0,1]
	v_lshl_or_b32 v13, v13, 7, v136
	global_load_dwordx4 v[120:123], v13, s[4:5]
	v_pk_fma_f32 v[94:95], v[94:95], v[20:21], v[98:99] op_sel_hi:[1,0,1]
	v_cvt_pk_f32_fp8_e32 v[98:99], v88
	v_cvt_pk_f32_fp8_sdwa v[108:109], v88 src0_sel:WORD_1
	v_cvt_pk_f32_fp8_e32 v[112:113], v89
	v_cvt_pk_f32_fp8_sdwa v[88:89], v89 src0_sel:WORD_1
	v_cvt_pk_f32_fp8_e32 v[114:115], v90
	v_cvt_pk_f32_fp8_sdwa v[116:117], v90 src0_sel:WORD_1
	v_cvt_pk_f32_fp8_e32 v[118:119], v91
	v_cvt_pk_f32_fp8_sdwa v[90:91], v91 src0_sel:WORD_1
	v_pk_fma_f32 v[98:99], v[98:99], v[20:21], v[102:103] op_sel:[0,1,0]
	v_pk_fma_f32 v[102:103], v[108:109], v[20:21], v[106:107] op_sel:[0,1,0]
	v_pk_fma_f32 v[106:107], v[112:113], v[20:21], v[110:111] op_sel:[0,1,0]
	v_pk_fma_f32 v[88:89], v[88:89], v[20:21], v[92:93] op_sel:[0,1,0]
	v_pk_fma_f32 v[92:93], v[114:115], v[20:21], v[96:97] op_sel:[0,1,0]
	v_pk_fma_f32 v[96:97], v[116:117], v[20:21], v[100:101] op_sel:[0,1,0]
	v_pk_fma_f32 v[100:101], v[118:119], v[20:21], v[104:105] op_sel:[0,1,0]
	v_lshl_or_b32 v14, v14, 7, v136
	global_load_dwordx4 v[116:119], v14, s[4:5]
	v_pk_fma_f32 v[90:91], v[90:91], v[20:21], v[94:95] op_sel:[0,1,0]
	v_cvt_pk_f32_fp8_e32 v[94:95], v84
	v_cvt_pk_f32_fp8_sdwa v[104:105], v84 src0_sel:WORD_1
	v_cvt_pk_f32_fp8_e32 v[108:109], v85
	v_cvt_pk_f32_fp8_sdwa v[84:85], v85 src0_sel:WORD_1
	v_cvt_pk_f32_fp8_e32 v[110:111], v86
	v_cvt_pk_f32_fp8_sdwa v[112:113], v86 src0_sel:WORD_1
	v_cvt_pk_f32_fp8_e32 v[114:115], v87
	v_cvt_pk_f32_fp8_sdwa v[86:87], v87 src0_sel:WORD_1
	v_pk_fma_f32 v[94:95], v[94:95], v[22:23], v[98:99] op_sel_hi:[1,0,1]
	v_pk_fma_f32 v[98:99], v[104:105], v[22:23], v[102:103] op_sel_hi:[1,0,1]
	v_pk_fma_f32 v[102:103], v[108:109], v[22:23], v[106:107] op_sel_hi:[1,0,1]
	v_pk_fma_f32 v[84:85], v[84:85], v[22:23], v[88:89] op_sel_hi:[1,0,1]
	v_pk_fma_f32 v[88:89], v[110:111], v[22:23], v[92:93] op_sel_hi:[1,0,1]
	v_pk_fma_f32 v[92:93], v[112:113], v[22:23], v[96:97] op_sel_hi:[1,0,1]
	v_pk_fma_f32 v[96:97], v[114:115], v[22:23], v[100:101] op_sel_hi:[1,0,1]
	v_pk_fma_f32 v[86:87], v[86:87], v[22:23], v[90:91] op_sel_hi:[1,0,1]
	v_cvt_pk_f32_fp8_e32 v[90:91], v80
	v_cvt_pk_f32_fp8_sdwa v[100:101], v80 src0_sel:WORD_1
	v_cvt_pk_f32_fp8_e32 v[104:105], v81
	v_cvt_pk_f32_fp8_sdwa v[80:81], v81 src0_sel:WORD_1
	v_cvt_pk_f32_fp8_e32 v[106:107], v82
	v_cvt_pk_f32_fp8_sdwa v[108:109], v82 src0_sel:WORD_1
	v_cvt_pk_f32_fp8_e32 v[110:111], v83
	v_cvt_pk_f32_fp8_sdwa v[82:83], v83 src0_sel:WORD_1
	v_mov_b32_e32 v112, v23
	v_pk_fma_f32 v[90:91], v[90:91], v[112:113], v[94:95] op_sel_hi:[1,0,1]
	v_pk_fma_f32 v[94:95], v[100:101], v[112:113], v[98:99] op_sel_hi:[1,0,1]
	v_pk_fma_f32 v[98:99], v[104:105], v[112:113], v[102:103] op_sel_hi:[1,0,1]
	v_pk_fma_f32 v[80:81], v[80:81], v[112:113], v[84:85] op_sel_hi:[1,0,1]
	v_pk_fma_f32 v[84:85], v[106:107], v[112:113], v[88:89] op_sel_hi:[1,0,1]
	v_pk_fma_f32 v[88:89], v[108:109], v[112:113], v[92:93] op_sel_hi:[1,0,1]
	v_pk_fma_f32 v[92:93], v[110:111], v[112:113], v[96:97] op_sel_hi:[1,0,1]
	v_lshl_or_b32 v8, v8, 7, v136
	global_load_dwordx4 v[108:111], v8, s[4:5]
	v_pk_fma_f32 v[82:83], v[82:83], v[112:113], v[86:87] op_sel_hi:[1,0,1]
	v_lshl_or_b32 v15, v15, 7, v136
	global_load_dwordx4 v[112:115], v15, s[4:5]
	v_cvt_pk_f32_fp8_e32 v[86:87], v76
	v_cvt_pk_f32_fp8_sdwa v[96:97], v76 src0_sel:WORD_1
	v_cvt_pk_f32_fp8_e32 v[100:101], v77
	v_cvt_pk_f32_fp8_sdwa v[76:77], v77 src0_sel:WORD_1
	v_cvt_pk_f32_fp8_e32 v[102:103], v78
	v_cvt_pk_f32_fp8_sdwa v[104:105], v78 src0_sel:WORD_1
	v_cvt_pk_f32_fp8_e32 v[106:107], v79
	v_cvt_pk_f32_fp8_sdwa v[78:79], v79 src0_sel:WORD_1
	v_pk_fma_f32 v[86:87], v[86:87], v[16:17], v[90:91] op_sel_hi:[1,0,1]
	v_pk_fma_f32 v[90:91], v[96:97], v[16:17], v[94:95] op_sel_hi:[1,0,1]
	v_pk_fma_f32 v[94:95], v[100:101], v[16:17], v[98:99] op_sel_hi:[1,0,1]
	v_pk_fma_f32 v[76:77], v[76:77], v[16:17], v[80:81] op_sel_hi:[1,0,1]
	v_pk_fma_f32 v[80:81], v[102:103], v[16:17], v[84:85] op_sel_hi:[1,0,1]
	v_pk_fma_f32 v[84:85], v[104:105], v[16:17], v[88:89] op_sel_hi:[1,0,1]
	v_pk_fma_f32 v[88:89], v[106:107], v[16:17], v[92:93] op_sel_hi:[1,0,1]
	v_lshl_or_b32 v9, v9, 7, v136
	global_load_dwordx4 v[104:107], v9, s[4:5]
	v_pk_fma_f32 v[78:79], v[78:79], v[16:17], v[82:83] op_sel_hi:[1,0,1]
	v_cvt_pk_f32_fp8_e32 v[82:83], v72
	v_cvt_pk_f32_fp8_sdwa v[92:93], v72 src0_sel:WORD_1
	v_cvt_pk_f32_fp8_e32 v[96:97], v73
	v_cvt_pk_f32_fp8_sdwa v[72:73], v73 src0_sel:WORD_1
	v_cvt_pk_f32_fp8_e32 v[98:99], v74
	v_cvt_pk_f32_fp8_sdwa v[100:101], v74 src0_sel:WORD_1
	v_cvt_pk_f32_fp8_e32 v[102:103], v75
	v_cvt_pk_f32_fp8_sdwa v[74:75], v75 src0_sel:WORD_1
	v_pk_fma_f32 v[82:83], v[82:83], v[16:17], v[86:87] op_sel:[0,1,0]
	v_pk_fma_f32 v[86:87], v[92:93], v[16:17], v[90:91] op_sel:[0,1,0]
	v_pk_fma_f32 v[90:91], v[96:97], v[16:17], v[94:95] op_sel:[0,1,0]
	v_pk_fma_f32 v[72:73], v[72:73], v[16:17], v[76:77] op_sel:[0,1,0]
	v_pk_fma_f32 v[76:77], v[98:99], v[16:17], v[80:81] op_sel:[0,1,0]
	v_pk_fma_f32 v[80:81], v[100:101], v[16:17], v[84:85] op_sel:[0,1,0]
	v_pk_fma_f32 v[84:85], v[102:103], v[16:17], v[88:89] op_sel:[0,1,0]
	v_lshl_or_b32 v10, v10, 7, v136
	global_load_dwordx4 v[100:103], v10, s[4:5]
	v_pk_fma_f32 v[74:75], v[74:75], v[16:17], v[78:79] op_sel:[0,1,0]
	v_cvt_pk_f32_fp8_e32 v[78:79], v68
	v_cvt_pk_f32_fp8_sdwa v[88:89], v68 src0_sel:WORD_1
	v_cvt_pk_f32_fp8_e32 v[92:93], v69
	v_cvt_pk_f32_fp8_sdwa v[68:69], v69 src0_sel:WORD_1
	v_cvt_pk_f32_fp8_e32 v[94:95], v70
	v_cvt_pk_f32_fp8_sdwa v[96:97], v70 src0_sel:WORD_1
	v_cvt_pk_f32_fp8_e32 v[98:99], v71
	v_cvt_pk_f32_fp8_sdwa v[70:71], v71 src0_sel:WORD_1
	v_pk_fma_f32 v[78:79], v[78:79], v[18:19], v[82:83] op_sel_hi:[1,0,1]
	v_pk_fma_f32 v[82:83], v[88:89], v[18:19], v[86:87] op_sel_hi:[1,0,1]
	v_pk_fma_f32 v[86:87], v[92:93], v[18:19], v[90:91] op_sel_hi:[1,0,1]
	v_pk_fma_f32 v[68:69], v[68:69], v[18:19], v[72:73] op_sel_hi:[1,0,1]
	v_pk_fma_f32 v[72:73], v[94:95], v[18:19], v[76:77] op_sel_hi:[1,0,1]
	v_pk_fma_f32 v[76:77], v[96:97], v[18:19], v[80:81] op_sel_hi:[1,0,1]
	v_pk_fma_f32 v[80:81], v[98:99], v[18:19], v[84:85] op_sel_hi:[1,0,1]
	v_pk_fma_f32 v[70:71], v[70:71], v[18:19], v[74:75] op_sel_hi:[1,0,1]
	v_cvt_pk_f32_fp8_e32 v[74:75], v64
	v_cvt_pk_f32_fp8_sdwa v[84:85], v64 src0_sel:WORD_1
	v_cvt_pk_f32_fp8_e32 v[88:89], v65
	v_cvt_pk_f32_fp8_sdwa v[64:65], v65 src0_sel:WORD_1
	v_cvt_pk_f32_fp8_e32 v[90:91], v66
	v_cvt_pk_f32_fp8_sdwa v[92:93], v66 src0_sel:WORD_1
	v_cvt_pk_f32_fp8_e32 v[94:95], v67
	v_cvt_pk_f32_fp8_sdwa v[66:67], v67 src0_sel:WORD_1
	v_mov_b32_e32 v96, v19
	v_pk_fma_f32 v[74:75], v[74:75], v[96:97], v[78:79] op_sel_hi:[1,0,1]
	v_pk_fma_f32 v[78:79], v[84:85], v[96:97], v[82:83] op_sel_hi:[1,0,1]
	v_pk_fma_f32 v[82:83], v[88:89], v[96:97], v[86:87] op_sel_hi:[1,0,1]
	v_lshl_or_b32 v6, v6, 7, v136
	global_load_dwordx4 v[84:87], v6, s[4:5]
	v_pk_fma_f32 v[64:65], v[64:65], v[96:97], v[68:69] op_sel_hi:[1,0,1]
	v_pk_fma_f32 v[68:69], v[90:91], v[96:97], v[72:73] op_sel_hi:[1,0,1]
	v_lshl_or_b32 v5, v5, 7, v136
	global_load_dwordx4 v[88:91], v5, s[4:5]
	v_pk_fma_f32 v[72:73], v[92:93], v[96:97], v[76:77] op_sel_hi:[1,0,1]
	v_pk_fma_f32 v[76:77], v[94:95], v[96:97], v[80:81] op_sel_hi:[1,0,1]
	v_lshl_or_b32 v4, v4, 7, v136
	global_load_dwordx4 v[92:95], v4, s[4:5]
	v_pk_fma_f32 v[66:67], v[66:67], v[96:97], v[70:71] op_sel_hi:[1,0,1]
	v_lshl_or_b32 v11, v11, 7, v136
	global_load_dwordx4 v[96:99], v11, s[4:5]
	v_permlane32_swap_b32_e32 v74, v68
	v_permlane32_swap_b32_e32 v75, v69
	v_permlane32_swap_b32_e32 v78, v72
	v_permlane32_swap_b32_e32 v79, v73
	v_permlane32_swap_b32_e32 v82, v76
	v_permlane32_swap_b32_e32 v83, v77
	v_permlane32_swap_b32_e32 v64, v66
	v_permlane32_swap_b32_e32 v65, v67
	v_add_f32_e32 v68, v74, v68
	v_add_f32_e32 v69, v75, v69
	v_add_f32_e32 v70, v78, v72
	v_add_f32_e32 v71, v79, v73
	v_add_f32_e32 v72, v82, v76
	v_add_f32_e32 v73, v83, v77
	v_lshl_or_b32 v7, v7, 7, v136
	global_load_dwordx4 v[80:83], v7, s[4:5]
	v_lshl_or_b32 v0, v0, 7, v136
	global_load_dwordx4 v[76:79], v0, s[4:5]
	v_add_f32_e32 v64, v64, v66
	v_add_f32_e32 v65, v65, v67
	v_permlane16_swap_b32_e32 v68, v72
	v_permlane16_swap_b32_e32 v69, v73
	v_permlane16_swap_b32_e32 v70, v64
	v_permlane16_swap_b32_e32 v71, v65
	v_pk_add_f32 v[66:67], v[68:69], v[72:73]
	v_lshl_or_b32 v1, v1, 7, v136
	global_load_dwordx4 v[72:75], v1, s[4:5]
	v_pk_add_f32 v[64:65], v[70:71], v[64:65]
	s_ashr_i32 s9, s8, 31
	v_cndmask_b32_e64 v68, v66, v64, s[0:1]
	v_cndmask_b32_e64 v70, v64, v66, s[0:1]
	v_cndmask_b32_e64 v64, v67, v65, s[0:1]
	v_mov_b32_dpp v68, v68 row_ror:8 row_mask:0xf bank_mask:0xf bound_ctrl:1
	v_cndmask_b32_e64 v71, v65, v67, s[0:1]
	v_mov_b32_dpp v69, v64 row_ror:8 row_mask:0xf bank_mask:0xf bound_ctrl:1
	v_pk_add_f32 v[66:67], v[70:71], v[68:69]
	s_lshl_b64 s[10:11], s[8:9], 11
	v_pk_mul_f32 v[64:65], v[66:67], v[66:67]
	v_cvt_pk_bf16_f32 v68, v66, v67
	v_add_f32_e32 v64, v64, v65
	v_lshl_add_u64 v[66:67], v[130:131], 0, s[10:11]
	global_store_dword v[66:67], v68, off
	v_add_f32_dpp v64, v64, v64 quad_perm:[1,0,3,2] row_mask:0xf bank_mask:0xf bound_ctrl:1
	s_nop 1
	v_add_f32_dpp v64, v64, v64 quad_perm:[2,3,0,1] row_mask:0xf bank_mask:0xf bound_ctrl:1
	s_nop 1
	v_add_f32_dpp v64, v64, v64 row_half_mirror row_mask:0xf bank_mask:0xf bound_ctrl:1
	s_nop 1
	v_add_f32_dpp v64, v64, v64 row_ror:8 row_mask:0xf bank_mask:0xf bound_ctrl:1
	v_mov_b32_e32 v65, v64
	s_nop 1
	v_permlane16_swap_b32_e32 v64, v65
	v_add_f32_e32 v64, v64, v65
	v_mov_b32_e32 v65, v64
	s_nop 1
	v_permlane32_swap_b32_e32 v64, v65
	s_and_saveexec_b64 s[10:11], s[2:3]
	s_lshl_b64 s[16:17], s[8:9], 2
	s_add_u32 s16, s12, s16
	v_add_f32_e32 v64, v64, v65
	s_addc_u32 s17, s13, s17
	global_store_dword v129, v64, s[16:17]
	s_or_b64 exec, exec, s[10:11]
	v_lshl_or_b32 v2, v2, 7, v136
	global_load_dwordx4 v[68:71], v2, s[4:5]
	v_lshl_or_b32 v3, v3, 7, v136
	global_load_dwordx4 v[64:67], v3, s[4:5]
	s_add_u32 s22, s20, 0x200
	s_lshl_b32 s22, s22, 9
	v_lshl_add_u64 v[28:29], v[134:135], 0, s[22:23]
	global_load_dwordx4 v[16:19], v[28:29], off offset:48
	global_load_dwordx4 v[20:23], v[28:29], off offset:32
	global_load_dwordx4 v[24:27], v[28:29], off offset:16
	s_nop 0
	global_load_dwordx4 v[28:31], v[28:29], off
	s_add_u32 s22, s20, 0x400
	s_lshl_b32 s22, s22, 9
	v_lshl_add_u64 v[12:13], v[132:133], 0, s[22:23]
	global_load_dwordx4 v[0:3], v[12:13], off offset:48
	global_load_dwordx4 v[4:7], v[12:13], off offset:32
	global_load_dwordx4 v[8:11], v[12:13], off offset:16
	s_nop 0
	global_load_dwordx4 v[12:15], v[12:13], off
	s_add_u32 s6, s20, 0x100
	s_waitcnt vmcnt(26)
	v_cvt_pk_f32_fp8_e32 v[138:139], v240
	v_cvt_pk_f32_fp8_sdwa v[140:141], v240 src0_sel:WORD_1
	v_cvt_pk_f32_fp8_e32 v[142:143], v241
	v_cvt_pk_f32_fp8_sdwa v[240:241], v241 src0_sel:WORD_1
	v_cvt_pk_f32_fp8_e32 v[144:145], v242
	v_cvt_pk_f32_fp8_sdwa v[146:147], v242 src0_sel:WORD_1
	v_cvt_pk_f32_fp8_e32 v[148:149], v243
	v_cvt_pk_f32_fp8_sdwa v[242:243], v243 src0_sel:WORD_1
	v_cvt_pk_f32_fp8_e32 v[150:151], v236
	v_cvt_pk_f32_fp8_sdwa v[152:153], v236 src0_sel:WORD_1
	v_cvt_pk_f32_fp8_e32 v[154:155], v237
	v_cvt_pk_f32_fp8_sdwa v[236:237], v237 src0_sel:WORD_1
	v_cvt_pk_f32_fp8_e32 v[156:157], v238
	v_cvt_pk_f32_fp8_sdwa v[158:159], v238 src0_sel:WORD_1
	v_cvt_pk_f32_fp8_e32 v[160:161], v239
	v_cvt_pk_f32_fp8_sdwa v[238:239], v239 src0_sel:WORD_1
	v_pk_fma_f32 v[138:139], v[138:139], v[48:49], 0 op_sel_hi:[1,0,0]
	v_pk_fma_f32 v[140:141], v[140:141], v[48:49], 0 op_sel_hi:[1,0,0]
	v_pk_fma_f32 v[142:143], v[142:143], v[48:49], 0 op_sel_hi:[1,0,0]
	v_pk_fma_f32 v[240:241], v[240:241], v[48:49], 0 op_sel_hi:[1,0,0]
	v_pk_fma_f32 v[144:145], v[144:145], v[48:49], 0 op_sel_hi:[1,0,0]
	v_pk_fma_f32 v[146:147], v[146:147], v[48:49], 0 op_sel_hi:[1,0,0]
	v_pk_fma_f32 v[148:149], v[148:149], v[48:49], 0 op_sel_hi:[1,0,0]
	v_pk_fma_f32 v[242:243], v[242:243], v[48:49], 0 op_sel_hi:[1,0,0]
	v_pk_fma_f32 v[138:139], v[150:151], v[48:49], v[138:139] op_sel:[0,1,0]
	v_pk_fma_f32 v[140:141], v[152:153], v[48:49], v[140:141] op_sel:[0,1,0]
	v_pk_fma_f32 v[142:143], v[154:155], v[48:49], v[142:143] op_sel:[0,1,0]
	v_pk_fma_f32 v[236:237], v[236:237], v[48:49], v[240:241] op_sel:[0,1,0]
	v_pk_fma_f32 v[240:241], v[156:157], v[48:49], v[144:145] op_sel:[0,1,0]
	v_pk_fma_f32 v[144:145], v[158:159], v[48:49], v[146:147] op_sel:[0,1,0]
	v_pk_fma_f32 v[146:147], v[160:161], v[48:49], v[148:149] op_sel:[0,1,0]
	v_pk_fma_f32 v[238:239], v[238:239], v[48:49], v[242:243] op_sel:[0,1,0]
	v_cvt_pk_f32_fp8_e32 v[242:243], v232
	v_cvt_pk_f32_fp8_sdwa v[148:149], v232 src0_sel:WORD_1
	v_cvt_pk_f32_fp8_e32 v[150:151], v233
	v_cvt_pk_f32_fp8_sdwa v[232:233], v233 src0_sel:WORD_1
	v_cvt_pk_f32_fp8_e32 v[152:153], v234
	v_cvt_pk_f32_fp8_sdwa v[154:155], v234 src0_sel:WORD_1
	v_cvt_pk_f32_fp8_e32 v[156:157], v235
	v_cvt_pk_f32_fp8_sdwa v[234:235], v235 src0_sel:WORD_1
	v_pk_fma_f32 v[242:243], v[242:243], v[50:51], v[138:139] op_sel_hi:[1,0,1]
	v_pk_fma_f32 v[138:139], v[148:149], v[50:51], v[140:141] op_sel_hi:[1,0,1]
	v_pk_fma_f32 v[140:141], v[150:151], v[50:51], v[142:143] op_sel_hi:[1,0,1]
	v_pk_fma_f32 v[232:233], v[232:233], v[50:51], v[236:237] op_sel_hi:[1,0,1]
	v_pk_fma_f32 v[236:237], v[152:153], v[50:51], v[240:241] op_sel_hi:[1,0,1]
	v_pk_fma_f32 v[240:241], v[154:155], v[50:51], v[144:145] op_sel_hi:[1,0,1]
	v_pk_fma_f32 v[142:143], v[156:157], v[50:51], v[146:147] op_sel_hi:[1,0,1]
	v_pk_fma_f32 v[234:235], v[234:235], v[50:51], v[238:239] op_sel_hi:[1,0,1]
	v_cvt_pk_f32_fp8_e32 v[238:239], v228
	v_cvt_pk_f32_fp8_sdwa v[144:145], v228 src0_sel:WORD_1
	v_cvt_pk_f32_fp8_e32 v[146:147], v229
	v_cvt_pk_f32_fp8_sdwa v[228:229], v229 src0_sel:WORD_1
	v_cvt_pk_f32_fp8_e32 v[148:149], v230
	v_cvt_pk_f32_fp8_sdwa v[150:151], v230 src0_sel:WORD_1
	v_cvt_pk_f32_fp8_e32 v[152:153], v231
	v_cvt_pk_f32_fp8_sdwa v[230:231], v231 src0_sel:WORD_1
	v_mov_b32_e32 v128, v51
	v_pk_fma_f32 v[238:239], v[238:239], v[128:129], v[242:243] op_sel_hi:[1,0,1]
	v_pk_fma_f32 v[242:243], v[144:145], v[128:129], v[138:139] op_sel_hi:[1,0,1]
	v_pk_fma_f32 v[138:139], v[146:147], v[128:129], v[140:141] op_sel_hi:[1,0,1]
	v_pk_fma_f32 v[228:229], v[228:229], v[128:129], v[232:233] op_sel_hi:[1,0,1]
	v_pk_fma_f32 v[232:233], v[148:149], v[128:129], v[236:237] op_sel_hi:[1,0,1]
	v_pk_fma_f32 v[236:237], v[150:151], v[128:129], v[240:241] op_sel_hi:[1,0,1]
	v_pk_fma_f32 v[240:241], v[152:153], v[128:129], v[142:143] op_sel_hi:[1,0,1]
	v_pk_fma_f32 v[230:231], v[230:231], v[128:129], v[234:235] op_sel_hi:[1,0,1]
	v_cvt_pk_f32_fp8_e32 v[234:235], v224
	v_cvt_pk_f32_fp8_sdwa v[140:141], v224 src0_sel:WORD_1
	v_cvt_pk_f32_fp8_e32 v[142:143], v225
	v_cvt_pk_f32_fp8_sdwa v[224:225], v225 src0_sel:WORD_1
	v_cvt_pk_f32_fp8_e32 v[144:145], v226
	v_cvt_pk_f32_fp8_sdwa v[146:147], v226 src0_sel:WORD_1
	v_cvt_pk_f32_fp8_e32 v[148:149], v227
	v_cvt_pk_f32_fp8_sdwa v[226:227], v227 src0_sel:WORD_1
	v_pk_fma_f32 v[234:235], v[234:235], v[52:53], v[238:239] op_sel_hi:[1,0,1]
	v_pk_fma_f32 v[238:239], v[140:141], v[52:53], v[242:243] op_sel_hi:[1,0,1]
	v_pk_fma_f32 v[242:243], v[142:143], v[52:53], v[138:139] op_sel_hi:[1,0,1]
	v_pk_fma_f32 v[224:225], v[224:225], v[52:53], v[228:229] op_sel_hi:[1,0,1]
	v_pk_fma_f32 v[228:229], v[144:145], v[52:53], v[232:233] op_sel_hi:[1,0,1]
	v_pk_fma_f32 v[232:233], v[146:147], v[52:53], v[236:237] op_sel_hi:[1,0,1]
	v_pk_fma_f32 v[236:237], v[148:149], v[52:53], v[240:241] op_sel_hi:[1,0,1]
	v_pk_fma_f32 v[226:227], v[226:227], v[52:53], v[230:231] op_sel_hi:[1,0,1]
	v_cvt_pk_f32_fp8_e32 v[230:231], v220
	v_cvt_pk_f32_fp8_sdwa v[240:241], v220 src0_sel:WORD_1
	v_cvt_pk_f32_fp8_e32 v[138:139], v221
	v_cvt_pk_f32_fp8_sdwa v[220:221], v221 src0_sel:WORD_1
	v_cvt_pk_f32_fp8_e32 v[140:141], v222
	v_cvt_pk_f32_fp8_sdwa v[142:143], v222 src0_sel:WORD_1
	v_cvt_pk_f32_fp8_e32 v[144:145], v223
	v_cvt_pk_f32_fp8_sdwa v[222:223], v223 src0_sel:WORD_1
	v_pk_fma_f32 v[230:231], v[230:231], v[52:53], v[234:235] op_sel:[0,1,0]
	v_pk_fma_f32 v[234:235], v[240:241], v[52:53], v[238:239] op_sel:[0,1,0]
	v_pk_fma_f32 v[238:239], v[138:139], v[52:53], v[242:243] op_sel:[0,1,0]
	v_pk_fma_f32 v[220:221], v[220:221], v[52:53], v[224:225] op_sel:[0,1,0]
	v_pk_fma_f32 v[224:225], v[140:141], v[52:53], v[228:229] op_sel:[0,1,0]
	v_pk_fma_f32 v[228:229], v[142:143], v[52:53], v[232:233] op_sel:[0,1,0]
	v_pk_fma_f32 v[232:233], v[144:145], v[52:53], v[236:237] op_sel:[0,1,0]
	v_pk_fma_f32 v[222:223], v[222:223], v[52:53], v[226:227] op_sel:[0,1,0]
	v_cvt_pk_f32_fp8_e32 v[226:227], v216
	v_cvt_pk_f32_fp8_sdwa v[236:237], v216 src0_sel:WORD_1
	v_cvt_pk_f32_fp8_e32 v[240:241], v217
	v_cvt_pk_f32_fp8_sdwa v[216:217], v217 src0_sel:WORD_1
	v_cvt_pk_f32_fp8_e32 v[242:243], v218
	v_cvt_pk_f32_fp8_sdwa v[138:139], v218 src0_sel:WORD_1
	v_cvt_pk_f32_fp8_e32 v[140:141], v219
	v_cvt_pk_f32_fp8_sdwa v[218:219], v219 src0_sel:WORD_1
	v_pk_fma_f32 v[226:227], v[226:227], v[54:55], v[230:231] op_sel_hi:[1,0,1]
	v_pk_fma_f32 v[230:231], v[236:237], v[54:55], v[234:235] op_sel_hi:[1,0,1]
	v_pk_fma_f32 v[234:235], v[240:241], v[54:55], v[238:239] op_sel_hi:[1,0,1]
	v_pk_fma_f32 v[216:217], v[216:217], v[54:55], v[220:221] op_sel_hi:[1,0,1]
	v_pk_fma_f32 v[220:221], v[242:243], v[54:55], v[224:225] op_sel_hi:[1,0,1]
	v_pk_fma_f32 v[224:225], v[138:139], v[54:55], v[228:229] op_sel_hi:[1,0,1]
	v_pk_fma_f32 v[228:229], v[140:141], v[54:55], v[232:233] op_sel_hi:[1,0,1]
	v_pk_fma_f32 v[218:219], v[218:219], v[54:55], v[222:223] op_sel_hi:[1,0,1]
	v_cvt_pk_f32_fp8_e32 v[222:223], v212
	v_cvt_pk_f32_fp8_sdwa v[232:233], v212 src0_sel:WORD_1
	v_cvt_pk_f32_fp8_e32 v[236:237], v213
	v_cvt_pk_f32_fp8_sdwa v[212:213], v213 src0_sel:WORD_1
	v_cvt_pk_f32_fp8_e32 v[238:239], v214
	v_cvt_pk_f32_fp8_sdwa v[240:241], v214 src0_sel:WORD_1
	v_cvt_pk_f32_fp8_e32 v[242:243], v215
	v_cvt_pk_f32_fp8_sdwa v[214:215], v215 src0_sel:WORD_1
	v_mov_b32_e32 v128, v55
	v_pk_fma_f32 v[222:223], v[222:223], v[128:129], v[226:227] op_sel_hi:[1,0,1]
	v_pk_fma_f32 v[226:227], v[232:233], v[128:129], v[230:231] op_sel_hi:[1,0,1]
	v_pk_fma_f32 v[230:231], v[236:237], v[128:129], v[234:235] op_sel_hi:[1,0,1]
	v_pk_fma_f32 v[212:213], v[212:213], v[128:129], v[216:217] op_sel_hi:[1,0,1]
	v_pk_fma_f32 v[216:217], v[238:239], v[128:129], v[220:221] op_sel_hi:[1,0,1]
	v_pk_fma_f32 v[220:221], v[240:241], v[128:129], v[224:225] op_sel_hi:[1,0,1]
	v_pk_fma_f32 v[224:225], v[242:243], v[128:129], v[228:229] op_sel_hi:[1,0,1]
	v_lshl_or_b32 v32, v32, 7, v136
	global_load_dwordx4 v[240:243], v32, s[4:5]
	v_pk_fma_f32 v[214:215], v[214:215], v[128:129], v[218:219] op_sel_hi:[1,0,1]
	v_cvt_pk_f32_fp8_e32 v[218:219], v200
	v_cvt_pk_f32_fp8_sdwa v[228:229], v200 src0_sel:WORD_1
	v_cvt_pk_f32_fp8_e32 v[232:233], v201
	v_cvt_pk_f32_fp8_sdwa v[200:201], v201 src0_sel:WORD_1
	v_cvt_pk_f32_fp8_e32 v[234:235], v202
	v_cvt_pk_f32_fp8_sdwa v[236:237], v202 src0_sel:WORD_1
	v_cvt_pk_f32_fp8_e32 v[238:239], v203
	v_cvt_pk_f32_fp8_sdwa v[202:203], v203 src0_sel:WORD_1
	v_pk_fma_f32 v[218:219], v[218:219], v[56:57], v[222:223] op_sel_hi:[1,0,1]
	v_pk_fma_f32 v[222:223], v[228:229], v[56:57], v[226:227] op_sel_hi:[1,0,1]
	v_pk_fma_f32 v[226:227], v[232:233], v[56:57], v[230:231] op_sel_hi:[1,0,1]
	v_pk_fma_f32 v[200:201], v[200:201], v[56:57], v[212:213] op_sel_hi:[1,0,1]
	v_pk_fma_f32 v[212:213], v[234:235], v[56:57], v[216:217] op_sel_hi:[1,0,1]
	v_pk_fma_f32 v[216:217], v[236:237], v[56:57], v[220:221] op_sel_hi:[1,0,1]
	v_pk_fma_f32 v[220:221], v[238:239], v[56:57], v[224:225] op_sel_hi:[1,0,1]
	v_lshl_or_b32 v33, v33, 7, v136
	global_load_dwordx4 v[236:239], v33, s[4:5]
	v_pk_fma_f32 v[202:203], v[202:203], v[56:57], v[214:215] op_sel_hi:[1,0,1]
	v_cvt_pk_f32_fp8_e32 v[214:215], v196
	v_cvt_pk_f32_fp8_sdwa v[224:225], v196 src0_sel:WORD_1
	v_cvt_pk_f32_fp8_e32 v[228:229], v197
	v_cvt_pk_f32_fp8_sdwa v[196:197], v197 src0_sel:WORD_1
	v_cvt_pk_f32_fp8_e32 v[230:231], v198
	v_cvt_pk_f32_fp8_sdwa v[232:233], v198 src0_sel:WORD_1
	v_cvt_pk_f32_fp8_e32 v[234:235], v199
	v_cvt_pk_f32_fp8_sdwa v[198:199], v199 src0_sel:WORD_1
	v_pk_fma_f32 v[214:215], v[214:215], v[56:57], v[218:219] op_sel:[0,1,0]
	v_pk_fma_f32 v[218:219], v[224:225], v[56:57], v[222:223] op_sel:[0,1,0]
	v_pk_fma_f32 v[222:223], v[228:229], v[56:57], v[226:227] op_sel:[0,1,0]
	v_pk_fma_f32 v[196:197], v[196:197], v[56:57], v[200:201] op_sel:[0,1,0]
	v_pk_fma_f32 v[200:201], v[230:231], v[56:57], v[212:213] op_sel:[0,1,0]
	v_pk_fma_f32 v[212:213], v[232:233], v[56:57], v[216:217] op_sel:[0,1,0]
	v_pk_fma_f32 v[216:217], v[234:235], v[56:57], v[220:221] op_sel:[0,1,0]
	v_lshl_or_b32 v34, v34, 7, v136
	global_load_dwordx4 v[232:235], v34, s[4:5]
	v_pk_fma_f32 v[198:199], v[198:199], v[56:57], v[202:203] op_sel:[0,1,0]
	v_cvt_pk_f32_fp8_e32 v[202:203], v192
	v_cvt_pk_f32_fp8_sdwa v[220:221], v192 src0_sel:WORD_1
	v_cvt_pk_f32_fp8_e32 v[224:225], v193
	v_cvt_pk_f32_fp8_sdwa v[192:193], v193 src0_sel:WORD_1
	v_cvt_pk_f32_fp8_e32 v[226:227], v194
	v_cvt_pk_f32_fp8_sdwa v[228:229], v194 src0_sel:WORD_1
	v_cvt_pk_f32_fp8_e32 v[230:231], v195
	v_cvt_pk_f32_fp8_sdwa v[194:195], v195 src0_sel:WORD_1
	v_pk_fma_f32 v[202:203], v[202:203], v[58:59], v[214:215] op_sel_hi:[1,0,1]
	v_pk_fma_f32 v[214:215], v[220:221], v[58:59], v[218:219] op_sel_hi:[1,0,1]
	v_pk_fma_f32 v[218:219], v[224:225], v[58:59], v[222:223] op_sel_hi:[1,0,1]
	v_pk_fma_f32 v[192:193], v[192:193], v[58:59], v[196:197] op_sel_hi:[1,0,1]
	v_pk_fma_f32 v[196:197], v[226:227], v[58:59], v[200:201] op_sel_hi:[1,0,1]
	v_pk_fma_f32 v[200:201], v[228:229], v[58:59], v[212:213] op_sel_hi:[1,0,1]
	v_pk_fma_f32 v[212:213], v[230:231], v[58:59], v[216:217] op_sel_hi:[1,0,1]
	v_pk_fma_f32 v[194:195], v[194:195], v[58:59], v[198:199] op_sel_hi:[1,0,1]
	v_cvt_pk_f32_fp8_e32 v[198:199], v184
	v_cvt_pk_f32_fp8_sdwa v[216:217], v184 src0_sel:WORD_1
	v_cvt_pk_f32_fp8_e32 v[220:221], v185
	v_cvt_pk_f32_fp8_sdwa v[184:185], v185 src0_sel:WORD_1
	v_cvt_pk_f32_fp8_e32 v[222:223], v186
	v_cvt_pk_f32_fp8_sdwa v[224:225], v186 src0_sel:WORD_1
	v_cvt_pk_f32_fp8_e32 v[226:227], v187
	v_cvt_pk_f32_fp8_sdwa v[186:187], v187 src0_sel:WORD_1
	v_mov_b32_e32 v228, v59
	v_pk_fma_f32 v[198:199], v[198:199], v[228:229], v[202:203] op_sel_hi:[1,0,1]
	v_pk_fma_f32 v[202:203], v[216:217], v[228:229], v[214:215] op_sel_hi:[1,0,1]
	v_pk_fma_f32 v[214:215], v[220:221], v[228:229], v[218:219] op_sel_hi:[1,0,1]
	v_pk_fma_f32 v[184:185], v[184:185], v[228:229], v[192:193] op_sel_hi:[1,0,1]
	v_pk_fma_f32 v[192:193], v[222:223], v[228:229], v[196:197] op_sel_hi:[1,0,1]
	v_pk_fma_f32 v[196:197], v[224:225], v[228:229], v[200:201] op_sel_hi:[1,0,1]
	v_pk_fma_f32 v[200:201], v[226:227], v[228:229], v[212:213] op_sel_hi:[1,0,1]
	v_lshl_or_b32 v36, v36, 7, v136
	global_load_dwordx4 v[224:227], v36, s[4:5]
	v_pk_fma_f32 v[186:187], v[186:187], v[228:229], v[194:195] op_sel_hi:[1,0,1]
	v_lshl_or_b32 v35, v35, 7, v136
	global_load_dwordx4 v[228:231], v35, s[4:5]
	v_cvt_pk_f32_fp8_e32 v[194:195], v180
	v_cvt_pk_f32_fp8_sdwa v[212:213], v180 src0_sel:WORD_1
	v_cvt_pk_f32_fp8_e32 v[216:217], v181
	v_cvt_pk_f32_fp8_sdwa v[180:181], v181 src0_sel:WORD_1
	v_cvt_pk_f32_fp8_e32 v[218:219], v182
	v_cvt_pk_f32_fp8_sdwa v[220:221], v182 src0_sel:WORD_1
	v_cvt_pk_f32_fp8_e32 v[222:223], v183
	v_cvt_pk_f32_fp8_sdwa v[182:183], v183 src0_sel:WORD_1
	v_pk_fma_f32 v[194:195], v[194:195], v[60:61], v[198:199] op_sel_hi:[1,0,1]
	v_pk_fma_f32 v[198:199], v[212:213], v[60:61], v[202:203] op_sel_hi:[1,0,1]
	v_pk_fma_f32 v[202:203], v[216:217], v[60:61], v[214:215] op_sel_hi:[1,0,1]
	v_pk_fma_f32 v[180:181], v[180:181], v[60:61], v[184:185] op_sel_hi:[1,0,1]
	v_pk_fma_f32 v[184:185], v[218:219], v[60:61], v[192:193] op_sel_hi:[1,0,1]
	v_pk_fma_f32 v[192:193], v[220:221], v[60:61], v[196:197] op_sel_hi:[1,0,1]
	v_pk_fma_f32 v[196:197], v[222:223], v[60:61], v[200:201] op_sel_hi:[1,0,1]
	v_lshl_or_b32 v37, v37, 7, v136
	global_load_dwordx4 v[220:223], v37, s[4:5]
	v_pk_fma_f32 v[182:183], v[182:183], v[60:61], v[186:187] op_sel_hi:[1,0,1]
	v_cvt_pk_f32_fp8_e32 v[186:187], v172
	v_cvt_pk_f32_fp8_sdwa v[200:201], v172 src0_sel:WORD_1
	v_cvt_pk_f32_fp8_e32 v[212:213], v173
	v_cvt_pk_f32_fp8_sdwa v[172:173], v173 src0_sel:WORD_1
	v_cvt_pk_f32_fp8_e32 v[214:215], v174
	v_cvt_pk_f32_fp8_sdwa v[216:217], v174 src0_sel:WORD_1
	v_cvt_pk_f32_fp8_e32 v[218:219], v175
	v_cvt_pk_f32_fp8_sdwa v[174:175], v175 src0_sel:WORD_1
	v_pk_fma_f32 v[186:187], v[186:187], v[60:61], v[194:195] op_sel:[0,1,0]
	v_pk_fma_f32 v[194:195], v[200:201], v[60:61], v[198:199] op_sel:[0,1,0]
	v_pk_fma_f32 v[198:199], v[212:213], v[60:61], v[202:203] op_sel:[0,1,0]
	v_pk_fma_f32 v[172:173], v[172:173], v[60:61], v[180:181] op_sel:[0,1,0]
	v_pk_fma_f32 v[180:181], v[214:215], v[60:61], v[184:185] op_sel:[0,1,0]
	v_pk_fma_f32 v[184:185], v[216:217], v[60:61], v[192:193] op_sel:[0,1,0]
	v_pk_fma_f32 v[192:193], v[218:219], v[60:61], v[196:197] op_sel:[0,1,0]
	v_lshl_or_b32 v38, v38, 7, v136
	global_load_dwordx4 v[216:219], v38, s[4:5]
	v_pk_fma_f32 v[174:175], v[174:175], v[60:61], v[182:183] op_sel:[0,1,0]
	v_cvt_pk_f32_fp8_e32 v[182:183], v168
	v_cvt_pk_f32_fp8_sdwa v[196:197], v168 src0_sel:WORD_1
	v_cvt_pk_f32_fp8_e32 v[200:201], v169
	v_cvt_pk_f32_fp8_sdwa v[168:169], v169 src0_sel:WORD_1
	v_cvt_pk_f32_fp8_e32 v[202:203], v170
	v_cvt_pk_f32_fp8_sdwa v[212:213], v170 src0_sel:WORD_1
	v_cvt_pk_f32_fp8_e32 v[214:215], v171
	v_cvt_pk_f32_fp8_sdwa v[170:171], v171 src0_sel:WORD_1
	v_pk_fma_f32 v[182:183], v[182:183], v[62:63], v[186:187] op_sel_hi:[1,0,1]
	v_pk_fma_f32 v[186:187], v[196:197], v[62:63], v[194:195] op_sel_hi:[1,0,1]
	v_pk_fma_f32 v[194:195], v[200:201], v[62:63], v[198:199] op_sel_hi:[1,0,1]
	v_pk_fma_f32 v[168:169], v[168:169], v[62:63], v[172:173] op_sel_hi:[1,0,1]
	v_pk_fma_f32 v[172:173], v[202:203], v[62:63], v[180:181] op_sel_hi:[1,0,1]
	v_pk_fma_f32 v[180:181], v[212:213], v[62:63], v[184:185] op_sel_hi:[1,0,1]
	v_pk_fma_f32 v[184:185], v[214:215], v[62:63], v[192:193] op_sel_hi:[1,0,1]
	v_pk_fma_f32 v[170:171], v[170:171], v[62:63], v[174:175] op_sel_hi:[1,0,1]
	v_cvt_pk_f32_fp8_e32 v[174:175], v164
	v_cvt_pk_f32_fp8_sdwa v[192:193], v164 src0_sel:WORD_1
	v_cvt_pk_f32_fp8_e32 v[196:197], v165
	v_cvt_pk_f32_fp8_sdwa v[164:165], v165 src0_sel:WORD_1
	v_cvt_pk_f32_fp8_e32 v[198:199], v166
	v_cvt_pk_f32_fp8_sdwa v[200:201], v166 src0_sel:WORD_1
	v_cvt_pk_f32_fp8_e32 v[202:203], v167
	v_cvt_pk_f32_fp8_sdwa v[166:167], v167 src0_sel:WORD_1
	v_mov_b32_e32 v212, v63
	v_pk_fma_f32 v[174:175], v[174:175], v[212:213], v[182:183] op_sel_hi:[1,0,1]
	v_pk_fma_f32 v[182:183], v[192:193], v[212:213], v[186:187] op_sel_hi:[1,0,1]
	v_pk_fma_f32 v[186:187], v[196:197], v[212:213], v[194:195] op_sel_hi:[1,0,1]
	v_lshl_or_b32 v42, v42, 7, v136
	global_load_dwordx4 v[192:195], v42, s[4:5]
	v_pk_fma_f32 v[164:165], v[164:165], v[212:213], v[168:169] op_sel_hi:[1,0,1]
	v_pk_fma_f32 v[168:169], v[198:199], v[212:213], v[172:173] op_sel_hi:[1,0,1]
	v_lshl_or_b32 v41, v41, 7, v136
	global_load_dwordx4 v[196:199], v41, s[4:5]
	v_pk_fma_f32 v[172:173], v[200:201], v[212:213], v[180:181] op_sel_hi:[1,0,1]
	v_pk_fma_f32 v[180:181], v[202:203], v[212:213], v[184:185] op_sel_hi:[1,0,1]
	v_lshl_or_b32 v40, v40, 7, v136
	global_load_dwordx4 v[200:203], v40, s[4:5]
	v_pk_fma_f32 v[166:167], v[166:167], v[212:213], v[170:171] op_sel_hi:[1,0,1]
	v_lshl_or_b32 v39, v39, 7, v136
	global_load_dwordx4 v[212:215], v39, s[4:5]
	v_permlane32_swap_b32_e32 v174, v168
	v_permlane32_swap_b32_e32 v175, v169
	v_permlane32_swap_b32_e32 v182, v172
	v_permlane32_swap_b32_e32 v183, v173
	v_permlane32_swap_b32_e32 v186, v180
	v_permlane32_swap_b32_e32 v187, v181
	v_permlane32_swap_b32_e32 v164, v166
	v_permlane32_swap_b32_e32 v165, v167
	v_add_f32_e32 v168, v174, v168
	v_add_f32_e32 v169, v175, v169
	v_add_f32_e32 v170, v182, v172
	v_add_f32_e32 v171, v183, v173
	v_add_f32_e32 v172, v186, v180
	v_add_f32_e32 v173, v187, v181
	v_lshl_or_b32 v43, v43, 7, v136
	global_load_dwordx4 v[184:187], v43, s[4:5]
	v_lshl_or_b32 v44, v44, 7, v136
	global_load_dwordx4 v[180:183], v44, s[4:5]
	v_add_f32_e32 v164, v164, v166
	v_add_f32_e32 v165, v165, v167
	v_permlane16_swap_b32_e32 v168, v172
	v_permlane16_swap_b32_e32 v169, v173
	v_permlane16_swap_b32_e32 v170, v164
	v_permlane16_swap_b32_e32 v171, v165
	v_pk_add_f32 v[166:167], v[168:169], v[172:173]
	v_lshl_or_b32 v45, v45, 7, v136
	global_load_dwordx4 v[172:175], v45, s[4:5]
	v_pk_add_f32 v[164:165], v[170:171], v[164:165]
	s_ashr_i32 s7, s6, 31
	v_cndmask_b32_e64 v168, v166, v164, s[0:1]
	v_cndmask_b32_e64 v170, v164, v166, s[0:1]
	v_cndmask_b32_e64 v164, v167, v165, s[0:1]
	v_mov_b32_dpp v168, v168 row_ror:8 row_mask:0xf bank_mask:0xf bound_ctrl:1
	v_cndmask_b32_e64 v171, v165, v167, s[0:1]
	v_mov_b32_dpp v169, v164 row_ror:8 row_mask:0xf bank_mask:0xf bound_ctrl:1
	v_pk_add_f32 v[166:167], v[170:171], v[168:169]
	s_lshl_b64 s[8:9], s[6:7], 11
	v_pk_mul_f32 v[164:165], v[166:167], v[166:167]
	v_cvt_pk_bf16_f32 v168, v166, v167
	v_add_f32_e32 v164, v164, v165
	v_lshl_add_u64 v[166:167], v[130:131], 0, s[8:9]
	global_store_dword v[166:167], v168, off
	v_add_f32_dpp v164, v164, v164 quad_perm:[1,0,3,2] row_mask:0xf bank_mask:0xf bound_ctrl:1
	s_nop 1
	v_add_f32_dpp v164, v164, v164 quad_perm:[2,3,0,1] row_mask:0xf bank_mask:0xf bound_ctrl:1
	s_nop 1
	v_add_f32_dpp v164, v164, v164 row_half_mirror row_mask:0xf bank_mask:0xf bound_ctrl:1
	s_nop 1
	v_add_f32_dpp v164, v164, v164 row_ror:8 row_mask:0xf bank_mask:0xf bound_ctrl:1
	v_mov_b32_e32 v165, v164
	s_nop 1
	v_permlane16_swap_b32_e32 v164, v165
	v_add_f32_e32 v164, v164, v165
	v_mov_b32_e32 v165, v164
	s_nop 1
	v_permlane32_swap_b32_e32 v164, v165
	s_and_saveexec_b64 s[8:9], s[2:3]
	s_lshl_b64 s[10:11], s[6:7], 2
	s_add_u32 s10, s12, s10
	v_add_f32_e32 v164, v164, v165
	s_addc_u32 s11, s13, s11
	global_store_dword v129, v164, s[10:11]
	s_or_b64 exec, exec, s[8:9]
	v_lshl_or_b32 v46, v46, 7, v136
	global_load_dwordx4 v[168:171], v46, s[4:5]
	v_lshl_or_b32 v47, v47, 7, v136
	global_load_dwordx4 v[164:167], v47, s[4:5]
	s_add_u32 s22, s20, 0x300
	s_lshl_b32 s22, s22, 9
	v_lshl_add_u64 v[48:49], v[134:135], 0, s[22:23]
	global_load_dwordx4 v[60:63], v[48:49], off offset:48
	global_load_dwordx4 v[56:59], v[48:49], off offset:32
	global_load_dwordx4 v[52:55], v[48:49], off offset:16
	s_nop 0
	global_load_dwordx4 v[48:51], v[48:49], off
	s_add_u32 s22, s20, 0x500
	s_lshl_b32 s22, s22, 9
	v_lshl_add_u64 v[32:33], v[132:133], 0, s[22:23]
	global_load_dwordx4 v[44:47], v[32:33], off offset:48
	global_load_dwordx4 v[40:43], v[32:33], off offset:32
	global_load_dwordx4 v[36:39], v[32:33], off offset:16
	s_nop 0
	global_load_dwordx4 v[32:35], v[32:33], off
	s_add_u32 s20, s20, 0x200
	s_mov_b32 s24, 61
.Lpu2_loop:
	s_mov_b32 s8, s20
	s_waitcnt vmcnt(26)
	v_cvt_pk_f32_fp8_e32 v[138:139], v124
	v_cvt_pk_f32_fp8_sdwa v[140:141], v124 src0_sel:WORD_1
	v_cvt_pk_f32_fp8_e32 v[142:143], v125
	v_cvt_pk_f32_fp8_sdwa v[124:125], v125 src0_sel:WORD_1
	v_cvt_pk_f32_fp8_e32 v[144:145], v126
	v_cvt_pk_f32_fp8_sdwa v[146:147], v126 src0_sel:WORD_1
	v_cvt_pk_f32_fp8_e32 v[148:149], v127
	v_cvt_pk_f32_fp8_sdwa v[126:127], v127 src0_sel:WORD_1
	v_cvt_pk_f32_fp8_e32 v[150:151], v120
	v_cvt_pk_f32_fp8_sdwa v[152:153], v120 src0_sel:WORD_1
	v_cvt_pk_f32_fp8_e32 v[154:155], v121
	v_cvt_pk_f32_fp8_sdwa v[120:121], v121 src0_sel:WORD_1
	v_cvt_pk_f32_fp8_e32 v[156:157], v122
	v_cvt_pk_f32_fp8_sdwa v[158:159], v122 src0_sel:WORD_1
	v_cvt_pk_f32_fp8_e32 v[160:161], v123
	v_cvt_pk_f32_fp8_sdwa v[122:123], v123 src0_sel:WORD_1
	v_pk_fma_f32 v[138:139], v[138:139], v[28:29], 0 op_sel_hi:[1,0,0]
	v_pk_fma_f32 v[140:141], v[140:141], v[28:29], 0 op_sel_hi:[1,0,0]
	v_pk_fma_f32 v[142:143], v[142:143], v[28:29], 0 op_sel_hi:[1,0,0]
	v_pk_fma_f32 v[124:125], v[124:125], v[28:29], 0 op_sel_hi:[1,0,0]
	v_pk_fma_f32 v[144:145], v[144:145], v[28:29], 0 op_sel_hi:[1,0,0]
	v_pk_fma_f32 v[146:147], v[146:147], v[28:29], 0 op_sel_hi:[1,0,0]
	v_pk_fma_f32 v[148:149], v[148:149], v[28:29], 0 op_sel_hi:[1,0,0]
	v_pk_fma_f32 v[126:127], v[126:127], v[28:29], 0 op_sel_hi:[1,0,0]
	v_pk_fma_f32 v[138:139], v[150:151], v[28:29], v[138:139] op_sel:[0,1,0]
	v_pk_fma_f32 v[140:141], v[152:153], v[28:29], v[140:141] op_sel:[0,1,0]
	v_pk_fma_f32 v[142:143], v[154:155], v[28:29], v[142:143] op_sel:[0,1,0]
	v_pk_fma_f32 v[120:121], v[120:121], v[28:29], v[124:125] op_sel:[0,1,0]
	v_pk_fma_f32 v[124:125], v[156:157], v[28:29], v[144:145] op_sel:[0,1,0]
	v_pk_fma_f32 v[144:145], v[158:159], v[28:29], v[146:147] op_sel:[0,1,0]
	v_pk_fma_f32 v[146:147], v[160:161], v[28:29], v[148:149] op_sel:[0,1,0]
	v_pk_fma_f32 v[122:123], v[122:123], v[28:29], v[126:127] op_sel:[0,1,0]
	v_cvt_pk_f32_fp8_e32 v[126:127], v116
	v_cvt_pk_f32_fp8_sdwa v[148:149], v116 src0_sel:WORD_1
	v_cvt_pk_f32_fp8_e32 v[150:151], v117
	v_cvt_pk_f32_fp8_sdwa v[116:117], v117 src0_sel:WORD_1
	v_cvt_pk_f32_fp8_e32 v[152:153], v118
	v_cvt_pk_f32_fp8_sdwa v[154:155], v118 src0_sel:WORD_1
	v_cvt_pk_f32_fp8_e32 v[156:157], v119
	v_cvt_pk_f32_fp8_sdwa v[118:119], v119 src0_sel:WORD_1
	v_pk_fma_f32 v[126:127], v[126:127], v[30:31], v[138:139] op_sel_hi:[1,0,1]
	v_pk_fma_f32 v[138:139], v[148:149], v[30:31], v[140:141] op_sel_hi:[1,0,1]
	v_pk_fma_f32 v[140:141], v[150:151], v[30:31], v[142:143] op_sel_hi:[1,0,1]
	v_pk_fma_f32 v[116:117], v[116:117], v[30:31], v[120:121] op_sel_hi:[1,0,1]
	v_pk_fma_f32 v[120:121], v[152:153], v[30:31], v[124:125] op_sel_hi:[1,0,1]
	v_pk_fma_f32 v[124:125], v[154:155], v[30:31], v[144:145] op_sel_hi:[1,0,1]
	v_pk_fma_f32 v[142:143], v[156:157], v[30:31], v[146:147] op_sel_hi:[1,0,1]
	v_pk_fma_f32 v[118:119], v[118:119], v[30:31], v[122:123] op_sel_hi:[1,0,1]
	v_cvt_pk_f32_fp8_e32 v[122:123], v112
	v_cvt_pk_f32_fp8_sdwa v[144:145], v112 src0_sel:WORD_1
	v_cvt_pk_f32_fp8_e32 v[146:147], v113
	v_cvt_pk_f32_fp8_sdwa v[112:113], v113 src0_sel:WORD_1
	v_cvt_pk_f32_fp8_e32 v[148:149], v114
	v_cvt_pk_f32_fp8_sdwa v[150:151], v114 src0_sel:WORD_1
	v_cvt_pk_f32_fp8_e32 v[152:153], v115
	v_cvt_pk_f32_fp8_sdwa v[114:115], v115 src0_sel:WORD_1
	v_mov_b32_e32 v128, v31
	v_pk_fma_f32 v[122:123], v[122:123], v[128:129], v[126:127] op_sel_hi:[1,0,1]
	v_pk_fma_f32 v[126:127], v[144:145], v[128:129], v[138:139] op_sel_hi:[1,0,1]
	v_pk_fma_f32 v[138:139], v[146:147], v[128:129], v[140:141] op_sel_hi:[1,0,1]
	v_pk_fma_f32 v[112:113], v[112:113], v[128:129], v[116:117] op_sel_hi:[1,0,1]
	v_pk_fma_f32 v[116:117], v[148:149], v[128:129], v[120:121] op_sel_hi:[1,0,1]
	v_pk_fma_f32 v[120:121], v[150:151], v[128:129], v[124:125] op_sel_hi:[1,0,1]
	v_pk_fma_f32 v[124:125], v[152:153], v[128:129], v[142:143] op_sel_hi:[1,0,1]
	v_pk_fma_f32 v[114:115], v[114:115], v[128:129], v[118:119] op_sel_hi:[1,0,1]
	v_cvt_pk_f32_fp8_e32 v[118:119], v108
	v_cvt_pk_f32_fp8_sdwa v[140:141], v108 src0_sel:WORD_1
	v_cvt_pk_f32_fp8_e32 v[142:143], v109
	v_cvt_pk_f32_fp8_sdwa v[108:109], v109 src0_sel:WORD_1
	v_cvt_pk_f32_fp8_e32 v[144:145], v110
	v_cvt_pk_f32_fp8_sdwa v[146:147], v110 src0_sel:WORD_1
	v_cvt_pk_f32_fp8_e32 v[148:149], v111
	v_cvt_pk_f32_fp8_sdwa v[110:111], v111 src0_sel:WORD_1
	v_pk_fma_f32 v[118:119], v[118:119], v[24:25], v[122:123] op_sel_hi:[1,0,1]
	v_pk_fma_f32 v[122:123], v[140:141], v[24:25], v[126:127] op_sel_hi:[1,0,1]
	v_pk_fma_f32 v[126:127], v[142:143], v[24:25], v[138:139] op_sel_hi:[1,0,1]
	v_pk_fma_f32 v[108:109], v[108:109], v[24:25], v[112:113] op_sel_hi:[1,0,1]
	v_pk_fma_f32 v[112:113], v[144:145], v[24:25], v[116:117] op_sel_hi:[1,0,1]
	v_pk_fma_f32 v[116:117], v[146:147], v[24:25], v[120:121] op_sel_hi:[1,0,1]
	v_pk_fma_f32 v[120:121], v[148:149], v[24:25], v[124:125] op_sel_hi:[1,0,1]
	v_pk_fma_f32 v[110:111], v[110:111], v[24:25], v[114:115] op_sel_hi:[1,0,1]
	v_cvt_pk_f32_fp8_e32 v[114:115], v104
	v_cvt_pk_f32_fp8_sdwa v[124:125], v104 src0_sel:WORD_1
	v_cvt_pk_f32_fp8_e32 v[138:139], v105
	v_cvt_pk_f32_fp8_sdwa v[104:105], v105 src0_sel:WORD_1
	v_cvt_pk_f32_fp8_e32 v[140:141], v106
	v_cvt_pk_f32_fp8_sdwa v[142:143], v106 src0_sel:WORD_1
	v_cvt_pk_f32_fp8_e32 v[144:145], v107
	v_cvt_pk_f32_fp8_sdwa v[106:107], v107 src0_sel:WORD_1
	v_pk_fma_f32 v[114:115], v[114:115], v[24:25], v[118:119] op_sel:[0,1,0]
	v_pk_fma_f32 v[118:119], v[124:125], v[24:25], v[122:123] op_sel:[0,1,0]
	v_pk_fma_f32 v[122:123], v[138:139], v[24:25], v[126:127] op_sel:[0,1,0]
	v_pk_fma_f32 v[104:105], v[104:105], v[24:25], v[108:109] op_sel:[0,1,0]
	v_pk_fma_f32 v[108:109], v[140:141], v[24:25], v[112:113] op_sel:[0,1,0]
	v_pk_fma_f32 v[112:113], v[142:143], v[24:25], v[116:117] op_sel:[0,1,0]
	v_pk_fma_f32 v[116:117], v[144:145], v[24:25], v[120:121] op_sel:[0,1,0]
	v_pk_fma_f32 v[106:107], v[106:107], v[24:25], v[110:111] op_sel:[0,1,0]
	v_cvt_pk_f32_fp8_e32 v[110:111], v100
	v_cvt_pk_f32_fp8_sdwa v[120:121], v100 src0_sel:WORD_1
	v_cvt_pk_f32_fp8_e32 v[124:125], v101
	v_cvt_pk_f32_fp8_sdwa v[100:101], v101 src0_sel:WORD_1
	v_cvt_pk_f32_fp8_e32 v[126:127], v102
	v_cvt_pk_f32_fp8_sdwa v[138:139], v102 src0_sel:WORD_1
	v_cvt_pk_f32_fp8_e32 v[140:141], v103
	v_cvt_pk_f32_fp8_sdwa v[102:103], v103 src0_sel:WORD_1
	v_pk_fma_f32 v[110:111], v[110:111], v[26:27], v[114:115] op_sel_hi:[1,0,1]
	v_pk_fma_f32 v[114:115], v[120:121], v[26:27], v[118:119] op_sel_hi:[1,0,1]
	v_pk_fma_f32 v[118:119], v[124:125], v[26:27], v[122:123] op_sel_hi:[1,0,1]
	v_pk_fma_f32 v[100:101], v[100:101], v[26:27], v[104:105] op_sel_hi:[1,0,1]
	v_pk_fma_f32 v[104:105], v[126:127], v[26:27], v[108:109] op_sel_hi:[1,0,1]
	v_pk_fma_f32 v[108:109], v[138:139], v[26:27], v[112:113] op_sel_hi:[1,0,1]
	v_pk_fma_f32 v[112:113], v[140:141], v[26:27], v[116:117] op_sel_hi:[1,0,1]
	v_pk_fma_f32 v[102:103], v[102:103], v[26:27], v[106:107] op_sel_hi:[1,0,1]
	v_cvt_pk_f32_fp8_e32 v[106:107], v96
	v_cvt_pk_f32_fp8_sdwa v[116:117], v96 src0_sel:WORD_1
	v_cvt_pk_f32_fp8_e32 v[120:121], v97
	v_cvt_pk_f32_fp8_sdwa v[96:97], v97 src0_sel:WORD_1
	v_cvt_pk_f32_fp8_e32 v[122:123], v98
	v_cvt_pk_f32_fp8_sdwa v[124:125], v98 src0_sel:WORD_1
	v_cvt_pk_f32_fp8_e32 v[126:127], v99
	v_cvt_pk_f32_fp8_sdwa v[98:99], v99 src0_sel:WORD_1
	v_mov_b32_e32 v128, v27
	v_pk_fma_f32 v[106:107], v[106:107], v[128:129], v[110:111] op_sel_hi:[1,0,1]
	v_pk_fma_f32 v[110:111], v[116:117], v[128:129], v[114:115] op_sel_hi:[1,0,1]
	v_pk_fma_f32 v[114:115], v[120:121], v[128:129], v[118:119] op_sel_hi:[1,0,1]
	v_pk_fma_f32 v[96:97], v[96:97], v[128:129], v[100:101] op_sel_hi:[1,0,1]
	v_pk_fma_f32 v[100:101], v[122:123], v[128:129], v[104:105] op_sel_hi:[1,0,1]
	v_pk_fma_f32 v[104:105], v[124:125], v[128:129], v[108:109] op_sel_hi:[1,0,1]
	v_pk_fma_f32 v[108:109], v[126:127], v[128:129], v[112:113] op_sel_hi:[1,0,1]
	v_lshl_or_b32 v12, v12, 7, v136
	global_load_dwordx4 v[124:127], v12, s[4:5]
	v_pk_fma_f32 v[98:99], v[98:99], v[128:129], v[102:103] op_sel_hi:[1,0,1]
	v_cvt_pk_f32_fp8_e32 v[102:103], v92
	v_cvt_pk_f32_fp8_sdwa v[112:113], v92 src0_sel:WORD_1
	v_cvt_pk_f32_fp8_e32 v[116:117], v93
	v_cvt_pk_f32_fp8_sdwa v[92:93], v93 src0_sel:WORD_1
	v_cvt_pk_f32_fp8_e32 v[118:119], v94
	v_cvt_pk_f32_fp8_sdwa v[120:121], v94 src0_sel:WORD_1
	v_cvt_pk_f32_fp8_e32 v[122:123], v95
	v_cvt_pk_f32_fp8_sdwa v[94:95], v95 src0_sel:WORD_1
	v_pk_fma_f32 v[102:103], v[102:103], v[20:21], v[106:107] op_sel_hi:[1,0,1]
	v_pk_fma_f32 v[106:107], v[112:113], v[20:21], v[110:111] op_sel_hi:[1,0,1]
	v_pk_fma_f32 v[110:111], v[116:117], v[20:21], v[114:115] op_sel_hi:[1,0,1]
	v_pk_fma_f32 v[92:93], v[92:93], v[20:21], v[96:97] op_sel_hi:[1,0,1]
	v_pk_fma_f32 v[96:97], v[118:119], v[20:21], v[100:101] op_sel_hi:[1,0,1]
	v_pk_fma_f32 v[100:101], v[120:121], v[20:21], v[104:105] op_sel_hi:[1,0,1]
	v_pk_fma_f32 v[104:105], v[122:123], v[20:21], v[108:109] op_sel_hi:[1,0,1]
	v_lshl_or_b32 v13, v13, 7, v136
	global_load_dwordx4 v[120:123], v13, s[4:5]
	v_pk_fma_f32 v[94:95], v[94:95], v[20:21], v[98:99] op_sel_hi:[1,0,1]
	v_cvt_pk_f32_fp8_e32 v[98:99], v88
	v_cvt_pk_f32_fp8_sdwa v[108:109], v88 src0_sel:WORD_1
	v_cvt_pk_f32_fp8_e32 v[112:113], v89
	v_cvt_pk_f32_fp8_sdwa v[88:89], v89 src0_sel:WORD_1
	v_cvt_pk_f32_fp8_e32 v[114:115], v90
	v_cvt_pk_f32_fp8_sdwa v[116:117], v90 src0_sel:WORD_1
	v_cvt_pk_f32_fp8_e32 v[118:119], v91
	v_cvt_pk_f32_fp8_sdwa v[90:91], v91 src0_sel:WORD_1
	v_pk_fma_f32 v[98:99], v[98:99], v[20:21], v[102:103] op_sel:[0,1,0]
	v_pk_fma_f32 v[102:103], v[108:109], v[20:21], v[106:107] op_sel:[0,1,0]
	v_pk_fma_f32 v[106:107], v[112:113], v[20:21], v[110:111] op_sel:[0,1,0]
	v_pk_fma_f32 v[88:89], v[88:89], v[20:21], v[92:93] op_sel:[0,1,0]
	v_pk_fma_f32 v[92:93], v[114:115], v[20:21], v[96:97] op_sel:[0,1,0]
	v_pk_fma_f32 v[96:97], v[116:117], v[20:21], v[100:101] op_sel:[0,1,0]
	v_pk_fma_f32 v[100:101], v[118:119], v[20:21], v[104:105] op_sel:[0,1,0]
	v_lshl_or_b32 v14, v14, 7, v136
	global_load_dwordx4 v[116:119], v14, s[4:5]
	v_pk_fma_f32 v[90:91], v[90:91], v[20:21], v[94:95] op_sel:[0,1,0]
	v_cvt_pk_f32_fp8_e32 v[94:95], v84
	v_cvt_pk_f32_fp8_sdwa v[104:105], v84 src0_sel:WORD_1
	v_cvt_pk_f32_fp8_e32 v[108:109], v85
	v_cvt_pk_f32_fp8_sdwa v[84:85], v85 src0_sel:WORD_1
	v_cvt_pk_f32_fp8_e32 v[110:111], v86
	v_cvt_pk_f32_fp8_sdwa v[112:113], v86 src0_sel:WORD_1
	v_cvt_pk_f32_fp8_e32 v[114:115], v87
	v_cvt_pk_f32_fp8_sdwa v[86:87], v87 src0_sel:WORD_1
	v_pk_fma_f32 v[94:95], v[94:95], v[22:23], v[98:99] op_sel_hi:[1,0,1]
	v_pk_fma_f32 v[98:99], v[104:105], v[22:23], v[102:103] op_sel_hi:[1,0,1]
	v_pk_fma_f32 v[102:103], v[108:109], v[22:23], v[106:107] op_sel_hi:[1,0,1]
	v_pk_fma_f32 v[84:85], v[84:85], v[22:23], v[88:89] op_sel_hi:[1,0,1]
	v_pk_fma_f32 v[88:89], v[110:111], v[22:23], v[92:93] op_sel_hi:[1,0,1]
	v_pk_fma_f32 v[92:93], v[112:113], v[22:23], v[96:97] op_sel_hi:[1,0,1]
	v_pk_fma_f32 v[96:97], v[114:115], v[22:23], v[100:101] op_sel_hi:[1,0,1]
	v_pk_fma_f32 v[86:87], v[86:87], v[22:23], v[90:91] op_sel_hi:[1,0,1]
	v_cvt_pk_f32_fp8_e32 v[90:91], v80
	v_cvt_pk_f32_fp8_sdwa v[100:101], v80 src0_sel:WORD_1
	v_cvt_pk_f32_fp8_e32 v[104:105], v81
	v_cvt_pk_f32_fp8_sdwa v[80:81], v81 src0_sel:WORD_1
	v_cvt_pk_f32_fp8_e32 v[106:107], v82
	v_cvt_pk_f32_fp8_sdwa v[108:109], v82 src0_sel:WORD_1
	v_cvt_pk_f32_fp8_e32 v[110:111], v83
	v_cvt_pk_f32_fp8_sdwa v[82:83], v83 src0_sel:WORD_1
	v_mov_b32_e32 v112, v23
	v_pk_fma_f32 v[90:91], v[90:91], v[112:113], v[94:95] op_sel_hi:[1,0,1]
	v_pk_fma_f32 v[94:95], v[100:101], v[112:113], v[98:99] op_sel_hi:[1,0,1]
	v_pk_fma_f32 v[98:99], v[104:105], v[112:113], v[102:103] op_sel_hi:[1,0,1]
	v_pk_fma_f32 v[80:81], v[80:81], v[112:113], v[84:85] op_sel_hi:[1,0,1]
	v_pk_fma_f32 v[84:85], v[106:107], v[112:113], v[88:89] op_sel_hi:[1,0,1]
	v_pk_fma_f32 v[88:89], v[108:109], v[112:113], v[92:93] op_sel_hi:[1,0,1]
	v_pk_fma_f32 v[92:93], v[110:111], v[112:113], v[96:97] op_sel_hi:[1,0,1]
	v_lshl_or_b32 v8, v8, 7, v136
	global_load_dwordx4 v[108:111], v8, s[4:5]
	v_pk_fma_f32 v[82:83], v[82:83], v[112:113], v[86:87] op_sel_hi:[1,0,1]
	v_lshl_or_b32 v15, v15, 7, v136
	global_load_dwordx4 v[112:115], v15, s[4:5]
	v_cvt_pk_f32_fp8_e32 v[86:87], v76
	v_cvt_pk_f32_fp8_sdwa v[96:97], v76 src0_sel:WORD_1
	v_cvt_pk_f32_fp8_e32 v[100:101], v77
	v_cvt_pk_f32_fp8_sdwa v[76:77], v77 src0_sel:WORD_1
	v_cvt_pk_f32_fp8_e32 v[102:103], v78
	v_cvt_pk_f32_fp8_sdwa v[104:105], v78 src0_sel:WORD_1
	v_cvt_pk_f32_fp8_e32 v[106:107], v79
	v_cvt_pk_f32_fp8_sdwa v[78:79], v79 src0_sel:WORD_1
	v_pk_fma_f32 v[86:87], v[86:87], v[16:17], v[90:91] op_sel_hi:[1,0,1]
	v_pk_fma_f32 v[90:91], v[96:97], v[16:17], v[94:95] op_sel_hi:[1,0,1]
	v_pk_fma_f32 v[94:95], v[100:101], v[16:17], v[98:99] op_sel_hi:[1,0,1]
	v_pk_fma_f32 v[76:77], v[76:77], v[16:17], v[80:81] op_sel_hi:[1,0,1]
	v_pk_fma_f32 v[80:81], v[102:103], v[16:17], v[84:85] op_sel_hi:[1,0,1]
	v_pk_fma_f32 v[84:85], v[104:105], v[16:17], v[88:89] op_sel_hi:[1,0,1]
	v_pk_fma_f32 v[88:89], v[106:107], v[16:17], v[92:93] op_sel_hi:[1,0,1]
	v_lshl_or_b32 v9, v9, 7, v136
	global_load_dwordx4 v[104:107], v9, s[4:5]
	v_pk_fma_f32 v[78:79], v[78:79], v[16:17], v[82:83] op_sel_hi:[1,0,1]
	v_cvt_pk_f32_fp8_e32 v[82:83], v72
	v_cvt_pk_f32_fp8_sdwa v[92:93], v72 src0_sel:WORD_1
	v_cvt_pk_f32_fp8_e32 v[96:97], v73
	v_cvt_pk_f32_fp8_sdwa v[72:73], v73 src0_sel:WORD_1
	v_cvt_pk_f32_fp8_e32 v[98:99], v74
	v_cvt_pk_f32_fp8_sdwa v[100:101], v74 src0_sel:WORD_1
	v_cvt_pk_f32_fp8_e32 v[102:103], v75
	v_cvt_pk_f32_fp8_sdwa v[74:75], v75 src0_sel:WORD_1
	v_pk_fma_f32 v[82:83], v[82:83], v[16:17], v[86:87] op_sel:[0,1,0]
	v_pk_fma_f32 v[86:87], v[92:93], v[16:17], v[90:91] op_sel:[0,1,0]
	v_pk_fma_f32 v[90:91], v[96:97], v[16:17], v[94:95] op_sel:[0,1,0]
	v_pk_fma_f32 v[72:73], v[72:73], v[16:17], v[76:77] op_sel:[0,1,0]
	v_pk_fma_f32 v[76:77], v[98:99], v[16:17], v[80:81] op_sel:[0,1,0]
	v_pk_fma_f32 v[80:81], v[100:101], v[16:17], v[84:85] op_sel:[0,1,0]
	v_pk_fma_f32 v[84:85], v[102:103], v[16:17], v[88:89] op_sel:[0,1,0]
	v_lshl_or_b32 v10, v10, 7, v136
	global_load_dwordx4 v[100:103], v10, s[4:5]
	v_pk_fma_f32 v[74:75], v[74:75], v[16:17], v[78:79] op_sel:[0,1,0]
	v_cvt_pk_f32_fp8_e32 v[78:79], v68
	v_cvt_pk_f32_fp8_sdwa v[88:89], v68 src0_sel:WORD_1
	v_cvt_pk_f32_fp8_e32 v[92:93], v69
	v_cvt_pk_f32_fp8_sdwa v[68:69], v69 src0_sel:WORD_1
	v_cvt_pk_f32_fp8_e32 v[94:95], v70
	v_cvt_pk_f32_fp8_sdwa v[96:97], v70 src0_sel:WORD_1
	v_cvt_pk_f32_fp8_e32 v[98:99], v71
	v_cvt_pk_f32_fp8_sdwa v[70:71], v71 src0_sel:WORD_1
	v_pk_fma_f32 v[78:79], v[78:79], v[18:19], v[82:83] op_sel_hi:[1,0,1]
	v_pk_fma_f32 v[82:83], v[88:89], v[18:19], v[86:87] op_sel_hi:[1,0,1]
	v_pk_fma_f32 v[86:87], v[92:93], v[18:19], v[90:91] op_sel_hi:[1,0,1]
	v_pk_fma_f32 v[68:69], v[68:69], v[18:19], v[72:73] op_sel_hi:[1,0,1]
	v_pk_fma_f32 v[72:73], v[94:95], v[18:19], v[76:77] op_sel_hi:[1,0,1]
	v_pk_fma_f32 v[76:77], v[96:97], v[18:19], v[80:81] op_sel_hi:[1,0,1]
	v_pk_fma_f32 v[80:81], v[98:99], v[18:19], v[84:85] op_sel_hi:[1,0,1]
	v_pk_fma_f32 v[70:71], v[70:71], v[18:19], v[74:75] op_sel_hi:[1,0,1]
	v_cvt_pk_f32_fp8_e32 v[74:75], v64
	v_cvt_pk_f32_fp8_sdwa v[84:85], v64 src0_sel:WORD_1
	v_cvt_pk_f32_fp8_e32 v[88:89], v65
	v_cvt_pk_f32_fp8_sdwa v[64:65], v65 src0_sel:WORD_1
	v_cvt_pk_f32_fp8_e32 v[90:91], v66
	v_cvt_pk_f32_fp8_sdwa v[92:93], v66 src0_sel:WORD_1
	v_cvt_pk_f32_fp8_e32 v[94:95], v67
	v_cvt_pk_f32_fp8_sdwa v[66:67], v67 src0_sel:WORD_1
	v_mov_b32_e32 v96, v19
	v_pk_fma_f32 v[74:75], v[74:75], v[96:97], v[78:79] op_sel_hi:[1,0,1]
	v_pk_fma_f32 v[78:79], v[84:85], v[96:97], v[82:83] op_sel_hi:[1,0,1]
	v_pk_fma_f32 v[82:83], v[88:89], v[96:97], v[86:87] op_sel_hi:[1,0,1]
	v_lshl_or_b32 v6, v6, 7, v136
	global_load_dwordx4 v[84:87], v6, s[4:5]
	v_pk_fma_f32 v[64:65], v[64:65], v[96:97], v[68:69] op_sel_hi:[1,0,1]
	v_pk_fma_f32 v[68:69], v[90:91], v[96:97], v[72:73] op_sel_hi:[1,0,1]
	v_lshl_or_b32 v5, v5, 7, v136
	global_load_dwordx4 v[88:91], v5, s[4:5]
	v_pk_fma_f32 v[72:73], v[92:93], v[96:97], v[76:77] op_sel_hi:[1,0,1]
	v_pk_fma_f32 v[76:77], v[94:95], v[96:97], v[80:81] op_sel_hi:[1,0,1]
	v_lshl_or_b32 v4, v4, 7, v136
	global_load_dwordx4 v[92:95], v4, s[4:5]
	v_pk_fma_f32 v[66:67], v[66:67], v[96:97], v[70:71] op_sel_hi:[1,0,1]
	v_lshl_or_b32 v11, v11, 7, v136
	global_load_dwordx4 v[96:99], v11, s[4:5]
	v_permlane32_swap_b32_e32 v74, v68
	v_permlane32_swap_b32_e32 v75, v69
	v_permlane32_swap_b32_e32 v78, v72
	v_permlane32_swap_b32_e32 v79, v73
	v_permlane32_swap_b32_e32 v82, v76
	v_permlane32_swap_b32_e32 v83, v77
	v_permlane32_swap_b32_e32 v64, v66
	v_permlane32_swap_b32_e32 v65, v67
	v_add_f32_e32 v68, v74, v68
	v_add_f32_e32 v69, v75, v69
	v_add_f32_e32 v70, v78, v72
	v_add_f32_e32 v71, v79, v73
	v_add_f32_e32 v72, v82, v76
	v_add_f32_e32 v73, v83, v77
	v_lshl_or_b32 v7, v7, 7, v136
	global_load_dwordx4 v[80:83], v7, s[4:5]
	v_lshl_or_b32 v0, v0, 7, v136
	global_load_dwordx4 v[76:79], v0, s[4:5]
	v_add_f32_e32 v64, v64, v66
	v_add_f32_e32 v65, v65, v67
	v_permlane16_swap_b32_e32 v68, v72
	v_permlane16_swap_b32_e32 v69, v73
	v_permlane16_swap_b32_e32 v70, v64
	v_permlane16_swap_b32_e32 v71, v65
	v_pk_add_f32 v[66:67], v[68:69], v[72:73]
	v_lshl_or_b32 v1, v1, 7, v136
	global_load_dwordx4 v[72:75], v1, s[4:5]
	v_pk_add_f32 v[64:65], v[70:71], v[64:65]
	s_ashr_i32 s9, s8, 31
	v_cndmask_b32_e64 v68, v66, v64, s[0:1]
	v_cndmask_b32_e64 v70, v64, v66, s[0:1]
	v_cndmask_b32_e64 v64, v67, v65, s[0:1]
	v_mov_b32_dpp v68, v68 row_ror:8 row_mask:0xf bank_mask:0xf bound_ctrl:1
	v_cndmask_b32_e64 v71, v65, v67, s[0:1]
	v_mov_b32_dpp v69, v64 row_ror:8 row_mask:0xf bank_mask:0xf bound_ctrl:1
	v_pk_add_f32 v[66:67], v[70:71], v[68:69]
	s_lshl_b64 s[10:11], s[8:9], 11
	v_pk_mul_f32 v[64:65], v[66:67], v[66:67]
	v_cvt_pk_bf16_f32 v68, v66, v67
	v_add_f32_e32 v64, v64, v65
	v_lshl_add_u64 v[66:67], v[130:131], 0, s[10:11]
	global_store_dword v[66:67], v68, off
	v_add_f32_dpp v64, v64, v64 quad_perm:[1,0,3,2] row_mask:0xf bank_mask:0xf bound_ctrl:1
	s_nop 1
	v_add_f32_dpp v64, v64, v64 quad_perm:[2,3,0,1] row_mask:0xf bank_mask:0xf bound_ctrl:1
	s_nop 1
	v_add_f32_dpp v64, v64, v64 row_half_mirror row_mask:0xf bank_mask:0xf bound_ctrl:1
	s_nop 1
	v_add_f32_dpp v64, v64, v64 row_ror:8 row_mask:0xf bank_mask:0xf bound_ctrl:1
	v_mov_b32_e32 v65, v64
	s_nop 1
	v_permlane16_swap_b32_e32 v64, v65
	v_add_f32_e32 v64, v64, v65
	v_mov_b32_e32 v65, v64
	s_nop 1
	v_permlane32_swap_b32_e32 v64, v65
	s_and_saveexec_b64 s[10:11], s[2:3]
	s_lshl_b64 s[16:17], s[8:9], 2
	s_add_u32 s16, s12, s16
	v_add_f32_e32 v64, v64, v65
	s_addc_u32 s17, s13, s17
	global_store_dword v129, v64, s[16:17]
	s_or_b64 exec, exec, s[10:11]
	v_lshl_or_b32 v2, v2, 7, v136
	global_load_dwordx4 v[68:71], v2, s[4:5]
	v_lshl_or_b32 v3, v3, 7, v136
	global_load_dwordx4 v[64:67], v3, s[4:5]
	s_add_u32 s22, s20, 0x200
	s_lshl_b32 s22, s22, 9
	v_lshl_add_u64 v[28:29], v[134:135], 0, s[22:23]
	global_load_dwordx4 v[16:19], v[28:29], off offset:48
	global_load_dwordx4 v[20:23], v[28:29], off offset:32
	global_load_dwordx4 v[24:27], v[28:29], off offset:16
	s_nop 0
	global_load_dwordx4 v[28:31], v[28:29], off
	s_add_u32 s22, s20, 0x400
	s_lshl_b32 s22, s22, 9
	v_lshl_add_u64 v[12:13], v[132:133], 0, s[22:23]
	global_load_dwordx4 v[0:3], v[12:13], off offset:48
	global_load_dwordx4 v[4:7], v[12:13], off offset:32
	global_load_dwordx4 v[8:11], v[12:13], off offset:16
	s_nop 0
	global_load_dwordx4 v[12:15], v[12:13], off
	s_add_u32 s6, s20, 0x100
	s_waitcnt vmcnt(26)
	v_cvt_pk_f32_fp8_e32 v[138:139], v240
	v_cvt_pk_f32_fp8_sdwa v[140:141], v240 src0_sel:WORD_1
	v_cvt_pk_f32_fp8_e32 v[142:143], v241
	v_cvt_pk_f32_fp8_sdwa v[240:241], v241 src0_sel:WORD_1
	v_cvt_pk_f32_fp8_e32 v[144:145], v242
	v_cvt_pk_f32_fp8_sdwa v[146:147], v242 src0_sel:WORD_1
	v_cvt_pk_f32_fp8_e32 v[148:149], v243
	v_cvt_pk_f32_fp8_sdwa v[242:243], v243 src0_sel:WORD_1
	v_cvt_pk_f32_fp8_e32 v[150:151], v236
	v_cvt_pk_f32_fp8_sdwa v[152:153], v236 src0_sel:WORD_1
	v_cvt_pk_f32_fp8_e32 v[154:155], v237
	v_cvt_pk_f32_fp8_sdwa v[236:237], v237 src0_sel:WORD_1
	v_cvt_pk_f32_fp8_e32 v[156:157], v238
	v_cvt_pk_f32_fp8_sdwa v[158:159], v238 src0_sel:WORD_1
	v_cvt_pk_f32_fp8_e32 v[160:161], v239
	v_cvt_pk_f32_fp8_sdwa v[238:239], v239 src0_sel:WORD_1
	v_pk_fma_f32 v[138:139], v[138:139], v[48:49], 0 op_sel_hi:[1,0,0]
	v_pk_fma_f32 v[140:141], v[140:141], v[48:49], 0 op_sel_hi:[1,0,0]
	v_pk_fma_f32 v[142:143], v[142:143], v[48:49], 0 op_sel_hi:[1,0,0]
	v_pk_fma_f32 v[240:241], v[240:241], v[48:49], 0 op_sel_hi:[1,0,0]
	v_pk_fma_f32 v[144:145], v[144:145], v[48:49], 0 op_sel_hi:[1,0,0]
	v_pk_fma_f32 v[146:147], v[146:147], v[48:49], 0 op_sel_hi:[1,0,0]
	v_pk_fma_f32 v[148:149], v[148:149], v[48:49], 0 op_sel_hi:[1,0,0]
	v_pk_fma_f32 v[242:243], v[242:243], v[48:49], 0 op_sel_hi:[1,0,0]
	v_pk_fma_f32 v[138:139], v[150:151], v[48:49], v[138:139] op_sel:[0,1,0]
	v_pk_fma_f32 v[140:141], v[152:153], v[48:49], v[140:141] op_sel:[0,1,0]
	v_pk_fma_f32 v[142:143], v[154:155], v[48:49], v[142:143] op_sel:[0,1,0]
	v_pk_fma_f32 v[236:237], v[236:237], v[48:49], v[240:241] op_sel:[0,1,0]
	v_pk_fma_f32 v[240:241], v[156:157], v[48:49], v[144:145] op_sel:[0,1,0]
	v_pk_fma_f32 v[144:145], v[158:159], v[48:49], v[146:147] op_sel:[0,1,0]
	v_pk_fma_f32 v[146:147], v[160:161], v[48:49], v[148:149] op_sel:[0,1,0]
	v_pk_fma_f32 v[238:239], v[238:239], v[48:49], v[242:243] op_sel:[0,1,0]
	v_cvt_pk_f32_fp8_e32 v[242:243], v232
	v_cvt_pk_f32_fp8_sdwa v[148:149], v232 src0_sel:WORD_1
	v_cvt_pk_f32_fp8_e32 v[150:151], v233
	v_cvt_pk_f32_fp8_sdwa v[232:233], v233 src0_sel:WORD_1
	v_cvt_pk_f32_fp8_e32 v[152:153], v234
	v_cvt_pk_f32_fp8_sdwa v[154:155], v234 src0_sel:WORD_1
	v_cvt_pk_f32_fp8_e32 v[156:157], v235
	v_cvt_pk_f32_fp8_sdwa v[234:235], v235 src0_sel:WORD_1
	v_pk_fma_f32 v[242:243], v[242:243], v[50:51], v[138:139] op_sel_hi:[1,0,1]
	v_pk_fma_f32 v[138:139], v[148:149], v[50:51], v[140:141] op_sel_hi:[1,0,1]
	v_pk_fma_f32 v[140:141], v[150:151], v[50:51], v[142:143] op_sel_hi:[1,0,1]
	v_pk_fma_f32 v[232:233], v[232:233], v[50:51], v[236:237] op_sel_hi:[1,0,1]
	v_pk_fma_f32 v[236:237], v[152:153], v[50:51], v[240:241] op_sel_hi:[1,0,1]
	v_pk_fma_f32 v[240:241], v[154:155], v[50:51], v[144:145] op_sel_hi:[1,0,1]
	v_pk_fma_f32 v[142:143], v[156:157], v[50:51], v[146:147] op_sel_hi:[1,0,1]
	v_pk_fma_f32 v[234:235], v[234:235], v[50:51], v[238:239] op_sel_hi:[1,0,1]
	v_cvt_pk_f32_fp8_e32 v[238:239], v228
	v_cvt_pk_f32_fp8_sdwa v[144:145], v228 src0_sel:WORD_1
	v_cvt_pk_f32_fp8_e32 v[146:147], v229
	v_cvt_pk_f32_fp8_sdwa v[228:229], v229 src0_sel:WORD_1
	v_cvt_pk_f32_fp8_e32 v[148:149], v230
	v_cvt_pk_f32_fp8_sdwa v[150:151], v230 src0_sel:WORD_1
	v_cvt_pk_f32_fp8_e32 v[152:153], v231
	v_cvt_pk_f32_fp8_sdwa v[230:231], v231 src0_sel:WORD_1
	v_mov_b32_e32 v128, v51
	v_pk_fma_f32 v[238:239], v[238:239], v[128:129], v[242:243] op_sel_hi:[1,0,1]
	v_pk_fma_f32 v[242:243], v[144:145], v[128:129], v[138:139] op_sel_hi:[1,0,1]
	v_pk_fma_f32 v[138:139], v[146:147], v[128:129], v[140:141] op_sel_hi:[1,0,1]
	v_pk_fma_f32 v[228:229], v[228:229], v[128:129], v[232:233] op_sel_hi:[1,0,1]
	v_pk_fma_f32 v[232:233], v[148:149], v[128:129], v[236:237] op_sel_hi:[1,0,1]
	v_pk_fma_f32 v[236:237], v[150:151], v[128:129], v[240:241] op_sel_hi:[1,0,1]
	v_pk_fma_f32 v[240:241], v[152:153], v[128:129], v[142:143] op_sel_hi:[1,0,1]
	v_pk_fma_f32 v[230:231], v[230:231], v[128:129], v[234:235] op_sel_hi:[1,0,1]
	v_cvt_pk_f32_fp8_e32 v[234:235], v224
	v_cvt_pk_f32_fp8_sdwa v[140:141], v224 src0_sel:WORD_1
	v_cvt_pk_f32_fp8_e32 v[142:143], v225
	v_cvt_pk_f32_fp8_sdwa v[224:225], v225 src0_sel:WORD_1
	v_cvt_pk_f32_fp8_e32 v[144:145], v226
	v_cvt_pk_f32_fp8_sdwa v[146:147], v226 src0_sel:WORD_1
	v_cvt_pk_f32_fp8_e32 v[148:149], v227
	v_cvt_pk_f32_fp8_sdwa v[226:227], v227 src0_sel:WORD_1
	v_pk_fma_f32 v[234:235], v[234:235], v[52:53], v[238:239] op_sel_hi:[1,0,1]
	v_pk_fma_f32 v[238:239], v[140:141], v[52:53], v[242:243] op_sel_hi:[1,0,1]
	v_pk_fma_f32 v[242:243], v[142:143], v[52:53], v[138:139] op_sel_hi:[1,0,1]
	v_pk_fma_f32 v[224:225], v[224:225], v[52:53], v[228:229] op_sel_hi:[1,0,1]
	v_pk_fma_f32 v[228:229], v[144:145], v[52:53], v[232:233] op_sel_hi:[1,0,1]
	v_pk_fma_f32 v[232:233], v[146:147], v[52:53], v[236:237] op_sel_hi:[1,0,1]
	v_pk_fma_f32 v[236:237], v[148:149], v[52:53], v[240:241] op_sel_hi:[1,0,1]
	v_pk_fma_f32 v[226:227], v[226:227], v[52:53], v[230:231] op_sel_hi:[1,0,1]
	v_cvt_pk_f32_fp8_e32 v[230:231], v220
	v_cvt_pk_f32_fp8_sdwa v[240:241], v220 src0_sel:WORD_1
	v_cvt_pk_f32_fp8_e32 v[138:139], v221
	v_cvt_pk_f32_fp8_sdwa v[220:221], v221 src0_sel:WORD_1
	v_cvt_pk_f32_fp8_e32 v[140:141], v222
	v_cvt_pk_f32_fp8_sdwa v[142:143], v222 src0_sel:WORD_1
	v_cvt_pk_f32_fp8_e32 v[144:145], v223
	v_cvt_pk_f32_fp8_sdwa v[222:223], v223 src0_sel:WORD_1
	v_pk_fma_f32 v[230:231], v[230:231], v[52:53], v[234:235] op_sel:[0,1,0]
	v_pk_fma_f32 v[234:235], v[240:241], v[52:53], v[238:239] op_sel:[0,1,0]
	v_pk_fma_f32 v[238:239], v[138:139], v[52:53], v[242:243] op_sel:[0,1,0]
	v_pk_fma_f32 v[220:221], v[220:221], v[52:53], v[224:225] op_sel:[0,1,0]
	v_pk_fma_f32 v[224:225], v[140:141], v[52:53], v[228:229] op_sel:[0,1,0]
	v_pk_fma_f32 v[228:229], v[142:143], v[52:53], v[232:233] op_sel:[0,1,0]
	v_pk_fma_f32 v[232:233], v[144:145], v[52:53], v[236:237] op_sel:[0,1,0]
	v_pk_fma_f32 v[222:223], v[222:223], v[52:53], v[226:227] op_sel:[0,1,0]
	v_cvt_pk_f32_fp8_e32 v[226:227], v216
	v_cvt_pk_f32_fp8_sdwa v[236:237], v216 src0_sel:WORD_1
	v_cvt_pk_f32_fp8_e32 v[240:241], v217
	v_cvt_pk_f32_fp8_sdwa v[216:217], v217 src0_sel:WORD_1
	v_cvt_pk_f32_fp8_e32 v[242:243], v218
	v_cvt_pk_f32_fp8_sdwa v[138:139], v218 src0_sel:WORD_1
	v_cvt_pk_f32_fp8_e32 v[140:141], v219
	v_cvt_pk_f32_fp8_sdwa v[218:219], v219 src0_sel:WORD_1
	v_pk_fma_f32 v[226:227], v[226:227], v[54:55], v[230:231] op_sel_hi:[1,0,1]
	v_pk_fma_f32 v[230:231], v[236:237], v[54:55], v[234:235] op_sel_hi:[1,0,1]
	v_pk_fma_f32 v[234:235], v[240:241], v[54:55], v[238:239] op_sel_hi:[1,0,1]
	v_pk_fma_f32 v[216:217], v[216:217], v[54:55], v[220:221] op_sel_hi:[1,0,1]
	v_pk_fma_f32 v[220:221], v[242:243], v[54:55], v[224:225] op_sel_hi:[1,0,1]
	v_pk_fma_f32 v[224:225], v[138:139], v[54:55], v[228:229] op_sel_hi:[1,0,1]
	v_pk_fma_f32 v[228:229], v[140:141], v[54:55], v[232:233] op_sel_hi:[1,0,1]
	v_pk_fma_f32 v[218:219], v[218:219], v[54:55], v[222:223] op_sel_hi:[1,0,1]
	v_cvt_pk_f32_fp8_e32 v[222:223], v212
	v_cvt_pk_f32_fp8_sdwa v[232:233], v212 src0_sel:WORD_1
	v_cvt_pk_f32_fp8_e32 v[236:237], v213
	v_cvt_pk_f32_fp8_sdwa v[212:213], v213 src0_sel:WORD_1
	v_cvt_pk_f32_fp8_e32 v[238:239], v214
	v_cvt_pk_f32_fp8_sdwa v[240:241], v214 src0_sel:WORD_1
	v_cvt_pk_f32_fp8_e32 v[242:243], v215
	v_cvt_pk_f32_fp8_sdwa v[214:215], v215 src0_sel:WORD_1
	v_mov_b32_e32 v128, v55
	v_pk_fma_f32 v[222:223], v[222:223], v[128:129], v[226:227] op_sel_hi:[1,0,1]
	v_pk_fma_f32 v[226:227], v[232:233], v[128:129], v[230:231] op_sel_hi:[1,0,1]
	v_pk_fma_f32 v[230:231], v[236:237], v[128:129], v[234:235] op_sel_hi:[1,0,1]
	v_pk_fma_f32 v[212:213], v[212:213], v[128:129], v[216:217] op_sel_hi:[1,0,1]
	v_pk_fma_f32 v[216:217], v[238:239], v[128:129], v[220:221] op_sel_hi:[1,0,1]
	v_pk_fma_f32 v[220:221], v[240:241], v[128:129], v[224:225] op_sel_hi:[1,0,1]
	v_pk_fma_f32 v[224:225], v[242:243], v[128:129], v[228:229] op_sel_hi:[1,0,1]
	v_lshl_or_b32 v32, v32, 7, v136
	global_load_dwordx4 v[240:243], v32, s[4:5]
	v_pk_fma_f32 v[214:215], v[214:215], v[128:129], v[218:219] op_sel_hi:[1,0,1]
	v_cvt_pk_f32_fp8_e32 v[218:219], v200
	v_cvt_pk_f32_fp8_sdwa v[228:229], v200 src0_sel:WORD_1
	v_cvt_pk_f32_fp8_e32 v[232:233], v201
	v_cvt_pk_f32_fp8_sdwa v[200:201], v201 src0_sel:WORD_1
	v_cvt_pk_f32_fp8_e32 v[234:235], v202
	v_cvt_pk_f32_fp8_sdwa v[236:237], v202 src0_sel:WORD_1
	v_cvt_pk_f32_fp8_e32 v[238:239], v203
	v_cvt_pk_f32_fp8_sdwa v[202:203], v203 src0_sel:WORD_1
	v_pk_fma_f32 v[218:219], v[218:219], v[56:57], v[222:223] op_sel_hi:[1,0,1]
	v_pk_fma_f32 v[222:223], v[228:229], v[56:57], v[226:227] op_sel_hi:[1,0,1]
	v_pk_fma_f32 v[226:227], v[232:233], v[56:57], v[230:231] op_sel_hi:[1,0,1]
	v_pk_fma_f32 v[200:201], v[200:201], v[56:57], v[212:213] op_sel_hi:[1,0,1]
	v_pk_fma_f32 v[212:213], v[234:235], v[56:57], v[216:217] op_sel_hi:[1,0,1]
	v_pk_fma_f32 v[216:217], v[236:237], v[56:57], v[220:221] op_sel_hi:[1,0,1]
	v_pk_fma_f32 v[220:221], v[238:239], v[56:57], v[224:225] op_sel_hi:[1,0,1]
	v_lshl_or_b32 v33, v33, 7, v136
	global_load_dwordx4 v[236:239], v33, s[4:5]
	v_pk_fma_f32 v[202:203], v[202:203], v[56:57], v[214:215] op_sel_hi:[1,0,1]
	v_cvt_pk_f32_fp8_e32 v[214:215], v196
	v_cvt_pk_f32_fp8_sdwa v[224:225], v196 src0_sel:WORD_1
	v_cvt_pk_f32_fp8_e32 v[228:229], v197
	v_cvt_pk_f32_fp8_sdwa v[196:197], v197 src0_sel:WORD_1
	v_cvt_pk_f32_fp8_e32 v[230:231], v198
	v_cvt_pk_f32_fp8_sdwa v[232:233], v198 src0_sel:WORD_1
	v_cvt_pk_f32_fp8_e32 v[234:235], v199
	v_cvt_pk_f32_fp8_sdwa v[198:199], v199 src0_sel:WORD_1
	v_pk_fma_f32 v[214:215], v[214:215], v[56:57], v[218:219] op_sel:[0,1,0]
	v_pk_fma_f32 v[218:219], v[224:225], v[56:57], v[222:223] op_sel:[0,1,0]
	v_pk_fma_f32 v[222:223], v[228:229], v[56:57], v[226:227] op_sel:[0,1,0]
	v_pk_fma_f32 v[196:197], v[196:197], v[56:57], v[200:201] op_sel:[0,1,0]
	v_pk_fma_f32 v[200:201], v[230:231], v[56:57], v[212:213] op_sel:[0,1,0]
	v_pk_fma_f32 v[212:213], v[232:233], v[56:57], v[216:217] op_sel:[0,1,0]
	v_pk_fma_f32 v[216:217], v[234:235], v[56:57], v[220:221] op_sel:[0,1,0]
	v_lshl_or_b32 v34, v34, 7, v136
	global_load_dwordx4 v[232:235], v34, s[4:5]
	v_pk_fma_f32 v[198:199], v[198:199], v[56:57], v[202:203] op_sel:[0,1,0]
	v_cvt_pk_f32_fp8_e32 v[202:203], v192
	v_cvt_pk_f32_fp8_sdwa v[220:221], v192 src0_sel:WORD_1
	v_cvt_pk_f32_fp8_e32 v[224:225], v193
	v_cvt_pk_f32_fp8_sdwa v[192:193], v193 src0_sel:WORD_1
	v_cvt_pk_f32_fp8_e32 v[226:227], v194
	v_cvt_pk_f32_fp8_sdwa v[228:229], v194 src0_sel:WORD_1
	v_cvt_pk_f32_fp8_e32 v[230:231], v195
	v_cvt_pk_f32_fp8_sdwa v[194:195], v195 src0_sel:WORD_1
	v_pk_fma_f32 v[202:203], v[202:203], v[58:59], v[214:215] op_sel_hi:[1,0,1]
	v_pk_fma_f32 v[214:215], v[220:221], v[58:59], v[218:219] op_sel_hi:[1,0,1]
	v_pk_fma_f32 v[218:219], v[224:225], v[58:59], v[222:223] op_sel_hi:[1,0,1]
	v_pk_fma_f32 v[192:193], v[192:193], v[58:59], v[196:197] op_sel_hi:[1,0,1]
	v_pk_fma_f32 v[196:197], v[226:227], v[58:59], v[200:201] op_sel_hi:[1,0,1]
	v_pk_fma_f32 v[200:201], v[228:229], v[58:59], v[212:213] op_sel_hi:[1,0,1]
	v_pk_fma_f32 v[212:213], v[230:231], v[58:59], v[216:217] op_sel_hi:[1,0,1]
	v_pk_fma_f32 v[194:195], v[194:195], v[58:59], v[198:199] op_sel_hi:[1,0,1]
	v_cvt_pk_f32_fp8_e32 v[198:199], v184
	v_cvt_pk_f32_fp8_sdwa v[216:217], v184 src0_sel:WORD_1
	v_cvt_pk_f32_fp8_e32 v[220:221], v185
	v_cvt_pk_f32_fp8_sdwa v[184:185], v185 src0_sel:WORD_1
	v_cvt_pk_f32_fp8_e32 v[222:223], v186
	v_cvt_pk_f32_fp8_sdwa v[224:225], v186 src0_sel:WORD_1
	v_cvt_pk_f32_fp8_e32 v[226:227], v187
	v_cvt_pk_f32_fp8_sdwa v[186:187], v187 src0_sel:WORD_1
	v_mov_b32_e32 v228, v59
	v_pk_fma_f32 v[198:199], v[198:199], v[228:229], v[202:203] op_sel_hi:[1,0,1]
	v_pk_fma_f32 v[202:203], v[216:217], v[228:229], v[214:215] op_sel_hi:[1,0,1]
	v_pk_fma_f32 v[214:215], v[220:221], v[228:229], v[218:219] op_sel_hi:[1,0,1]
	v_pk_fma_f32 v[184:185], v[184:185], v[228:229], v[192:193] op_sel_hi:[1,0,1]
	v_pk_fma_f32 v[192:193], v[222:223], v[228:229], v[196:197] op_sel_hi:[1,0,1]
	v_pk_fma_f32 v[196:197], v[224:225], v[228:229], v[200:201] op_sel_hi:[1,0,1]
	v_pk_fma_f32 v[200:201], v[226:227], v[228:229], v[212:213] op_sel_hi:[1,0,1]
	v_lshl_or_b32 v36, v36, 7, v136
	global_load_dwordx4 v[224:227], v36, s[4:5]
	v_pk_fma_f32 v[186:187], v[186:187], v[228:229], v[194:195] op_sel_hi:[1,0,1]
	v_lshl_or_b32 v35, v35, 7, v136
	global_load_dwordx4 v[228:231], v35, s[4:5]
	v_cvt_pk_f32_fp8_e32 v[194:195], v180
	v_cvt_pk_f32_fp8_sdwa v[212:213], v180 src0_sel:WORD_1
	v_cvt_pk_f32_fp8_e32 v[216:217], v181
	v_cvt_pk_f32_fp8_sdwa v[180:181], v181 src0_sel:WORD_1
	v_cvt_pk_f32_fp8_e32 v[218:219], v182
	v_cvt_pk_f32_fp8_sdwa v[220:221], v182 src0_sel:WORD_1
	v_cvt_pk_f32_fp8_e32 v[222:223], v183
	v_cvt_pk_f32_fp8_sdwa v[182:183], v183 src0_sel:WORD_1
	v_pk_fma_f32 v[194:195], v[194:195], v[60:61], v[198:199] op_sel_hi:[1,0,1]
	v_pk_fma_f32 v[198:199], v[212:213], v[60:61], v[202:203] op_sel_hi:[1,0,1]
	v_pk_fma_f32 v[202:203], v[216:217], v[60:61], v[214:215] op_sel_hi:[1,0,1]
	v_pk_fma_f32 v[180:181], v[180:181], v[60:61], v[184:185] op_sel_hi:[1,0,1]
	v_pk_fma_f32 v[184:185], v[218:219], v[60:61], v[192:193] op_sel_hi:[1,0,1]
	v_pk_fma_f32 v[192:193], v[220:221], v[60:61], v[196:197] op_sel_hi:[1,0,1]
	v_pk_fma_f32 v[196:197], v[222:223], v[60:61], v[200:201] op_sel_hi:[1,0,1]
	v_lshl_or_b32 v37, v37, 7, v136
	global_load_dwordx4 v[220:223], v37, s[4:5]
	v_pk_fma_f32 v[182:183], v[182:183], v[60:61], v[186:187] op_sel_hi:[1,0,1]
	v_cvt_pk_f32_fp8_e32 v[186:187], v172
	v_cvt_pk_f32_fp8_sdwa v[200:201], v172 src0_sel:WORD_1
	v_cvt_pk_f32_fp8_e32 v[212:213], v173
	v_cvt_pk_f32_fp8_sdwa v[172:173], v173 src0_sel:WORD_1
	v_cvt_pk_f32_fp8_e32 v[214:215], v174
	v_cvt_pk_f32_fp8_sdwa v[216:217], v174 src0_sel:WORD_1
	v_cvt_pk_f32_fp8_e32 v[218:219], v175
	v_cvt_pk_f32_fp8_sdwa v[174:175], v175 src0_sel:WORD_1
	v_pk_fma_f32 v[186:187], v[186:187], v[60:61], v[194:195] op_sel:[0,1,0]
	v_pk_fma_f32 v[194:195], v[200:201], v[60:61], v[198:199] op_sel:[0,1,0]
	v_pk_fma_f32 v[198:199], v[212:213], v[60:61], v[202:203] op_sel:[0,1,0]
	v_pk_fma_f32 v[172:173], v[172:173], v[60:61], v[180:181] op_sel:[0,1,0]
	v_pk_fma_f32 v[180:181], v[214:215], v[60:61], v[184:185] op_sel:[0,1,0]
	v_pk_fma_f32 v[184:185], v[216:217], v[60:61], v[192:193] op_sel:[0,1,0]
	v_pk_fma_f32 v[192:193], v[218:219], v[60:61], v[196:197] op_sel:[0,1,0]
	v_lshl_or_b32 v38, v38, 7, v136
; #define PU_IDX(t, E, C) do { const char* eb_ = eiu + (size_t)(t) * 512; const char* cb_ = cfu + (size_t)(t) * 512; \
;     _Pragma("unroll") for (int q = 0; q < 4; ++q) { E[q] = *(const i32x4_t*)(eb_ + (eio + 16u * q)); C[q] = *(const f32x4*)(cb_ + (eio + 16u * q)); } } while (0)
; #define PU_TAB(E, W) do { _Pragma("unroll") for (int q = 0; q < 16; ++q) W[q] = *(const u32x4*)(tabu + ((unsigned)E[q >> 2][q & 3] * 128u + tabo)); } while (0)
; DI void phase_peerup(const Params& p, int bid, int nb) {
;     ...
;     PU_TAB(eB, w);
;     const int t2 = t1 + nw; if (t2 < T_) PU_IDX(t2, eA, cA);
;     PU_MATH(t1, w, cB);
;     if (t2 >= T_) break;
;     t = t2;
;   }
	global_load_dwordx4 v[216:219], v38, s[4:5]
	v_pk_fma_f32 v[174:175], v[174:175], v[60:61], v[182:183] op_sel:[0,1,0]
	v_cvt_pk_f32_fp8_e32 v[182:183], v168
	v_cvt_pk_f32_fp8_sdwa v[196:197], v168 src0_sel:WORD_1
	v_cvt_pk_f32_fp8_e32 v[200:201], v169
	v_cvt_pk_f32_fp8_sdwa v[168:169], v169 src0_sel:WORD_1
	v_cvt_pk_f32_fp8_e32 v[202:203], v170
	v_cvt_pk_f32_fp8_sdwa v[212:213], v170 src0_sel:WORD_1
	v_cvt_pk_f32_fp8_e32 v[214:215], v171
	v_cvt_pk_f32_fp8_sdwa v[170:171], v171 src0_sel:WORD_1
	v_pk_fma_f32 v[182:183], v[182:183], v[62:63], v[186:187] op_sel_hi:[1,0,1]
	v_pk_fma_f32 v[186:187], v[196:197], v[62:63], v[194:195] op_sel_hi:[1,0,1]
	v_pk_fma_f32 v[194:195], v[200:201], v[62:63], v[198:199] op_sel_hi:[1,0,1]
	v_pk_fma_f32 v[168:169], v[168:169], v[62:63], v[172:173] op_sel_hi:[1,0,1]
	v_pk_fma_f32 v[172:173], v[202:203], v[62:63], v[180:181] op_sel_hi:[1,0,1]
	v_pk_fma_f32 v[180:181], v[212:213], v[62:63], v[184:185] op_sel_hi:[1,0,1]
	v_pk_fma_f32 v[184:185], v[214:215], v[62:63], v[192:193] op_sel_hi:[1,0,1]
	v_pk_fma_f32 v[170:171], v[170:171], v[62:63], v[174:175] op_sel_hi:[1,0,1]
	v_cvt_pk_f32_fp8_e32 v[174:175], v164
	v_cvt_pk_f32_fp8_sdwa v[192:193], v164 src0_sel:WORD_1
	v_cvt_pk_f32_fp8_e32 v[196:197], v165
	v_cvt_pk_f32_fp8_sdwa v[164:165], v165 src0_sel:WORD_1
	v_cvt_pk_f32_fp8_e32 v[198:199], v166
	v_cvt_pk_f32_fp8_sdwa v[200:201], v166 src0_sel:WORD_1
	v_cvt_pk_f32_fp8_e32 v[202:203], v167
	v_cvt_pk_f32_fp8_sdwa v[166:167], v167 src0_sel:WORD_1
	v_mov_b32_e32 v212, v63
	v_pk_fma_f32 v[174:175], v[174:175], v[212:213], v[182:183] op_sel_hi:[1,0,1]
	v_pk_fma_f32 v[182:183], v[192:193], v[212:213], v[186:187] op_sel_hi:[1,0,1]
	v_pk_fma_f32 v[186:187], v[196:197], v[212:213], v[194:195] op_sel_hi:[1,0,1]
	v_lshl_or_b32 v42, v42, 7, v136
	global_load_dwordx4 v[192:195], v42, s[4:5]
	v_pk_fma_f32 v[164:165], v[164:165], v[212:213], v[168:169] op_sel_hi:[1,0,1]
	v_pk_fma_f32 v[168:169], v[198:199], v[212:213], v[172:173] op_sel_hi:[1,0,1]
	v_lshl_or_b32 v41, v41, 7, v136
	global_load_dwordx4 v[196:199], v41, s[4:5]
	v_pk_fma_f32 v[172:173], v[200:201], v[212:213], v[180:181] op_sel_hi:[1,0,1]
	v_pk_fma_f32 v[180:181], v[202:203], v[212:213], v[184:185] op_sel_hi:[1,0,1]
	v_lshl_or_b32 v40, v40, 7, v136
	global_load_dwordx4 v[200:203], v40, s[4:5]
	v_pk_fma_f32 v[166:167], v[166:167], v[212:213], v[170:171] op_sel_hi:[1,0,1]
	v_lshl_or_b32 v39, v39, 7, v136
	global_load_dwordx4 v[212:215], v39, s[4:5]
	v_permlane32_swap_b32_e32 v174, v168
	v_permlane32_swap_b32_e32 v175, v169
	v_permlane32_swap_b32_e32 v182, v172
	v_permlane32_swap_b32_e32 v183, v173
	v_permlane32_swap_b32_e32 v186, v180
	v_permlane32_swap_b32_e32 v187, v181
	v_permlane32_swap_b32_e32 v164, v166
	v_permlane32_swap_b32_e32 v165, v167
	v_add_f32_e32 v168, v174, v168
	v_add_f32_e32 v169, v175, v169
	v_add_f32_e32 v170, v182, v172
	v_add_f32_e32 v171, v183, v173
	v_add_f32_e32 v172, v186, v180
	v_add_f32_e32 v173, v187, v181
	v_lshl_or_b32 v43, v43, 7, v136
	global_load_dwordx4 v[184:187], v43, s[4:5]
	v_lshl_or_b32 v44, v44, 7, v136
	global_load_dwordx4 v[180:183], v44, s[4:5]
	v_add_f32_e32 v164, v164, v166
	v_add_f32_e32 v165, v165, v167
	v_permlane16_swap_b32_e32 v168, v172
	v_permlane16_swap_b32_e32 v169, v173
	v_permlane16_swap_b32_e32 v170, v164
	v_permlane16_swap_b32_e32 v171, v165
	v_pk_add_f32 v[166:167], v[168:169], v[172:173]
	v_lshl_or_b32 v45, v45, 7, v136
	global_load_dwordx4 v[172:175], v45, s[4:5]
	v_pk_add_f32 v[164:165], v[170:171], v[164:165]
	s_ashr_i32 s7, s6, 31
	v_cndmask_b32_e64 v168, v166, v164, s[0:1]
	v_cndmask_b32_e64 v170, v164, v166, s[0:1]
	v_cndmask_b32_e64 v164, v167, v165, s[0:1]
	v_mov_b32_dpp v168, v168 row_ror:8 row_mask:0xf bank_mask:0xf bound_ctrl:1
	v_cndmask_b32_e64 v171, v165, v167, s[0:1]
	v_mov_b32_dpp v169, v164 row_ror:8 row_mask:0xf bank_mask:0xf bound_ctrl:1
	v_pk_add_f32 v[166:167], v[170:171], v[168:169]
	s_lshl_b64 s[8:9], s[6:7], 11
	v_pk_mul_f32 v[164:165], v[166:167], v[166:167]
	v_cvt_pk_bf16_f32 v168, v166, v167
	v_add_f32_e32 v164, v164, v165
	v_lshl_add_u64 v[166:167], v[130:131], 0, s[8:9]
	global_store_dword v[166:167], v168, off
	v_add_f32_dpp v164, v164, v164 quad_perm:[1,0,3,2] row_mask:0xf bank_mask:0xf bound_ctrl:1
	s_nop 1
	v_add_f32_dpp v164, v164, v164 quad_perm:[2,3,0,1] row_mask:0xf bank_mask:0xf bound_ctrl:1
	s_nop 1
	v_add_f32_dpp v164, v164, v164 row_half_mirror row_mask:0xf bank_mask:0xf bound_ctrl:1
	s_nop 1
	v_add_f32_dpp v164, v164, v164 row_ror:8 row_mask:0xf bank_mask:0xf bound_ctrl:1
	v_mov_b32_e32 v165, v164
	s_nop 1
	v_permlane16_swap_b32_e32 v164, v165
	v_add_f32_e32 v164, v164, v165
	v_mov_b32_e32 v165, v164
	s_nop 1
	v_permlane32_swap_b32_e32 v164, v165
	s_and_saveexec_b64 s[8:9], s[2:3]
	s_lshl_b64 s[10:11], s[6:7], 2
	s_add_u32 s10, s12, s10
	v_add_f32_e32 v164, v164, v165
	s_addc_u32 s11, s13, s11
	global_store_dword v129, v164, s[10:11]
	s_or_b64 exec, exec, s[8:9]
	v_lshl_or_b32 v46, v46, 7, v136
	global_load_dwordx4 v[168:171], v46, s[4:5]
	v_lshl_or_b32 v47, v47, 7, v136
	global_load_dwordx4 v[164:167], v47, s[4:5]
	s_add_u32 s22, s20, 0x300
	s_lshl_b32 s22, s22, 9
	v_lshl_add_u64 v[48:49], v[134:135], 0, s[22:23]
	global_load_dwordx4 v[60:63], v[48:49], off offset:48
	global_load_dwordx4 v[56:59], v[48:49], off offset:32
	global_load_dwordx4 v[52:55], v[48:49], off offset:16
	s_nop 0
	global_load_dwordx4 v[48:51], v[48:49], off
	s_add_u32 s22, s20, 0x500
	s_lshl_b32 s22, s22, 9
	v_lshl_add_u64 v[32:33], v[132:133], 0, s[22:23]
	global_load_dwordx4 v[44:47], v[32:33], off offset:48
	global_load_dwordx4 v[40:43], v[32:33], off offset:32
	global_load_dwordx4 v[36:39], v[32:33], off offset:16
	s_nop 0
	global_load_dwordx4 v[32:35], v[32:33], off
	s_add_u32 s20, s20, 0x200
	s_sub_u32 s24, s24, 1
	s_cmp_lg_u32 s24, 0
	s_cbranch_scc1 .Lpu2_loop
	s_mov_b32 s8, s20
	s_waitcnt vmcnt(26)
	v_cvt_pk_f32_fp8_e32 v[138:139], v124
	v_cvt_pk_f32_fp8_sdwa v[140:141], v124 src0_sel:WORD_1
	v_cvt_pk_f32_fp8_e32 v[142:143], v125
	v_cvt_pk_f32_fp8_sdwa v[124:125], v125 src0_sel:WORD_1
	v_cvt_pk_f32_fp8_e32 v[144:145], v126
	v_cvt_pk_f32_fp8_sdwa v[146:147], v126 src0_sel:WORD_1
	v_cvt_pk_f32_fp8_e32 v[148:149], v127
	v_cvt_pk_f32_fp8_sdwa v[126:127], v127 src0_sel:WORD_1
	v_cvt_pk_f32_fp8_e32 v[150:151], v120
	v_cvt_pk_f32_fp8_sdwa v[152:153], v120 src0_sel:WORD_1
	v_cvt_pk_f32_fp8_e32 v[154:155], v121
	v_cvt_pk_f32_fp8_sdwa v[120:121], v121 src0_sel:WORD_1
	v_cvt_pk_f32_fp8_e32 v[156:157], v122
	v_cvt_pk_f32_fp8_sdwa v[158:159], v122 src0_sel:WORD_1
	v_cvt_pk_f32_fp8_e32 v[160:161], v123
	v_cvt_pk_f32_fp8_sdwa v[122:123], v123 src0_sel:WORD_1
	v_pk_fma_f32 v[138:139], v[138:139], v[28:29], 0 op_sel_hi:[1,0,0]
	v_pk_fma_f32 v[140:141], v[140:141], v[28:29], 0 op_sel_hi:[1,0,0]
	v_pk_fma_f32 v[142:143], v[142:143], v[28:29], 0 op_sel_hi:[1,0,0]
	v_pk_fma_f32 v[124:125], v[124:125], v[28:29], 0 op_sel_hi:[1,0,0]
	v_pk_fma_f32 v[144:145], v[144:145], v[28:29], 0 op_sel_hi:[1,0,0]
	v_pk_fma_f32 v[146:147], v[146:147], v[28:29], 0 op_sel_hi:[1,0,0]
	v_pk_fma_f32 v[148:149], v[148:149], v[28:29], 0 op_sel_hi:[1,0,0]
	v_pk_fma_f32 v[126:127], v[126:127], v[28:29], 0 op_sel_hi:[1,0,0]
	v_pk_fma_f32 v[138:139], v[150:151], v[28:29], v[138:139] op_sel:[0,1,0]
	v_pk_fma_f32 v[140:141], v[152:153], v[28:29], v[140:141] op_sel:[0,1,0]
	v_pk_fma_f32 v[142:143], v[154:155], v[28:29], v[142:143] op_sel:[0,1,0]
	v_pk_fma_f32 v[120:121], v[120:121], v[28:29], v[124:125] op_sel:[0,1,0]
	v_pk_fma_f32 v[124:125], v[156:157], v[28:29], v[144:145] op_sel:[0,1,0]
	v_pk_fma_f32 v[144:145], v[158:159], v[28:29], v[146:147] op_sel:[0,1,0]
	v_pk_fma_f32 v[146:147], v[160:161], v[28:29], v[148:149] op_sel:[0,1,0]
	v_pk_fma_f32 v[122:123], v[122:123], v[28:29], v[126:127] op_sel:[0,1,0]
	v_cvt_pk_f32_fp8_e32 v[126:127], v116
	v_cvt_pk_f32_fp8_sdwa v[148:149], v116 src0_sel:WORD_1
	v_cvt_pk_f32_fp8_e32 v[150:151], v117
	v_cvt_pk_f32_fp8_sdwa v[116:117], v117 src0_sel:WORD_1
	v_cvt_pk_f32_fp8_e32 v[152:153], v118
	v_cvt_pk_f32_fp8_sdwa v[154:155], v118 src0_sel:WORD_1
	v_cvt_pk_f32_fp8_e32 v[156:157], v119
	v_cvt_pk_f32_fp8_sdwa v[118:119], v119 src0_sel:WORD_1
	v_pk_fma_f32 v[126:127], v[126:127], v[30:31], v[138:139] op_sel_hi:[1,0,1]
	v_pk_fma_f32 v[138:139], v[148:149], v[30:31], v[140:141] op_sel_hi:[1,0,1]
	v_pk_fma_f32 v[140:141], v[150:151], v[30:31], v[142:143] op_sel_hi:[1,0,1]
	v_pk_fma_f32 v[116:117], v[116:117], v[30:31], v[120:121] op_sel_hi:[1,0,1]
	v_pk_fma_f32 v[120:121], v[152:153], v[30:31], v[124:125] op_sel_hi:[1,0,1]
	v_pk_fma_f32 v[124:125], v[154:155], v[30:31], v[144:145] op_sel_hi:[1,0,1]
	v_pk_fma_f32 v[142:143], v[156:157], v[30:31], v[146:147] op_sel_hi:[1,0,1]
	v_pk_fma_f32 v[118:119], v[118:119], v[30:31], v[122:123] op_sel_hi:[1,0,1]
	v_cvt_pk_f32_fp8_e32 v[122:123], v112
	v_cvt_pk_f32_fp8_sdwa v[144:145], v112 src0_sel:WORD_1
	v_cvt_pk_f32_fp8_e32 v[146:147], v113
	v_cvt_pk_f32_fp8_sdwa v[112:113], v113 src0_sel:WORD_1
	v_cvt_pk_f32_fp8_e32 v[148:149], v114
	v_cvt_pk_f32_fp8_sdwa v[150:151], v114 src0_sel:WORD_1
	v_cvt_pk_f32_fp8_e32 v[152:153], v115
	v_cvt_pk_f32_fp8_sdwa v[114:115], v115 src0_sel:WORD_1
	v_mov_b32_e32 v128, v31
	v_pk_fma_f32 v[122:123], v[122:123], v[128:129], v[126:127] op_sel_hi:[1,0,1]
	v_pk_fma_f32 v[126:127], v[144:145], v[128:129], v[138:139] op_sel_hi:[1,0,1]
	v_pk_fma_f32 v[138:139], v[146:147], v[128:129], v[140:141] op_sel_hi:[1,0,1]
	v_pk_fma_f32 v[112:113], v[112:113], v[128:129], v[116:117] op_sel_hi:[1,0,1]
	v_pk_fma_f32 v[116:117], v[148:149], v[128:129], v[120:121] op_sel_hi:[1,0,1]
	v_pk_fma_f32 v[120:121], v[150:151], v[128:129], v[124:125] op_sel_hi:[1,0,1]
	v_pk_fma_f32 v[124:125], v[152:153], v[128:129], v[142:143] op_sel_hi:[1,0,1]
	v_pk_fma_f32 v[114:115], v[114:115], v[128:129], v[118:119] op_sel_hi:[1,0,1]
	v_cvt_pk_f32_fp8_e32 v[118:119], v108
	v_cvt_pk_f32_fp8_sdwa v[140:141], v108 src0_sel:WORD_1
	v_cvt_pk_f32_fp8_e32 v[142:143], v109
	v_cvt_pk_f32_fp8_sdwa v[108:109], v109 src0_sel:WORD_1
	v_cvt_pk_f32_fp8_e32 v[144:145], v110
	v_cvt_pk_f32_fp8_sdwa v[146:147], v110 src0_sel:WORD_1
	v_cvt_pk_f32_fp8_e32 v[148:149], v111
	v_cvt_pk_f32_fp8_sdwa v[110:111], v111 src0_sel:WORD_1
	v_pk_fma_f32 v[118:119], v[118:119], v[24:25], v[122:123] op_sel_hi:[1,0,1]
	v_pk_fma_f32 v[122:123], v[140:141], v[24:25], v[126:127] op_sel_hi:[1,0,1]
	v_pk_fma_f32 v[126:127], v[142:143], v[24:25], v[138:139] op_sel_hi:[1,0,1]
	v_pk_fma_f32 v[108:109], v[108:109], v[24:25], v[112:113] op_sel_hi:[1,0,1]
	v_pk_fma_f32 v[112:113], v[144:145], v[24:25], v[116:117] op_sel_hi:[1,0,1]
	v_pk_fma_f32 v[116:117], v[146:147], v[24:25], v[120:121] op_sel_hi:[1,0,1]
	v_pk_fma_f32 v[120:121], v[148:149], v[24:25], v[124:125] op_sel_hi:[1,0,1]
	v_pk_fma_f32 v[110:111], v[110:111], v[24:25], v[114:115] op_sel_hi:[1,0,1]
	v_cvt_pk_f32_fp8_e32 v[114:115], v104
	v_cvt_pk_f32_fp8_sdwa v[124:125], v104 src0_sel:WORD_1
	v_cvt_pk_f32_fp8_e32 v[138:139], v105
	v_cvt_pk_f32_fp8_sdwa v[104:105], v105 src0_sel:WORD_1
	v_cvt_pk_f32_fp8_e32 v[140:141], v106
	v_cvt_pk_f32_fp8_sdwa v[142:143], v106 src0_sel:WORD_1
	v_cvt_pk_f32_fp8_e32 v[144:145], v107
	v_cvt_pk_f32_fp8_sdwa v[106:107], v107 src0_sel:WORD_1
	v_pk_fma_f32 v[114:115], v[114:115], v[24:25], v[118:119] op_sel:[0,1,0]
	v_pk_fma_f32 v[118:119], v[124:125], v[24:25], v[122:123] op_sel:[0,1,0]
	v_pk_fma_f32 v[122:123], v[138:139], v[24:25], v[126:127] op_sel:[0,1,0]
	v_pk_fma_f32 v[104:105], v[104:105], v[24:25], v[108:109] op_sel:[0,1,0]
	v_pk_fma_f32 v[108:109], v[140:141], v[24:25], v[112:113] op_sel:[0,1,0]
	v_pk_fma_f32 v[112:113], v[142:143], v[24:25], v[116:117] op_sel:[0,1,0]
	v_pk_fma_f32 v[116:117], v[144:145], v[24:25], v[120:121] op_sel:[0,1,0]
	v_pk_fma_f32 v[106:107], v[106:107], v[24:25], v[110:111] op_sel:[0,1,0]
	v_cvt_pk_f32_fp8_e32 v[110:111], v100
	v_cvt_pk_f32_fp8_sdwa v[120:121], v100 src0_sel:WORD_1
	v_cvt_pk_f32_fp8_e32 v[124:125], v101
	v_cvt_pk_f32_fp8_sdwa v[100:101], v101 src0_sel:WORD_1
	v_cvt_pk_f32_fp8_e32 v[126:127], v102
	v_cvt_pk_f32_fp8_sdwa v[138:139], v102 src0_sel:WORD_1
	v_cvt_pk_f32_fp8_e32 v[140:141], v103
	v_cvt_pk_f32_fp8_sdwa v[102:103], v103 src0_sel:WORD_1
	v_pk_fma_f32 v[110:111], v[110:111], v[26:27], v[114:115] op_sel_hi:[1,0,1]
	v_pk_fma_f32 v[114:115], v[120:121], v[26:27], v[118:119] op_sel_hi:[1,0,1]
	v_pk_fma_f32 v[118:119], v[124:125], v[26:27], v[122:123] op_sel_hi:[1,0,1]
	v_pk_fma_f32 v[100:101], v[100:101], v[26:27], v[104:105] op_sel_hi:[1,0,1]
	v_pk_fma_f32 v[104:105], v[126:127], v[26:27], v[108:109] op_sel_hi:[1,0,1]
	v_pk_fma_f32 v[108:109], v[138:139], v[26:27], v[112:113] op_sel_hi:[1,0,1]
	v_pk_fma_f32 v[112:113], v[140:141], v[26:27], v[116:117] op_sel_hi:[1,0,1]
	v_pk_fma_f32 v[102:103], v[102:103], v[26:27], v[106:107] op_sel_hi:[1,0,1]
	v_cvt_pk_f32_fp8_e32 v[106:107], v96
	v_cvt_pk_f32_fp8_sdwa v[116:117], v96 src0_sel:WORD_1
	v_cvt_pk_f32_fp8_e32 v[120:121], v97
	v_cvt_pk_f32_fp8_sdwa v[96:97], v97 src0_sel:WORD_1
	v_cvt_pk_f32_fp8_e32 v[122:123], v98
	v_cvt_pk_f32_fp8_sdwa v[124:125], v98 src0_sel:WORD_1
	v_cvt_pk_f32_fp8_e32 v[126:127], v99
	v_cvt_pk_f32_fp8_sdwa v[98:99], v99 src0_sel:WORD_1
	v_mov_b32_e32 v128, v27
	v_pk_fma_f32 v[106:107], v[106:107], v[128:129], v[110:111] op_sel_hi:[1,0,1]
	v_pk_fma_f32 v[110:111], v[116:117], v[128:129], v[114:115] op_sel_hi:[1,0,1]
	v_pk_fma_f32 v[114:115], v[120:121], v[128:129], v[118:119] op_sel_hi:[1,0,1]
	v_pk_fma_f32 v[96:97], v[96:97], v[128:129], v[100:101] op_sel_hi:[1,0,1]
	v_pk_fma_f32 v[100:101], v[122:123], v[128:129], v[104:105] op_sel_hi:[1,0,1]
	v_pk_fma_f32 v[104:105], v[124:125], v[128:129], v[108:109] op_sel_hi:[1,0,1]
	v_pk_fma_f32 v[108:109], v[126:127], v[128:129], v[112:113] op_sel_hi:[1,0,1]
	v_lshl_or_b32 v12, v12, 7, v136
	global_load_dwordx4 v[124:127], v12, s[4:5]
	v_pk_fma_f32 v[98:99], v[98:99], v[128:129], v[102:103] op_sel_hi:[1,0,1]
	v_cvt_pk_f32_fp8_e32 v[102:103], v92
	v_cvt_pk_f32_fp8_sdwa v[112:113], v92 src0_sel:WORD_1
	v_cvt_pk_f32_fp8_e32 v[116:117], v93
	v_cvt_pk_f32_fp8_sdwa v[92:93], v93 src0_sel:WORD_1
	v_cvt_pk_f32_fp8_e32 v[118:119], v94
	v_cvt_pk_f32_fp8_sdwa v[120:121], v94 src0_sel:WORD_1
	v_cvt_pk_f32_fp8_e32 v[122:123], v95
	v_cvt_pk_f32_fp8_sdwa v[94:95], v95 src0_sel:WORD_1
	v_pk_fma_f32 v[102:103], v[102:103], v[20:21], v[106:107] op_sel_hi:[1,0,1]
	v_pk_fma_f32 v[106:107], v[112:113], v[20:21], v[110:111] op_sel_hi:[1,0,1]
	v_pk_fma_f32 v[110:111], v[116:117], v[20:21], v[114:115] op_sel_hi:[1,0,1]
	v_pk_fma_f32 v[92:93], v[92:93], v[20:21], v[96:97] op_sel_hi:[1,0,1]
	v_pk_fma_f32 v[96:97], v[118:119], v[20:21], v[100:101] op_sel_hi:[1,0,1]
	v_pk_fma_f32 v[100:101], v[120:121], v[20:21], v[104:105] op_sel_hi:[1,0,1]
	v_pk_fma_f32 v[104:105], v[122:123], v[20:21], v[108:109] op_sel_hi:[1,0,1]
	v_lshl_or_b32 v13, v13, 7, v136
	global_load_dwordx4 v[120:123], v13, s[4:5]
	v_pk_fma_f32 v[94:95], v[94:95], v[20:21], v[98:99] op_sel_hi:[1,0,1]
	v_cvt_pk_f32_fp8_e32 v[98:99], v88
	v_cvt_pk_f32_fp8_sdwa v[108:109], v88 src0_sel:WORD_1
	v_cvt_pk_f32_fp8_e32 v[112:113], v89
	v_cvt_pk_f32_fp8_sdwa v[88:89], v89 src0_sel:WORD_1
	v_cvt_pk_f32_fp8_e32 v[114:115], v90
	v_cvt_pk_f32_fp8_sdwa v[116:117], v90 src0_sel:WORD_1
	v_cvt_pk_f32_fp8_e32 v[118:119], v91
	v_cvt_pk_f32_fp8_sdwa v[90:91], v91 src0_sel:WORD_1
	v_pk_fma_f32 v[98:99], v[98:99], v[20:21], v[102:103] op_sel:[0,1,0]
	v_pk_fma_f32 v[102:103], v[108:109], v[20:21], v[106:107] op_sel:[0,1,0]
	v_pk_fma_f32 v[106:107], v[112:113], v[20:21], v[110:111] op_sel:[0,1,0]
	v_pk_fma_f32 v[88:89], v[88:89], v[20:21], v[92:93] op_sel:[0,1,0]
	v_pk_fma_f32 v[92:93], v[114:115], v[20:21], v[96:97] op_sel:[0,1,0]
	v_pk_fma_f32 v[96:97], v[116:117], v[20:21], v[100:101] op_sel:[0,1,0]
	v_pk_fma_f32 v[100:101], v[118:119], v[20:21], v[104:105] op_sel:[0,1,0]
	v_lshl_or_b32 v14, v14, 7, v136
	global_load_dwordx4 v[116:119], v14, s[4:5]
	v_pk_fma_f32 v[90:91], v[90:91], v[20:21], v[94:95] op_sel:[0,1,0]
	v_cvt_pk_f32_fp8_e32 v[94:95], v84
	v_cvt_pk_f32_fp8_sdwa v[104:105], v84 src0_sel:WORD_1
	v_cvt_pk_f32_fp8_e32 v[108:109], v85
	v_cvt_pk_f32_fp8_sdwa v[84:85], v85 src0_sel:WORD_1
	v_cvt_pk_f32_fp8_e32 v[110:111], v86
	v_cvt_pk_f32_fp8_sdwa v[112:113], v86 src0_sel:WORD_1
	v_cvt_pk_f32_fp8_e32 v[114:115], v87
	v_cvt_pk_f32_fp8_sdwa v[86:87], v87 src0_sel:WORD_1
	v_pk_fma_f32 v[94:95], v[94:95], v[22:23], v[98:99] op_sel_hi:[1,0,1]
	v_pk_fma_f32 v[98:99], v[104:105], v[22:23], v[102:103] op_sel_hi:[1,0,1]
	v_pk_fma_f32 v[102:103], v[108:109], v[22:23], v[106:107] op_sel_hi:[1,0,1]
	v_pk_fma_f32 v[84:85], v[84:85], v[22:23], v[88:89] op_sel_hi:[1,0,1]
	v_pk_fma_f32 v[88:89], v[110:111], v[22:23], v[92:93] op_sel_hi:[1,0,1]
	v_pk_fma_f32 v[92:93], v[112:113], v[22:23], v[96:97] op_sel_hi:[1,0,1]
	v_pk_fma_f32 v[96:97], v[114:115], v[22:23], v[100:101] op_sel_hi:[1,0,1]
	v_pk_fma_f32 v[86:87], v[86:87], v[22:23], v[90:91] op_sel_hi:[1,0,1]
	v_cvt_pk_f32_fp8_e32 v[90:91], v80
	v_cvt_pk_f32_fp8_sdwa v[100:101], v80 src0_sel:WORD_1
	v_cvt_pk_f32_fp8_e32 v[104:105], v81
	v_cvt_pk_f32_fp8_sdwa v[80:81], v81 src0_sel:WORD_1
	v_cvt_pk_f32_fp8_e32 v[106:107], v82
	v_cvt_pk_f32_fp8_sdwa v[108:109], v82 src0_sel:WORD_1
	v_cvt_pk_f32_fp8_e32 v[110:111], v83
	v_cvt_pk_f32_fp8_sdwa v[82:83], v83 src0_sel:WORD_1
	v_mov_b32_e32 v112, v23
	v_pk_fma_f32 v[90:91], v[90:91], v[112:113], v[94:95] op_sel_hi:[1,0,1]
	v_pk_fma_f32 v[94:95], v[100:101], v[112:113], v[98:99] op_sel_hi:[1,0,1]
	v_pk_fma_f32 v[98:99], v[104:105], v[112:113], v[102:103] op_sel_hi:[1,0,1]
	v_pk_fma_f32 v[80:81], v[80:81], v[112:113], v[84:85] op_sel_hi:[1,0,1]
	v_pk_fma_f32 v[84:85], v[106:107], v[112:113], v[88:89] op_sel_hi:[1,0,1]
	v_pk_fma_f32 v[88:89], v[108:109], v[112:113], v[92:93] op_sel_hi:[1,0,1]
	v_pk_fma_f32 v[92:93], v[110:111], v[112:113], v[96:97] op_sel_hi:[1,0,1]
	v_lshl_or_b32 v8, v8, 7, v136
	global_load_dwordx4 v[108:111], v8, s[4:5]
	v_pk_fma_f32 v[82:83], v[82:83], v[112:113], v[86:87] op_sel_hi:[1,0,1]
	v_lshl_or_b32 v15, v15, 7, v136
	global_load_dwordx4 v[112:115], v15, s[4:5]
	v_cvt_pk_f32_fp8_e32 v[86:87], v76
	v_cvt_pk_f32_fp8_sdwa v[96:97], v76 src0_sel:WORD_1
	v_cvt_pk_f32_fp8_e32 v[100:101], v77
	v_cvt_pk_f32_fp8_sdwa v[76:77], v77 src0_sel:WORD_1
	v_cvt_pk_f32_fp8_e32 v[102:103], v78
	v_cvt_pk_f32_fp8_sdwa v[104:105], v78 src0_sel:WORD_1
	v_cvt_pk_f32_fp8_e32 v[106:107], v79
	v_cvt_pk_f32_fp8_sdwa v[78:79], v79 src0_sel:WORD_1
	v_pk_fma_f32 v[86:87], v[86:87], v[16:17], v[90:91] op_sel_hi:[1,0,1]
	v_pk_fma_f32 v[90:91], v[96:97], v[16:17], v[94:95] op_sel_hi:[1,0,1]
	v_pk_fma_f32 v[94:95], v[100:101], v[16:17], v[98:99] op_sel_hi:[1,0,1]
	v_pk_fma_f32 v[76:77], v[76:77], v[16:17], v[80:81] op_sel_hi:[1,0,1]
	v_pk_fma_f32 v[80:81], v[102:103], v[16:17], v[84:85] op_sel_hi:[1,0,1]
	v_pk_fma_f32 v[84:85], v[104:105], v[16:17], v[88:89] op_sel_hi:[1,0,1]
	v_pk_fma_f32 v[88:89], v[106:107], v[16:17], v[92:93] op_sel_hi:[1,0,1]
	v_lshl_or_b32 v9, v9, 7, v136
	global_load_dwordx4 v[104:107], v9, s[4:5]
	v_pk_fma_f32 v[78:79], v[78:79], v[16:17], v[82:83] op_sel_hi:[1,0,1]
	v_cvt_pk_f32_fp8_e32 v[82:83], v72
	v_cvt_pk_f32_fp8_sdwa v[92:93], v72 src0_sel:WORD_1
	v_cvt_pk_f32_fp8_e32 v[96:97], v73
	v_cvt_pk_f32_fp8_sdwa v[72:73], v73 src0_sel:WORD_1
	v_cvt_pk_f32_fp8_e32 v[98:99], v74
	v_cvt_pk_f32_fp8_sdwa v[100:101], v74 src0_sel:WORD_1
	v_cvt_pk_f32_fp8_e32 v[102:103], v75
	v_cvt_pk_f32_fp8_sdwa v[74:75], v75 src0_sel:WORD_1
	v_pk_fma_f32 v[82:83], v[82:83], v[16:17], v[86:87] op_sel:[0,1,0]
	v_pk_fma_f32 v[86:87], v[92:93], v[16:17], v[90:91] op_sel:[0,1,0]
	v_pk_fma_f32 v[90:91], v[96:97], v[16:17], v[94:95] op_sel:[0,1,0]
	v_pk_fma_f32 v[72:73], v[72:73], v[16:17], v[76:77] op_sel:[0,1,0]
	v_pk_fma_f32 v[76:77], v[98:99], v[16:17], v[80:81] op_sel:[0,1,0]
	v_pk_fma_f32 v[80:81], v[100:101], v[16:17], v[84:85] op_sel:[0,1,0]
	v_pk_fma_f32 v[84:85], v[102:103], v[16:17], v[88:89] op_sel:[0,1,0]
	v_lshl_or_b32 v10, v10, 7, v136
	global_load_dwordx4 v[100:103], v10, s[4:5]
	v_pk_fma_f32 v[74:75], v[74:75], v[16:17], v[78:79] op_sel:[0,1,0]
	v_cvt_pk_f32_fp8_e32 v[78:79], v68
	v_cvt_pk_f32_fp8_sdwa v[88:89], v68 src0_sel:WORD_1
	v_cvt_pk_f32_fp8_e32 v[92:93], v69
	v_cvt_pk_f32_fp8_sdwa v[68:69], v69 src0_sel:WORD_1
	v_cvt_pk_f32_fp8_e32 v[94:95], v70
	v_cvt_pk_f32_fp8_sdwa v[96:97], v70 src0_sel:WORD_1
	v_cvt_pk_f32_fp8_e32 v[98:99], v71
	v_cvt_pk_f32_fp8_sdwa v[70:71], v71 src0_sel:WORD_1
	v_pk_fma_f32 v[78:79], v[78:79], v[18:19], v[82:83] op_sel_hi:[1,0,1]
	v_pk_fma_f32 v[82:83], v[88:89], v[18:19], v[86:87] op_sel_hi:[1,0,1]
	v_pk_fma_f32 v[86:87], v[92:93], v[18:19], v[90:91] op_sel_hi:[1,0,1]
	v_pk_fma_f32 v[68:69], v[68:69], v[18:19], v[72:73] op_sel_hi:[1,0,1]
	v_pk_fma_f32 v[72:73], v[94:95], v[18:19], v[76:77] op_sel_hi:[1,0,1]
	v_pk_fma_f32 v[76:77], v[96:97], v[18:19], v[80:81] op_sel_hi:[1,0,1]
	v_pk_fma_f32 v[80:81], v[98:99], v[18:19], v[84:85] op_sel_hi:[1,0,1]
	v_pk_fma_f32 v[70:71], v[70:71], v[18:19], v[74:75] op_sel_hi:[1,0,1]
	v_cvt_pk_f32_fp8_e32 v[74:75], v64
	v_cvt_pk_f32_fp8_sdwa v[84:85], v64 src0_sel:WORD_1
	v_cvt_pk_f32_fp8_e32 v[88:89], v65
	v_cvt_pk_f32_fp8_sdwa v[64:65], v65 src0_sel:WORD_1
	v_cvt_pk_f32_fp8_e32 v[90:91], v66
	v_cvt_pk_f32_fp8_sdwa v[92:93], v66 src0_sel:WORD_1
	v_cvt_pk_f32_fp8_e32 v[94:95], v67
	v_cvt_pk_f32_fp8_sdwa v[66:67], v67 src0_sel:WORD_1
	v_mov_b32_e32 v96, v19
	v_pk_fma_f32 v[74:75], v[74:75], v[96:97], v[78:79] op_sel_hi:[1,0,1]
	v_pk_fma_f32 v[78:79], v[84:85], v[96:97], v[82:83] op_sel_hi:[1,0,1]
	v_pk_fma_f32 v[82:83], v[88:89], v[96:97], v[86:87] op_sel_hi:[1,0,1]
	v_lshl_or_b32 v6, v6, 7, v136
	global_load_dwordx4 v[84:87], v6, s[4:5]
	v_pk_fma_f32 v[64:65], v[64:65], v[96:97], v[68:69] op_sel_hi:[1,0,1]
	v_pk_fma_f32 v[68:69], v[90:91], v[96:97], v[72:73] op_sel_hi:[1,0,1]
	v_lshl_or_b32 v5, v5, 7, v136
	global_load_dwordx4 v[88:91], v5, s[4:5]
	v_pk_fma_f32 v[72:73], v[92:93], v[96:97], v[76:77] op_sel_hi:[1,0,1]
	v_pk_fma_f32 v[76:77], v[94:95], v[96:97], v[80:81] op_sel_hi:[1,0,1]
	v_lshl_or_b32 v4, v4, 7, v136
	global_load_dwordx4 v[92:95], v4, s[4:5]
	v_pk_fma_f32 v[66:67], v[66:67], v[96:97], v[70:71] op_sel_hi:[1,0,1]
	v_lshl_or_b32 v11, v11, 7, v136
	global_load_dwordx4 v[96:99], v11, s[4:5]
	v_permlane32_swap_b32_e32 v74, v68
	v_permlane32_swap_b32_e32 v75, v69
	v_permlane32_swap_b32_e32 v78, v72
	v_permlane32_swap_b32_e32 v79, v73
	v_permlane32_swap_b32_e32 v82, v76
	v_permlane32_swap_b32_e32 v83, v77
	v_permlane32_swap_b32_e32 v64, v66
	v_permlane32_swap_b32_e32 v65, v67
	v_add_f32_e32 v68, v74, v68
	v_add_f32_e32 v69, v75, v69
	v_add_f32_e32 v70, v78, v72
	v_add_f32_e32 v71, v79, v73
	v_add_f32_e32 v72, v82, v76
	v_add_f32_e32 v73, v83, v77
	v_lshl_or_b32 v7, v7, 7, v136
	global_load_dwordx4 v[80:83], v7, s[4:5]
	v_lshl_or_b32 v0, v0, 7, v136
; #define PU_IDX(t, E, C) do { const char* eb_ = eiu + (size_t)(t) * 512; const char* cb_ = cfu + (size_t)(t) * 512; \
;     _Pragma("unroll") for (int q = 0; q < 4; ++q) { E[q] = *(const i32x4_t*)(eb_ + (eio + 16u * q)); C[q] = *(const f32x4*)(cb_ + (eio + 16u * q)); } } while (0)
; #define PU_TAB(E, W) do { _Pragma("unroll") for (int q = 0; q < 16; ++q) W[q] = *(const u32x4*)(tabu + ((unsigned)E[q >> 2][q & 3] * 128u + tabo)); } while (0)
; DI void phase_peerup(const Params& p, int bid, int nb) {
;     ...
;     PU_TAB(eB, w);
;     const int t2 = t1 + nw; if (t2 < T_) PU_IDX(t2, eA, cA);
;     PU_MATH(t1, w, cB);
	global_load_dwordx4 v[76:79], v0, s[4:5]
	v_add_f32_e32 v64, v64, v66
	v_add_f32_e32 v65, v65, v67
	v_permlane16_swap_b32_e32 v68, v72
	v_permlane16_swap_b32_e32 v69, v73
	v_permlane16_swap_b32_e32 v70, v64
	v_permlane16_swap_b32_e32 v71, v65
	v_pk_add_f32 v[66:67], v[68:69], v[72:73]
	v_lshl_or_b32 v1, v1, 7, v136
	global_load_dwordx4 v[72:75], v1, s[4:5]
	v_pk_add_f32 v[64:65], v[70:71], v[64:65]
	s_ashr_i32 s9, s8, 31
	v_cndmask_b32_e64 v68, v66, v64, s[0:1]
	v_cndmask_b32_e64 v70, v64, v66, s[0:1]
	v_cndmask_b32_e64 v64, v67, v65, s[0:1]
	v_mov_b32_dpp v68, v68 row_ror:8 row_mask:0xf bank_mask:0xf bound_ctrl:1
	v_cndmask_b32_e64 v71, v65, v67, s[0:1]
	v_mov_b32_dpp v69, v64 row_ror:8 row_mask:0xf bank_mask:0xf bound_ctrl:1
	v_pk_add_f32 v[66:67], v[70:71], v[68:69]
	s_lshl_b64 s[10:11], s[8:9], 11
	v_pk_mul_f32 v[64:65], v[66:67], v[66:67]
	v_cvt_pk_bf16_f32 v68, v66, v67
	v_add_f32_e32 v64, v64, v65
	v_lshl_add_u64 v[66:67], v[130:131], 0, s[10:11]
	global_store_dword v[66:67], v68, off
	v_add_f32_dpp v64, v64, v64 quad_perm:[1,0,3,2] row_mask:0xf bank_mask:0xf bound_ctrl:1
	s_nop 1
	v_add_f32_dpp v64, v64, v64 quad_perm:[2,3,0,1] row_mask:0xf bank_mask:0xf bound_ctrl:1
	s_nop 1
	v_add_f32_dpp v64, v64, v64 row_half_mirror row_mask:0xf bank_mask:0xf bound_ctrl:1
	s_nop 1
	v_add_f32_dpp v64, v64, v64 row_ror:8 row_mask:0xf bank_mask:0xf bound_ctrl:1
	v_mov_b32_e32 v65, v64
	s_nop 1
	v_permlane16_swap_b32_e32 v64, v65
	v_add_f32_e32 v64, v64, v65
	v_mov_b32_e32 v65, v64
	s_nop 1
	v_permlane32_swap_b32_e32 v64, v65
	s_and_saveexec_b64 s[10:11], s[2:3]
	s_lshl_b64 s[16:17], s[8:9], 2
	s_add_u32 s16, s12, s16
	v_add_f32_e32 v64, v64, v65
	s_addc_u32 s17, s13, s17
	global_store_dword v129, v64, s[16:17]
	s_or_b64 exec, exec, s[10:11]
	v_lshl_or_b32 v2, v2, 7, v136
	global_load_dwordx4 v[68:71], v2, s[4:5]
	v_lshl_or_b32 v3, v3, 7, v136
	global_load_dwordx4 v[64:67], v3, s[4:5]
	s_add_u32 s22, s20, 0x200
	s_lshl_b32 s22, s22, 9
	v_lshl_add_u64 v[28:29], v[134:135], 0, s[22:23]
	global_load_dwordx4 v[16:19], v[28:29], off offset:48
	global_load_dwordx4 v[20:23], v[28:29], off offset:32
	global_load_dwordx4 v[24:27], v[28:29], off offset:16
	s_nop 0
	global_load_dwordx4 v[28:31], v[28:29], off
	s_add_u32 s6, s20, 0x100
	s_waitcnt vmcnt(22)
	v_cvt_pk_f32_fp8_e32 v[138:139], v240
	v_cvt_pk_f32_fp8_sdwa v[140:141], v240 src0_sel:WORD_1
	v_cvt_pk_f32_fp8_e32 v[142:143], v241
	v_cvt_pk_f32_fp8_sdwa v[240:241], v241 src0_sel:WORD_1
	v_cvt_pk_f32_fp8_e32 v[144:145], v242
	v_cvt_pk_f32_fp8_sdwa v[146:147], v242 src0_sel:WORD_1
	v_cvt_pk_f32_fp8_e32 v[148:149], v243
	v_cvt_pk_f32_fp8_sdwa v[242:243], v243 src0_sel:WORD_1
	v_cvt_pk_f32_fp8_e32 v[150:151], v236
	v_cvt_pk_f32_fp8_sdwa v[152:153], v236 src0_sel:WORD_1
	v_cvt_pk_f32_fp8_e32 v[154:155], v237
	v_cvt_pk_f32_fp8_sdwa v[236:237], v237 src0_sel:WORD_1
	v_cvt_pk_f32_fp8_e32 v[156:157], v238
	v_cvt_pk_f32_fp8_sdwa v[158:159], v238 src0_sel:WORD_1
	v_cvt_pk_f32_fp8_e32 v[160:161], v239
	v_cvt_pk_f32_fp8_sdwa v[238:239], v239 src0_sel:WORD_1
	v_pk_fma_f32 v[138:139], v[138:139], v[48:49], 0 op_sel_hi:[1,0,0]
	v_pk_fma_f32 v[140:141], v[140:141], v[48:49], 0 op_sel_hi:[1,0,0]
	v_pk_fma_f32 v[142:143], v[142:143], v[48:49], 0 op_sel_hi:[1,0,0]
	v_pk_fma_f32 v[240:241], v[240:241], v[48:49], 0 op_sel_hi:[1,0,0]
	v_pk_fma_f32 v[144:145], v[144:145], v[48:49], 0 op_sel_hi:[1,0,0]
	v_pk_fma_f32 v[146:147], v[146:147], v[48:49], 0 op_sel_hi:[1,0,0]
	v_pk_fma_f32 v[148:149], v[148:149], v[48:49], 0 op_sel_hi:[1,0,0]
	v_pk_fma_f32 v[242:243], v[242:243], v[48:49], 0 op_sel_hi:[1,0,0]
	v_pk_fma_f32 v[138:139], v[150:151], v[48:49], v[138:139] op_sel:[0,1,0]
	v_pk_fma_f32 v[140:141], v[152:153], v[48:49], v[140:141] op_sel:[0,1,0]
	v_pk_fma_f32 v[142:143], v[154:155], v[48:49], v[142:143] op_sel:[0,1,0]
	v_pk_fma_f32 v[236:237], v[236:237], v[48:49], v[240:241] op_sel:[0,1,0]
	v_pk_fma_f32 v[240:241], v[156:157], v[48:49], v[144:145] op_sel:[0,1,0]
	v_pk_fma_f32 v[144:145], v[158:159], v[48:49], v[146:147] op_sel:[0,1,0]
	v_pk_fma_f32 v[146:147], v[160:161], v[48:49], v[148:149] op_sel:[0,1,0]
	v_pk_fma_f32 v[238:239], v[238:239], v[48:49], v[242:243] op_sel:[0,1,0]
	v_cvt_pk_f32_fp8_e32 v[242:243], v232
	v_cvt_pk_f32_fp8_sdwa v[148:149], v232 src0_sel:WORD_1
	v_cvt_pk_f32_fp8_e32 v[150:151], v233
	v_cvt_pk_f32_fp8_sdwa v[232:233], v233 src0_sel:WORD_1
	v_cvt_pk_f32_fp8_e32 v[152:153], v234
	v_cvt_pk_f32_fp8_sdwa v[154:155], v234 src0_sel:WORD_1
	v_cvt_pk_f32_fp8_e32 v[156:157], v235
	v_cvt_pk_f32_fp8_sdwa v[234:235], v235 src0_sel:WORD_1
	v_pk_fma_f32 v[242:243], v[242:243], v[50:51], v[138:139] op_sel_hi:[1,0,1]
	v_pk_fma_f32 v[138:139], v[148:149], v[50:51], v[140:141] op_sel_hi:[1,0,1]
	v_pk_fma_f32 v[140:141], v[150:151], v[50:51], v[142:143] op_sel_hi:[1,0,1]
	v_pk_fma_f32 v[232:233], v[232:233], v[50:51], v[236:237] op_sel_hi:[1,0,1]
	v_pk_fma_f32 v[236:237], v[152:153], v[50:51], v[240:241] op_sel_hi:[1,0,1]
	v_pk_fma_f32 v[240:241], v[154:155], v[50:51], v[144:145] op_sel_hi:[1,0,1]
	v_pk_fma_f32 v[142:143], v[156:157], v[50:51], v[146:147] op_sel_hi:[1,0,1]
	v_pk_fma_f32 v[234:235], v[234:235], v[50:51], v[238:239] op_sel_hi:[1,0,1]
	v_cvt_pk_f32_fp8_e32 v[238:239], v228
	v_cvt_pk_f32_fp8_sdwa v[144:145], v228 src0_sel:WORD_1
	v_cvt_pk_f32_fp8_e32 v[146:147], v229
	v_cvt_pk_f32_fp8_sdwa v[228:229], v229 src0_sel:WORD_1
	v_cvt_pk_f32_fp8_e32 v[148:149], v230
	v_cvt_pk_f32_fp8_sdwa v[150:151], v230 src0_sel:WORD_1
	v_cvt_pk_f32_fp8_e32 v[152:153], v231
	v_cvt_pk_f32_fp8_sdwa v[230:231], v231 src0_sel:WORD_1
	v_mov_b32_e32 v128, v51
	v_pk_fma_f32 v[238:239], v[238:239], v[128:129], v[242:243] op_sel_hi:[1,0,1]
	v_pk_fma_f32 v[242:243], v[144:145], v[128:129], v[138:139] op_sel_hi:[1,0,1]
	v_pk_fma_f32 v[138:139], v[146:147], v[128:129], v[140:141] op_sel_hi:[1,0,1]
	v_pk_fma_f32 v[228:229], v[228:229], v[128:129], v[232:233] op_sel_hi:[1,0,1]
	v_pk_fma_f32 v[232:233], v[148:149], v[128:129], v[236:237] op_sel_hi:[1,0,1]
	v_pk_fma_f32 v[236:237], v[150:151], v[128:129], v[240:241] op_sel_hi:[1,0,1]
	v_pk_fma_f32 v[240:241], v[152:153], v[128:129], v[142:143] op_sel_hi:[1,0,1]
	v_pk_fma_f32 v[230:231], v[230:231], v[128:129], v[234:235] op_sel_hi:[1,0,1]
	v_cvt_pk_f32_fp8_e32 v[234:235], v224
	v_cvt_pk_f32_fp8_sdwa v[140:141], v224 src0_sel:WORD_1
	v_cvt_pk_f32_fp8_e32 v[142:143], v225
	v_cvt_pk_f32_fp8_sdwa v[224:225], v225 src0_sel:WORD_1
	v_cvt_pk_f32_fp8_e32 v[144:145], v226
	v_cvt_pk_f32_fp8_sdwa v[146:147], v226 src0_sel:WORD_1
	v_cvt_pk_f32_fp8_e32 v[148:149], v227
	v_cvt_pk_f32_fp8_sdwa v[226:227], v227 src0_sel:WORD_1
	v_pk_fma_f32 v[234:235], v[234:235], v[52:53], v[238:239] op_sel_hi:[1,0,1]
	v_pk_fma_f32 v[238:239], v[140:141], v[52:53], v[242:243] op_sel_hi:[1,0,1]
	v_pk_fma_f32 v[242:243], v[142:143], v[52:53], v[138:139] op_sel_hi:[1,0,1]
	v_pk_fma_f32 v[224:225], v[224:225], v[52:53], v[228:229] op_sel_hi:[1,0,1]
	v_pk_fma_f32 v[228:229], v[144:145], v[52:53], v[232:233] op_sel_hi:[1,0,1]
	v_pk_fma_f32 v[232:233], v[146:147], v[52:53], v[236:237] op_sel_hi:[1,0,1]
	v_pk_fma_f32 v[236:237], v[148:149], v[52:53], v[240:241] op_sel_hi:[1,0,1]
	v_pk_fma_f32 v[226:227], v[226:227], v[52:53], v[230:231] op_sel_hi:[1,0,1]
	v_cvt_pk_f32_fp8_e32 v[230:231], v220
	v_cvt_pk_f32_fp8_sdwa v[240:241], v220 src0_sel:WORD_1
	v_cvt_pk_f32_fp8_e32 v[138:139], v221
	v_cvt_pk_f32_fp8_sdwa v[220:221], v221 src0_sel:WORD_1
	v_cvt_pk_f32_fp8_e32 v[140:141], v222
	v_cvt_pk_f32_fp8_sdwa v[142:143], v222 src0_sel:WORD_1
	v_cvt_pk_f32_fp8_e32 v[144:145], v223
	v_cvt_pk_f32_fp8_sdwa v[222:223], v223 src0_sel:WORD_1
	v_pk_fma_f32 v[230:231], v[230:231], v[52:53], v[234:235] op_sel:[0,1,0]
	v_pk_fma_f32 v[234:235], v[240:241], v[52:53], v[238:239] op_sel:[0,1,0]
	v_pk_fma_f32 v[238:239], v[138:139], v[52:53], v[242:243] op_sel:[0,1,0]
	v_pk_fma_f32 v[220:221], v[220:221], v[52:53], v[224:225] op_sel:[0,1,0]
	v_pk_fma_f32 v[224:225], v[140:141], v[52:53], v[228:229] op_sel:[0,1,0]
	v_pk_fma_f32 v[228:229], v[142:143], v[52:53], v[232:233] op_sel:[0,1,0]
	v_pk_fma_f32 v[232:233], v[144:145], v[52:53], v[236:237] op_sel:[0,1,0]
	v_pk_fma_f32 v[222:223], v[222:223], v[52:53], v[226:227] op_sel:[0,1,0]
	v_cvt_pk_f32_fp8_e32 v[226:227], v216
	v_cvt_pk_f32_fp8_sdwa v[236:237], v216 src0_sel:WORD_1
	v_cvt_pk_f32_fp8_e32 v[240:241], v217
	v_cvt_pk_f32_fp8_sdwa v[216:217], v217 src0_sel:WORD_1
	v_cvt_pk_f32_fp8_e32 v[242:243], v218
	v_cvt_pk_f32_fp8_sdwa v[138:139], v218 src0_sel:WORD_1
	v_cvt_pk_f32_fp8_e32 v[140:141], v219
	v_cvt_pk_f32_fp8_sdwa v[218:219], v219 src0_sel:WORD_1
	v_pk_fma_f32 v[226:227], v[226:227], v[54:55], v[230:231] op_sel_hi:[1,0,1]
	v_pk_fma_f32 v[230:231], v[236:237], v[54:55], v[234:235] op_sel_hi:[1,0,1]
	v_pk_fma_f32 v[234:235], v[240:241], v[54:55], v[238:239] op_sel_hi:[1,0,1]
	v_pk_fma_f32 v[216:217], v[216:217], v[54:55], v[220:221] op_sel_hi:[1,0,1]
	v_pk_fma_f32 v[220:221], v[242:243], v[54:55], v[224:225] op_sel_hi:[1,0,1]
	v_pk_fma_f32 v[224:225], v[138:139], v[54:55], v[228:229] op_sel_hi:[1,0,1]
	v_pk_fma_f32 v[228:229], v[140:141], v[54:55], v[232:233] op_sel_hi:[1,0,1]
	v_pk_fma_f32 v[218:219], v[218:219], v[54:55], v[222:223] op_sel_hi:[1,0,1]
	v_cvt_pk_f32_fp8_e32 v[222:223], v212
	v_cvt_pk_f32_fp8_sdwa v[232:233], v212 src0_sel:WORD_1
	v_cvt_pk_f32_fp8_e32 v[236:237], v213
	v_cvt_pk_f32_fp8_sdwa v[212:213], v213 src0_sel:WORD_1
	v_cvt_pk_f32_fp8_e32 v[238:239], v214
	v_cvt_pk_f32_fp8_sdwa v[240:241], v214 src0_sel:WORD_1
	v_cvt_pk_f32_fp8_e32 v[242:243], v215
	v_cvt_pk_f32_fp8_sdwa v[214:215], v215 src0_sel:WORD_1
	v_mov_b32_e32 v128, v55
	v_pk_fma_f32 v[222:223], v[222:223], v[128:129], v[226:227] op_sel_hi:[1,0,1]
	v_pk_fma_f32 v[226:227], v[232:233], v[128:129], v[230:231] op_sel_hi:[1,0,1]
	v_pk_fma_f32 v[230:231], v[236:237], v[128:129], v[234:235] op_sel_hi:[1,0,1]
	v_pk_fma_f32 v[212:213], v[212:213], v[128:129], v[216:217] op_sel_hi:[1,0,1]
	v_pk_fma_f32 v[216:217], v[238:239], v[128:129], v[220:221] op_sel_hi:[1,0,1]
	v_pk_fma_f32 v[220:221], v[240:241], v[128:129], v[224:225] op_sel_hi:[1,0,1]
	v_pk_fma_f32 v[224:225], v[242:243], v[128:129], v[228:229] op_sel_hi:[1,0,1]
	v_lshl_or_b32 v32, v32, 7, v136
	global_load_dwordx4 v[240:243], v32, s[4:5]
	v_pk_fma_f32 v[214:215], v[214:215], v[128:129], v[218:219] op_sel_hi:[1,0,1]
	v_cvt_pk_f32_fp8_e32 v[218:219], v200
	v_cvt_pk_f32_fp8_sdwa v[228:229], v200 src0_sel:WORD_1
	v_cvt_pk_f32_fp8_e32 v[232:233], v201
	v_cvt_pk_f32_fp8_sdwa v[200:201], v201 src0_sel:WORD_1
	v_cvt_pk_f32_fp8_e32 v[234:235], v202
	v_cvt_pk_f32_fp8_sdwa v[236:237], v202 src0_sel:WORD_1
	v_cvt_pk_f32_fp8_e32 v[238:239], v203
	v_cvt_pk_f32_fp8_sdwa v[202:203], v203 src0_sel:WORD_1
	v_pk_fma_f32 v[218:219], v[218:219], v[56:57], v[222:223] op_sel_hi:[1,0,1]
	v_pk_fma_f32 v[222:223], v[228:229], v[56:57], v[226:227] op_sel_hi:[1,0,1]
	v_pk_fma_f32 v[226:227], v[232:233], v[56:57], v[230:231] op_sel_hi:[1,0,1]
	v_pk_fma_f32 v[200:201], v[200:201], v[56:57], v[212:213] op_sel_hi:[1,0,1]
	v_pk_fma_f32 v[212:213], v[234:235], v[56:57], v[216:217] op_sel_hi:[1,0,1]
	v_pk_fma_f32 v[216:217], v[236:237], v[56:57], v[220:221] op_sel_hi:[1,0,1]
	v_pk_fma_f32 v[220:221], v[238:239], v[56:57], v[224:225] op_sel_hi:[1,0,1]
	v_lshl_or_b32 v33, v33, 7, v136
	global_load_dwordx4 v[236:239], v33, s[4:5]
	v_pk_fma_f32 v[202:203], v[202:203], v[56:57], v[214:215] op_sel_hi:[1,0,1]
	v_cvt_pk_f32_fp8_e32 v[214:215], v196
	v_cvt_pk_f32_fp8_sdwa v[224:225], v196 src0_sel:WORD_1
	v_cvt_pk_f32_fp8_e32 v[228:229], v197
	v_cvt_pk_f32_fp8_sdwa v[196:197], v197 src0_sel:WORD_1
	v_cvt_pk_f32_fp8_e32 v[230:231], v198
	v_cvt_pk_f32_fp8_sdwa v[232:233], v198 src0_sel:WORD_1
	v_cvt_pk_f32_fp8_e32 v[234:235], v199
	v_cvt_pk_f32_fp8_sdwa v[198:199], v199 src0_sel:WORD_1
	v_pk_fma_f32 v[214:215], v[214:215], v[56:57], v[218:219] op_sel:[0,1,0]
	v_pk_fma_f32 v[218:219], v[224:225], v[56:57], v[222:223] op_sel:[0,1,0]
	v_pk_fma_f32 v[222:223], v[228:229], v[56:57], v[226:227] op_sel:[0,1,0]
	v_pk_fma_f32 v[196:197], v[196:197], v[56:57], v[200:201] op_sel:[0,1,0]
	v_pk_fma_f32 v[200:201], v[230:231], v[56:57], v[212:213] op_sel:[0,1,0]
	v_pk_fma_f32 v[212:213], v[232:233], v[56:57], v[216:217] op_sel:[0,1,0]
	v_pk_fma_f32 v[216:217], v[234:235], v[56:57], v[220:221] op_sel:[0,1,0]
	v_lshl_or_b32 v34, v34, 7, v136
	global_load_dwordx4 v[232:235], v34, s[4:5]
	v_pk_fma_f32 v[198:199], v[198:199], v[56:57], v[202:203] op_sel:[0,1,0]
	v_cvt_pk_f32_fp8_e32 v[202:203], v192
	v_cvt_pk_f32_fp8_sdwa v[220:221], v192 src0_sel:WORD_1
	v_cvt_pk_f32_fp8_e32 v[224:225], v193
	v_cvt_pk_f32_fp8_sdwa v[192:193], v193 src0_sel:WORD_1
	v_cvt_pk_f32_fp8_e32 v[226:227], v194
	v_cvt_pk_f32_fp8_sdwa v[228:229], v194 src0_sel:WORD_1
	v_cvt_pk_f32_fp8_e32 v[230:231], v195
	v_cvt_pk_f32_fp8_sdwa v[194:195], v195 src0_sel:WORD_1
	v_pk_fma_f32 v[202:203], v[202:203], v[58:59], v[214:215] op_sel_hi:[1,0,1]
	v_pk_fma_f32 v[214:215], v[220:221], v[58:59], v[218:219] op_sel_hi:[1,0,1]
	v_pk_fma_f32 v[218:219], v[224:225], v[58:59], v[222:223] op_sel_hi:[1,0,1]
	v_pk_fma_f32 v[192:193], v[192:193], v[58:59], v[196:197] op_sel_hi:[1,0,1]
	v_pk_fma_f32 v[196:197], v[226:227], v[58:59], v[200:201] op_sel_hi:[1,0,1]
	v_pk_fma_f32 v[200:201], v[228:229], v[58:59], v[212:213] op_sel_hi:[1,0,1]
	v_pk_fma_f32 v[212:213], v[230:231], v[58:59], v[216:217] op_sel_hi:[1,0,1]
	v_pk_fma_f32 v[194:195], v[194:195], v[58:59], v[198:199] op_sel_hi:[1,0,1]
	v_cvt_pk_f32_fp8_e32 v[198:199], v184
	v_cvt_pk_f32_fp8_sdwa v[216:217], v184 src0_sel:WORD_1
	v_cvt_pk_f32_fp8_e32 v[220:221], v185
	v_cvt_pk_f32_fp8_sdwa v[184:185], v185 src0_sel:WORD_1
	v_cvt_pk_f32_fp8_e32 v[222:223], v186
	v_cvt_pk_f32_fp8_sdwa v[224:225], v186 src0_sel:WORD_1
	v_cvt_pk_f32_fp8_e32 v[226:227], v187
	v_cvt_pk_f32_fp8_sdwa v[186:187], v187 src0_sel:WORD_1
	v_mov_b32_e32 v228, v59
	v_pk_fma_f32 v[198:199], v[198:199], v[228:229], v[202:203] op_sel_hi:[1,0,1]
	v_pk_fma_f32 v[202:203], v[216:217], v[228:229], v[214:215] op_sel_hi:[1,0,1]
	v_pk_fma_f32 v[214:215], v[220:221], v[228:229], v[218:219] op_sel_hi:[1,0,1]
	v_pk_fma_f32 v[184:185], v[184:185], v[228:229], v[192:193] op_sel_hi:[1,0,1]
	v_pk_fma_f32 v[192:193], v[222:223], v[228:229], v[196:197] op_sel_hi:[1,0,1]
	v_pk_fma_f32 v[196:197], v[224:225], v[228:229], v[200:201] op_sel_hi:[1,0,1]
	v_pk_fma_f32 v[200:201], v[226:227], v[228:229], v[212:213] op_sel_hi:[1,0,1]
	v_lshl_or_b32 v36, v36, 7, v136
	global_load_dwordx4 v[224:227], v36, s[4:5]
	v_pk_fma_f32 v[186:187], v[186:187], v[228:229], v[194:195] op_sel_hi:[1,0,1]
	v_lshl_or_b32 v35, v35, 7, v136
	global_load_dwordx4 v[228:231], v35, s[4:5]
	v_cvt_pk_f32_fp8_e32 v[194:195], v180
	v_cvt_pk_f32_fp8_sdwa v[212:213], v180 src0_sel:WORD_1
	v_cvt_pk_f32_fp8_e32 v[216:217], v181
	v_cvt_pk_f32_fp8_sdwa v[180:181], v181 src0_sel:WORD_1
	v_cvt_pk_f32_fp8_e32 v[218:219], v182
	v_cvt_pk_f32_fp8_sdwa v[220:221], v182 src0_sel:WORD_1
	v_cvt_pk_f32_fp8_e32 v[222:223], v183
	v_cvt_pk_f32_fp8_sdwa v[182:183], v183 src0_sel:WORD_1
	v_pk_fma_f32 v[194:195], v[194:195], v[60:61], v[198:199] op_sel_hi:[1,0,1]
	v_pk_fma_f32 v[198:199], v[212:213], v[60:61], v[202:203] op_sel_hi:[1,0,1]
	v_pk_fma_f32 v[202:203], v[216:217], v[60:61], v[214:215] op_sel_hi:[1,0,1]
	v_pk_fma_f32 v[180:181], v[180:181], v[60:61], v[184:185] op_sel_hi:[1,0,1]
	v_pk_fma_f32 v[184:185], v[218:219], v[60:61], v[192:193] op_sel_hi:[1,0,1]
	v_pk_fma_f32 v[192:193], v[220:221], v[60:61], v[196:197] op_sel_hi:[1,0,1]
	v_pk_fma_f32 v[196:197], v[222:223], v[60:61], v[200:201] op_sel_hi:[1,0,1]
	v_lshl_or_b32 v37, v37, 7, v136
	global_load_dwordx4 v[220:223], v37, s[4:5]
	v_pk_fma_f32 v[182:183], v[182:183], v[60:61], v[186:187] op_sel_hi:[1,0,1]
	v_cvt_pk_f32_fp8_e32 v[186:187], v172
	v_cvt_pk_f32_fp8_sdwa v[200:201], v172 src0_sel:WORD_1
	v_cvt_pk_f32_fp8_e32 v[212:213], v173
	v_cvt_pk_f32_fp8_sdwa v[172:173], v173 src0_sel:WORD_1
	v_cvt_pk_f32_fp8_e32 v[214:215], v174
	v_cvt_pk_f32_fp8_sdwa v[216:217], v174 src0_sel:WORD_1
	v_cvt_pk_f32_fp8_e32 v[218:219], v175
	v_cvt_pk_f32_fp8_sdwa v[174:175], v175 src0_sel:WORD_1
	v_pk_fma_f32 v[186:187], v[186:187], v[60:61], v[194:195] op_sel:[0,1,0]
	v_pk_fma_f32 v[194:195], v[200:201], v[60:61], v[198:199] op_sel:[0,1,0]
	v_pk_fma_f32 v[198:199], v[212:213], v[60:61], v[202:203] op_sel:[0,1,0]
	v_pk_fma_f32 v[172:173], v[172:173], v[60:61], v[180:181] op_sel:[0,1,0]
	v_pk_fma_f32 v[180:181], v[214:215], v[60:61], v[184:185] op_sel:[0,1,0]
	v_pk_fma_f32 v[184:185], v[216:217], v[60:61], v[192:193] op_sel:[0,1,0]
	v_pk_fma_f32 v[192:193], v[218:219], v[60:61], v[196:197] op_sel:[0,1,0]
	v_lshl_or_b32 v38, v38, 7, v136
	global_load_dwordx4 v[216:219], v38, s[4:5]
	v_pk_fma_f32 v[174:175], v[174:175], v[60:61], v[182:183] op_sel:[0,1,0]
	v_cvt_pk_f32_fp8_e32 v[182:183], v168
	v_cvt_pk_f32_fp8_sdwa v[196:197], v168 src0_sel:WORD_1
	v_cvt_pk_f32_fp8_e32 v[200:201], v169
	v_cvt_pk_f32_fp8_sdwa v[168:169], v169 src0_sel:WORD_1
; #define PU_IDX(t, E, C) do { const char* eb_ = eiu + (size_t)(t) * 512; const char* cb_ = cfu + (size_t)(t) * 512; \
;     _Pragma("unroll") for (int q = 0; q < 4; ++q) { E[q] = *(const i32x4_t*)(eb_ + (eio + 16u * q)); C[q] = *(const f32x4*)(cb_ + (eio + 16u * q)); } } while (0)
; #define PU_TAB(E, W) do { _Pragma("unroll") for (int q = 0; q < 16; ++q) W[q] = *(const u32x4*)(tabu + ((unsigned)E[q >> 2][q & 3] * 128u + tabo)); } while (0)
; DI void phase_peerup(const Params& p, int bid, int nb) {
;     ...
;     PU_TAB(eB, w);
;     const int t2 = t1 + nw; if (t2 < T_) PU_IDX(t2, eA, cA);
;     PU_MATH(t1, w, cB);
	v_cvt_pk_f32_fp8_e32 v[202:203], v170
	v_cvt_pk_f32_fp8_sdwa v[212:213], v170 src0_sel:WORD_1
	v_cvt_pk_f32_fp8_e32 v[214:215], v171
	v_cvt_pk_f32_fp8_sdwa v[170:171], v171 src0_sel:WORD_1
	v_pk_fma_f32 v[182:183], v[182:183], v[62:63], v[186:187] op_sel_hi:[1,0,1]
	v_pk_fma_f32 v[186:187], v[196:197], v[62:63], v[194:195] op_sel_hi:[1,0,1]
	v_pk_fma_f32 v[194:195], v[200:201], v[62:63], v[198:199] op_sel_hi:[1,0,1]
	v_pk_fma_f32 v[168:169], v[168:169], v[62:63], v[172:173] op_sel_hi:[1,0,1]
	v_pk_fma_f32 v[172:173], v[202:203], v[62:63], v[180:181] op_sel_hi:[1,0,1]
	v_pk_fma_f32 v[180:181], v[212:213], v[62:63], v[184:185] op_sel_hi:[1,0,1]
	v_pk_fma_f32 v[184:185], v[214:215], v[62:63], v[192:193] op_sel_hi:[1,0,1]
	v_pk_fma_f32 v[170:171], v[170:171], v[62:63], v[174:175] op_sel_hi:[1,0,1]
	v_cvt_pk_f32_fp8_e32 v[174:175], v164
	v_cvt_pk_f32_fp8_sdwa v[192:193], v164 src0_sel:WORD_1
	v_cvt_pk_f32_fp8_e32 v[196:197], v165
	v_cvt_pk_f32_fp8_sdwa v[164:165], v165 src0_sel:WORD_1
	v_cvt_pk_f32_fp8_e32 v[198:199], v166
	v_cvt_pk_f32_fp8_sdwa v[200:201], v166 src0_sel:WORD_1
	v_cvt_pk_f32_fp8_e32 v[202:203], v167
	v_cvt_pk_f32_fp8_sdwa v[166:167], v167 src0_sel:WORD_1
	v_mov_b32_e32 v212, v63
	v_pk_fma_f32 v[174:175], v[174:175], v[212:213], v[182:183] op_sel_hi:[1,0,1]
	v_pk_fma_f32 v[182:183], v[192:193], v[212:213], v[186:187] op_sel_hi:[1,0,1]
	v_pk_fma_f32 v[186:187], v[196:197], v[212:213], v[194:195] op_sel_hi:[1,0,1]
	v_lshl_or_b32 v42, v42, 7, v136
	global_load_dwordx4 v[192:195], v42, s[4:5]
	v_pk_fma_f32 v[164:165], v[164:165], v[212:213], v[168:169] op_sel_hi:[1,0,1]
	v_pk_fma_f32 v[168:169], v[198:199], v[212:213], v[172:173] op_sel_hi:[1,0,1]
	v_lshl_or_b32 v41, v41, 7, v136
	global_load_dwordx4 v[196:199], v41, s[4:5]
	v_pk_fma_f32 v[172:173], v[200:201], v[212:213], v[180:181] op_sel_hi:[1,0,1]
	v_pk_fma_f32 v[180:181], v[202:203], v[212:213], v[184:185] op_sel_hi:[1,0,1]
	v_lshl_or_b32 v40, v40, 7, v136
	global_load_dwordx4 v[200:203], v40, s[4:5]
	v_pk_fma_f32 v[166:167], v[166:167], v[212:213], v[170:171] op_sel_hi:[1,0,1]
	v_lshl_or_b32 v39, v39, 7, v136
	global_load_dwordx4 v[212:215], v39, s[4:5]
	v_permlane32_swap_b32_e32 v174, v168
	v_permlane32_swap_b32_e32 v175, v169
	v_permlane32_swap_b32_e32 v182, v172
	v_permlane32_swap_b32_e32 v183, v173
	v_permlane32_swap_b32_e32 v186, v180
	v_permlane32_swap_b32_e32 v187, v181
	v_permlane32_swap_b32_e32 v164, v166
	v_permlane32_swap_b32_e32 v165, v167
	v_add_f32_e32 v168, v174, v168
	v_add_f32_e32 v169, v175, v169
	v_add_f32_e32 v170, v182, v172
	v_add_f32_e32 v171, v183, v173
	v_add_f32_e32 v172, v186, v180
	v_add_f32_e32 v173, v187, v181
	v_lshl_or_b32 v43, v43, 7, v136
	global_load_dwordx4 v[184:187], v43, s[4:5]
	v_lshl_or_b32 v44, v44, 7, v136
	global_load_dwordx4 v[180:183], v44, s[4:5]
	v_add_f32_e32 v164, v164, v166
	v_add_f32_e32 v165, v165, v167
	v_permlane16_swap_b32_e32 v168, v172
	v_permlane16_swap_b32_e32 v169, v173
	v_permlane16_swap_b32_e32 v170, v164
	v_permlane16_swap_b32_e32 v171, v165
	v_pk_add_f32 v[166:167], v[168:169], v[172:173]
	v_lshl_or_b32 v45, v45, 7, v136
	global_load_dwordx4 v[172:175], v45, s[4:5]
	v_pk_add_f32 v[164:165], v[170:171], v[164:165]
	s_ashr_i32 s7, s6, 31
	v_cndmask_b32_e64 v168, v166, v164, s[0:1]
	v_cndmask_b32_e64 v170, v164, v166, s[0:1]
	v_cndmask_b32_e64 v164, v167, v165, s[0:1]
	v_mov_b32_dpp v168, v168 row_ror:8 row_mask:0xf bank_mask:0xf bound_ctrl:1
	v_cndmask_b32_e64 v171, v165, v167, s[0:1]
	v_mov_b32_dpp v169, v164 row_ror:8 row_mask:0xf bank_mask:0xf bound_ctrl:1
	v_pk_add_f32 v[166:167], v[170:171], v[168:169]
	s_lshl_b64 s[8:9], s[6:7], 11
	v_pk_mul_f32 v[164:165], v[166:167], v[166:167]
	v_cvt_pk_bf16_f32 v168, v166, v167
	v_add_f32_e32 v164, v164, v165
	v_lshl_add_u64 v[166:167], v[130:131], 0, s[8:9]
	global_store_dword v[166:167], v168, off
	v_add_f32_dpp v164, v164, v164 quad_perm:[1,0,3,2] row_mask:0xf bank_mask:0xf bound_ctrl:1
	s_nop 1
	v_add_f32_dpp v164, v164, v164 quad_perm:[2,3,0,1] row_mask:0xf bank_mask:0xf bound_ctrl:1
	s_nop 1
	v_add_f32_dpp v164, v164, v164 row_half_mirror row_mask:0xf bank_mask:0xf bound_ctrl:1
	s_nop 1
	v_add_f32_dpp v164, v164, v164 row_ror:8 row_mask:0xf bank_mask:0xf bound_ctrl:1
	v_mov_b32_e32 v165, v164
	s_nop 1
	v_permlane16_swap_b32_e32 v164, v165
	v_add_f32_e32 v164, v164, v165
	v_mov_b32_e32 v165, v164
	s_nop 1
	v_permlane32_swap_b32_e32 v164, v165
	s_and_saveexec_b64 s[8:9], s[2:3]
	s_lshl_b64 s[10:11], s[6:7], 2
	s_add_u32 s10, s12, s10
	v_add_f32_e32 v164, v164, v165
	s_addc_u32 s11, s13, s11
	global_store_dword v129, v164, s[10:11]
	s_or_b64 exec, exec, s[8:9]
	v_lshl_or_b32 v46, v46, 7, v136
	global_load_dwordx4 v[168:171], v46, s[4:5]
	v_lshl_or_b32 v47, v47, 7, v136
	global_load_dwordx4 v[164:167], v47, s[4:5]
	s_add_u32 s22, s20, 0x300
	s_lshl_b32 s22, s22, 9
	v_lshl_add_u64 v[48:49], v[134:135], 0, s[22:23]
	global_load_dwordx4 v[60:63], v[48:49], off offset:48
	global_load_dwordx4 v[56:59], v[48:49], off offset:32
	global_load_dwordx4 v[52:55], v[48:49], off offset:16
	s_nop 0
	global_load_dwordx4 v[48:51], v[48:49], off
	s_add_u32 s20, s20, 0x200
	s_mov_b32 s8, s20
	s_waitcnt vmcnt(22)
	v_cvt_pk_f32_fp8_e32 v[138:139], v124
	v_cvt_pk_f32_fp8_sdwa v[140:141], v124 src0_sel:WORD_1
	v_cvt_pk_f32_fp8_e32 v[142:143], v125
	v_cvt_pk_f32_fp8_sdwa v[124:125], v125 src0_sel:WORD_1
	v_cvt_pk_f32_fp8_e32 v[144:145], v126
	v_cvt_pk_f32_fp8_sdwa v[146:147], v126 src0_sel:WORD_1
	v_cvt_pk_f32_fp8_e32 v[148:149], v127
	v_cvt_pk_f32_fp8_sdwa v[126:127], v127 src0_sel:WORD_1
	v_cvt_pk_f32_fp8_e32 v[150:151], v120
	v_cvt_pk_f32_fp8_sdwa v[152:153], v120 src0_sel:WORD_1
	v_cvt_pk_f32_fp8_e32 v[154:155], v121
	v_cvt_pk_f32_fp8_sdwa v[120:121], v121 src0_sel:WORD_1
	v_cvt_pk_f32_fp8_e32 v[156:157], v122
	v_cvt_pk_f32_fp8_sdwa v[158:159], v122 src0_sel:WORD_1
	v_cvt_pk_f32_fp8_e32 v[160:161], v123
	v_cvt_pk_f32_fp8_sdwa v[122:123], v123 src0_sel:WORD_1
	v_pk_fma_f32 v[138:139], v[138:139], v[28:29], 0 op_sel_hi:[1,0,0]
	v_pk_fma_f32 v[140:141], v[140:141], v[28:29], 0 op_sel_hi:[1,0,0]
	v_pk_fma_f32 v[142:143], v[142:143], v[28:29], 0 op_sel_hi:[1,0,0]
	v_pk_fma_f32 v[124:125], v[124:125], v[28:29], 0 op_sel_hi:[1,0,0]
	v_pk_fma_f32 v[144:145], v[144:145], v[28:29], 0 op_sel_hi:[1,0,0]
	v_pk_fma_f32 v[146:147], v[146:147], v[28:29], 0 op_sel_hi:[1,0,0]
	v_pk_fma_f32 v[148:149], v[148:149], v[28:29], 0 op_sel_hi:[1,0,0]
	v_pk_fma_f32 v[126:127], v[126:127], v[28:29], 0 op_sel_hi:[1,0,0]
	v_pk_fma_f32 v[138:139], v[150:151], v[28:29], v[138:139] op_sel:[0,1,0]
	v_pk_fma_f32 v[140:141], v[152:153], v[28:29], v[140:141] op_sel:[0,1,0]
	v_pk_fma_f32 v[142:143], v[154:155], v[28:29], v[142:143] op_sel:[0,1,0]
	v_pk_fma_f32 v[120:121], v[120:121], v[28:29], v[124:125] op_sel:[0,1,0]
	v_pk_fma_f32 v[124:125], v[156:157], v[28:29], v[144:145] op_sel:[0,1,0]
	v_pk_fma_f32 v[144:145], v[158:159], v[28:29], v[146:147] op_sel:[0,1,0]
	v_pk_fma_f32 v[146:147], v[160:161], v[28:29], v[148:149] op_sel:[0,1,0]
	v_pk_fma_f32 v[122:123], v[122:123], v[28:29], v[126:127] op_sel:[0,1,0]
	v_cvt_pk_f32_fp8_e32 v[126:127], v116
	v_cvt_pk_f32_fp8_sdwa v[148:149], v116 src0_sel:WORD_1
	v_cvt_pk_f32_fp8_e32 v[150:151], v117
	v_cvt_pk_f32_fp8_sdwa v[116:117], v117 src0_sel:WORD_1
	v_cvt_pk_f32_fp8_e32 v[152:153], v118
	v_cvt_pk_f32_fp8_sdwa v[154:155], v118 src0_sel:WORD_1
	v_cvt_pk_f32_fp8_e32 v[156:157], v119
	v_cvt_pk_f32_fp8_sdwa v[118:119], v119 src0_sel:WORD_1
	v_pk_fma_f32 v[126:127], v[126:127], v[30:31], v[138:139] op_sel_hi:[1,0,1]
	v_pk_fma_f32 v[138:139], v[148:149], v[30:31], v[140:141] op_sel_hi:[1,0,1]
	v_pk_fma_f32 v[140:141], v[150:151], v[30:31], v[142:143] op_sel_hi:[1,0,1]
	v_pk_fma_f32 v[116:117], v[116:117], v[30:31], v[120:121] op_sel_hi:[1,0,1]
	v_pk_fma_f32 v[120:121], v[152:153], v[30:31], v[124:125] op_sel_hi:[1,0,1]
	v_pk_fma_f32 v[124:125], v[154:155], v[30:31], v[144:145] op_sel_hi:[1,0,1]
	v_pk_fma_f32 v[142:143], v[156:157], v[30:31], v[146:147] op_sel_hi:[1,0,1]
	v_pk_fma_f32 v[118:119], v[118:119], v[30:31], v[122:123] op_sel_hi:[1,0,1]
	v_cvt_pk_f32_fp8_e32 v[122:123], v112
	v_cvt_pk_f32_fp8_sdwa v[144:145], v112 src0_sel:WORD_1
	v_cvt_pk_f32_fp8_e32 v[146:147], v113
	v_cvt_pk_f32_fp8_sdwa v[112:113], v113 src0_sel:WORD_1
	v_cvt_pk_f32_fp8_e32 v[148:149], v114
	v_cvt_pk_f32_fp8_sdwa v[150:151], v114 src0_sel:WORD_1
	v_cvt_pk_f32_fp8_e32 v[152:153], v115
	v_cvt_pk_f32_fp8_sdwa v[114:115], v115 src0_sel:WORD_1
	v_mov_b32_e32 v128, v31
	v_pk_fma_f32 v[122:123], v[122:123], v[128:129], v[126:127] op_sel_hi:[1,0,1]
	v_pk_fma_f32 v[126:127], v[144:145], v[128:129], v[138:139] op_sel_hi:[1,0,1]
	v_pk_fma_f32 v[138:139], v[146:147], v[128:129], v[140:141] op_sel_hi:[1,0,1]
	v_pk_fma_f32 v[112:113], v[112:113], v[128:129], v[116:117] op_sel_hi:[1,0,1]
	v_pk_fma_f32 v[116:117], v[148:149], v[128:129], v[120:121] op_sel_hi:[1,0,1]
	v_pk_fma_f32 v[120:121], v[150:151], v[128:129], v[124:125] op_sel_hi:[1,0,1]
	v_pk_fma_f32 v[124:125], v[152:153], v[128:129], v[142:143] op_sel_hi:[1,0,1]
	v_pk_fma_f32 v[114:115], v[114:115], v[128:129], v[118:119] op_sel_hi:[1,0,1]
	v_cvt_pk_f32_fp8_e32 v[118:119], v108
	v_cvt_pk_f32_fp8_sdwa v[140:141], v108 src0_sel:WORD_1
	v_cvt_pk_f32_fp8_e32 v[142:143], v109
	v_cvt_pk_f32_fp8_sdwa v[108:109], v109 src0_sel:WORD_1
	v_cvt_pk_f32_fp8_e32 v[144:145], v110
	v_cvt_pk_f32_fp8_sdwa v[146:147], v110 src0_sel:WORD_1
	v_cvt_pk_f32_fp8_e32 v[148:149], v111
	v_cvt_pk_f32_fp8_sdwa v[110:111], v111 src0_sel:WORD_1
	v_pk_fma_f32 v[118:119], v[118:119], v[24:25], v[122:123] op_sel_hi:[1,0,1]
	v_pk_fma_f32 v[122:123], v[140:141], v[24:25], v[126:127] op_sel_hi:[1,0,1]
	v_pk_fma_f32 v[126:127], v[142:143], v[24:25], v[138:139] op_sel_hi:[1,0,1]
	v_pk_fma_f32 v[108:109], v[108:109], v[24:25], v[112:113] op_sel_hi:[1,0,1]
	v_pk_fma_f32 v[112:113], v[144:145], v[24:25], v[116:117] op_sel_hi:[1,0,1]
	v_pk_fma_f32 v[116:117], v[146:147], v[24:25], v[120:121] op_sel_hi:[1,0,1]
	v_pk_fma_f32 v[120:121], v[148:149], v[24:25], v[124:125] op_sel_hi:[1,0,1]
	v_pk_fma_f32 v[110:111], v[110:111], v[24:25], v[114:115] op_sel_hi:[1,0,1]
	v_cvt_pk_f32_fp8_e32 v[114:115], v104
	v_cvt_pk_f32_fp8_sdwa v[124:125], v104 src0_sel:WORD_1
	v_cvt_pk_f32_fp8_e32 v[138:139], v105
	v_cvt_pk_f32_fp8_sdwa v[104:105], v105 src0_sel:WORD_1
	v_cvt_pk_f32_fp8_e32 v[140:141], v106
	v_cvt_pk_f32_fp8_sdwa v[142:143], v106 src0_sel:WORD_1
	v_cvt_pk_f32_fp8_e32 v[144:145], v107
	v_cvt_pk_f32_fp8_sdwa v[106:107], v107 src0_sel:WORD_1
	v_pk_fma_f32 v[114:115], v[114:115], v[24:25], v[118:119] op_sel:[0,1,0]
	v_pk_fma_f32 v[118:119], v[124:125], v[24:25], v[122:123] op_sel:[0,1,0]
	v_pk_fma_f32 v[122:123], v[138:139], v[24:25], v[126:127] op_sel:[0,1,0]
	v_pk_fma_f32 v[104:105], v[104:105], v[24:25], v[108:109] op_sel:[0,1,0]
	v_pk_fma_f32 v[108:109], v[140:141], v[24:25], v[112:113] op_sel:[0,1,0]
	v_pk_fma_f32 v[112:113], v[142:143], v[24:25], v[116:117] op_sel:[0,1,0]
	v_pk_fma_f32 v[116:117], v[144:145], v[24:25], v[120:121] op_sel:[0,1,0]
	v_pk_fma_f32 v[106:107], v[106:107], v[24:25], v[110:111] op_sel:[0,1,0]
	v_cvt_pk_f32_fp8_e32 v[110:111], v100
	v_cvt_pk_f32_fp8_sdwa v[120:121], v100 src0_sel:WORD_1
	v_cvt_pk_f32_fp8_e32 v[124:125], v101
	v_cvt_pk_f32_fp8_sdwa v[100:101], v101 src0_sel:WORD_1
	v_cvt_pk_f32_fp8_e32 v[126:127], v102
	v_cvt_pk_f32_fp8_sdwa v[138:139], v102 src0_sel:WORD_1
	v_cvt_pk_f32_fp8_e32 v[140:141], v103
	v_cvt_pk_f32_fp8_sdwa v[102:103], v103 src0_sel:WORD_1
	v_pk_fma_f32 v[110:111], v[110:111], v[26:27], v[114:115] op_sel_hi:[1,0,1]
	v_pk_fma_f32 v[114:115], v[120:121], v[26:27], v[118:119] op_sel_hi:[1,0,1]
	v_pk_fma_f32 v[118:119], v[124:125], v[26:27], v[122:123] op_sel_hi:[1,0,1]
	v_pk_fma_f32 v[100:101], v[100:101], v[26:27], v[104:105] op_sel_hi:[1,0,1]
	v_pk_fma_f32 v[104:105], v[126:127], v[26:27], v[108:109] op_sel_hi:[1,0,1]
	v_pk_fma_f32 v[108:109], v[138:139], v[26:27], v[112:113] op_sel_hi:[1,0,1]
	v_pk_fma_f32 v[112:113], v[140:141], v[26:27], v[116:117] op_sel_hi:[1,0,1]
	v_pk_fma_f32 v[102:103], v[102:103], v[26:27], v[106:107] op_sel_hi:[1,0,1]
	v_cvt_pk_f32_fp8_e32 v[106:107], v96
	v_cvt_pk_f32_fp8_sdwa v[116:117], v96 src0_sel:WORD_1
	v_cvt_pk_f32_fp8_e32 v[120:121], v97
	v_cvt_pk_f32_fp8_sdwa v[96:97], v97 src0_sel:WORD_1
	v_cvt_pk_f32_fp8_e32 v[122:123], v98
	v_cvt_pk_f32_fp8_sdwa v[124:125], v98 src0_sel:WORD_1
	v_cvt_pk_f32_fp8_e32 v[126:127], v99
	v_cvt_pk_f32_fp8_sdwa v[98:99], v99 src0_sel:WORD_1
	v_mov_b32_e32 v128, v27
	v_pk_fma_f32 v[106:107], v[106:107], v[128:129], v[110:111] op_sel_hi:[1,0,1]
	v_pk_fma_f32 v[110:111], v[116:117], v[128:129], v[114:115] op_sel_hi:[1,0,1]
	v_pk_fma_f32 v[114:115], v[120:121], v[128:129], v[118:119] op_sel_hi:[1,0,1]
	v_pk_fma_f32 v[96:97], v[96:97], v[128:129], v[100:101] op_sel_hi:[1,0,1]
	v_pk_fma_f32 v[100:101], v[122:123], v[128:129], v[104:105] op_sel_hi:[1,0,1]
	v_pk_fma_f32 v[104:105], v[124:125], v[128:129], v[108:109] op_sel_hi:[1,0,1]
	v_pk_fma_f32 v[108:109], v[126:127], v[128:129], v[112:113] op_sel_hi:[1,0,1]
	v_pk_fma_f32 v[98:99], v[98:99], v[128:129], v[102:103] op_sel_hi:[1,0,1]
	v_cvt_pk_f32_fp8_e32 v[102:103], v92
	v_cvt_pk_f32_fp8_sdwa v[112:113], v92 src0_sel:WORD_1
	v_cvt_pk_f32_fp8_e32 v[116:117], v93
	v_cvt_pk_f32_fp8_sdwa v[92:93], v93 src0_sel:WORD_1
	v_cvt_pk_f32_fp8_e32 v[118:119], v94
	v_cvt_pk_f32_fp8_sdwa v[120:121], v94 src0_sel:WORD_1
	v_cvt_pk_f32_fp8_e32 v[122:123], v95
	v_cvt_pk_f32_fp8_sdwa v[94:95], v95 src0_sel:WORD_1
	v_pk_fma_f32 v[102:103], v[102:103], v[20:21], v[106:107] op_sel_hi:[1,0,1]
	v_pk_fma_f32 v[106:107], v[112:113], v[20:21], v[110:111] op_sel_hi:[1,0,1]
	v_pk_fma_f32 v[110:111], v[116:117], v[20:21], v[114:115] op_sel_hi:[1,0,1]
	v_pk_fma_f32 v[92:93], v[92:93], v[20:21], v[96:97] op_sel_hi:[1,0,1]
	v_pk_fma_f32 v[96:97], v[118:119], v[20:21], v[100:101] op_sel_hi:[1,0,1]
	v_pk_fma_f32 v[100:101], v[120:121], v[20:21], v[104:105] op_sel_hi:[1,0,1]
	v_pk_fma_f32 v[104:105], v[122:123], v[20:21], v[108:109] op_sel_hi:[1,0,1]
	v_pk_fma_f32 v[94:95], v[94:95], v[20:21], v[98:99] op_sel_hi:[1,0,1]
	v_cvt_pk_f32_fp8_e32 v[98:99], v88
	v_cvt_pk_f32_fp8_sdwa v[108:109], v88 src0_sel:WORD_1
	v_cvt_pk_f32_fp8_e32 v[112:113], v89
	v_cvt_pk_f32_fp8_sdwa v[88:89], v89 src0_sel:WORD_1
	v_cvt_pk_f32_fp8_e32 v[114:115], v90
	v_cvt_pk_f32_fp8_sdwa v[116:117], v90 src0_sel:WORD_1
	v_cvt_pk_f32_fp8_e32 v[118:119], v91
	v_cvt_pk_f32_fp8_sdwa v[90:91], v91 src0_sel:WORD_1
	v_pk_fma_f32 v[98:99], v[98:99], v[20:21], v[102:103] op_sel:[0,1,0]
	v_pk_fma_f32 v[102:103], v[108:109], v[20:21], v[106:107] op_sel:[0,1,0]
	v_pk_fma_f32 v[106:107], v[112:113], v[20:21], v[110:111] op_sel:[0,1,0]
	v_pk_fma_f32 v[88:89], v[88:89], v[20:21], v[92:93] op_sel:[0,1,0]
	v_pk_fma_f32 v[92:93], v[114:115], v[20:21], v[96:97] op_sel:[0,1,0]
	v_pk_fma_f32 v[96:97], v[116:117], v[20:21], v[100:101] op_sel:[0,1,0]
	v_pk_fma_f32 v[100:101], v[118:119], v[20:21], v[104:105] op_sel:[0,1,0]
	v_pk_fma_f32 v[90:91], v[90:91], v[20:21], v[94:95] op_sel:[0,1,0]
	v_cvt_pk_f32_fp8_e32 v[94:95], v84
	v_cvt_pk_f32_fp8_sdwa v[104:105], v84 src0_sel:WORD_1
	v_cvt_pk_f32_fp8_e32 v[108:109], v85
	v_cvt_pk_f32_fp8_sdwa v[84:85], v85 src0_sel:WORD_1
	v_cvt_pk_f32_fp8_e32 v[110:111], v86
	v_cvt_pk_f32_fp8_sdwa v[112:113], v86 src0_sel:WORD_1
	v_cvt_pk_f32_fp8_e32 v[114:115], v87
	v_cvt_pk_f32_fp8_sdwa v[86:87], v87 src0_sel:WORD_1
	v_pk_fma_f32 v[94:95], v[94:95], v[22:23], v[98:99] op_sel_hi:[1,0,1]
	v_pk_fma_f32 v[98:99], v[104:105], v[22:23], v[102:103] op_sel_hi:[1,0,1]
	v_pk_fma_f32 v[102:103], v[108:109], v[22:23], v[106:107] op_sel_hi:[1,0,1]
	v_pk_fma_f32 v[84:85], v[84:85], v[22:23], v[88:89] op_sel_hi:[1,0,1]
	v_pk_fma_f32 v[88:89], v[110:111], v[22:23], v[92:93] op_sel_hi:[1,0,1]
	v_pk_fma_f32 v[92:93], v[112:113], v[22:23], v[96:97] op_sel_hi:[1,0,1]
	v_pk_fma_f32 v[96:97], v[114:115], v[22:23], v[100:101] op_sel_hi:[1,0,1]
	v_pk_fma_f32 v[86:87], v[86:87], v[22:23], v[90:91] op_sel_hi:[1,0,1]
	v_cvt_pk_f32_fp8_e32 v[90:91], v80
	v_cvt_pk_f32_fp8_sdwa v[100:101], v80 src0_sel:WORD_1
	v_cvt_pk_f32_fp8_e32 v[104:105], v81
	v_cvt_pk_f32_fp8_sdwa v[80:81], v81 src0_sel:WORD_1
	v_cvt_pk_f32_fp8_e32 v[106:107], v82
	v_cvt_pk_f32_fp8_sdwa v[108:109], v82 src0_sel:WORD_1
	v_cvt_pk_f32_fp8_e32 v[110:111], v83
	v_cvt_pk_f32_fp8_sdwa v[82:83], v83 src0_sel:WORD_1
	v_mov_b32_e32 v112, v23
	v_pk_fma_f32 v[90:91], v[90:91], v[112:113], v[94:95] op_sel_hi:[1,0,1]
	v_pk_fma_f32 v[94:95], v[100:101], v[112:113], v[98:99] op_sel_hi:[1,0,1]
; DI void phase_peerup(const Params& p, int bid, int nb) {
;     ...
;     PU_MATH(t1, w, cB);
;     if (t2 >= T_) break;
;     t = t2;
	v_pk_fma_f32 v[98:99], v[104:105], v[112:113], v[102:103] op_sel_hi:[1,0,1]
	v_pk_fma_f32 v[80:81], v[80:81], v[112:113], v[84:85] op_sel_hi:[1,0,1]
	v_pk_fma_f32 v[84:85], v[106:107], v[112:113], v[88:89] op_sel_hi:[1,0,1]
	v_pk_fma_f32 v[88:89], v[108:109], v[112:113], v[92:93] op_sel_hi:[1,0,1]
	v_pk_fma_f32 v[92:93], v[110:111], v[112:113], v[96:97] op_sel_hi:[1,0,1]
	v_pk_fma_f32 v[82:83], v[82:83], v[112:113], v[86:87] op_sel_hi:[1,0,1]
	v_cvt_pk_f32_fp8_e32 v[86:87], v76
	v_cvt_pk_f32_fp8_sdwa v[96:97], v76 src0_sel:WORD_1
	v_cvt_pk_f32_fp8_e32 v[100:101], v77
	v_cvt_pk_f32_fp8_sdwa v[76:77], v77 src0_sel:WORD_1
	v_cvt_pk_f32_fp8_e32 v[102:103], v78
	v_cvt_pk_f32_fp8_sdwa v[104:105], v78 src0_sel:WORD_1
	v_cvt_pk_f32_fp8_e32 v[106:107], v79
	v_cvt_pk_f32_fp8_sdwa v[78:79], v79 src0_sel:WORD_1
	v_pk_fma_f32 v[86:87], v[86:87], v[16:17], v[90:91] op_sel_hi:[1,0,1]
	v_pk_fma_f32 v[90:91], v[96:97], v[16:17], v[94:95] op_sel_hi:[1,0,1]
	v_pk_fma_f32 v[94:95], v[100:101], v[16:17], v[98:99] op_sel_hi:[1,0,1]
	v_pk_fma_f32 v[76:77], v[76:77], v[16:17], v[80:81] op_sel_hi:[1,0,1]
	v_pk_fma_f32 v[80:81], v[102:103], v[16:17], v[84:85] op_sel_hi:[1,0,1]
	v_pk_fma_f32 v[84:85], v[104:105], v[16:17], v[88:89] op_sel_hi:[1,0,1]
	v_pk_fma_f32 v[88:89], v[106:107], v[16:17], v[92:93] op_sel_hi:[1,0,1]
	v_pk_fma_f32 v[78:79], v[78:79], v[16:17], v[82:83] op_sel_hi:[1,0,1]
	v_cvt_pk_f32_fp8_e32 v[82:83], v72
	v_cvt_pk_f32_fp8_sdwa v[92:93], v72 src0_sel:WORD_1
	v_cvt_pk_f32_fp8_e32 v[96:97], v73
	v_cvt_pk_f32_fp8_sdwa v[72:73], v73 src0_sel:WORD_1
	v_cvt_pk_f32_fp8_e32 v[98:99], v74
	v_cvt_pk_f32_fp8_sdwa v[100:101], v74 src0_sel:WORD_1
	v_cvt_pk_f32_fp8_e32 v[102:103], v75
	v_cvt_pk_f32_fp8_sdwa v[74:75], v75 src0_sel:WORD_1
	v_pk_fma_f32 v[82:83], v[82:83], v[16:17], v[86:87] op_sel:[0,1,0]
	v_pk_fma_f32 v[86:87], v[92:93], v[16:17], v[90:91] op_sel:[0,1,0]
	v_pk_fma_f32 v[90:91], v[96:97], v[16:17], v[94:95] op_sel:[0,1,0]
	v_pk_fma_f32 v[72:73], v[72:73], v[16:17], v[76:77] op_sel:[0,1,0]
	v_pk_fma_f32 v[76:77], v[98:99], v[16:17], v[80:81] op_sel:[0,1,0]
	v_pk_fma_f32 v[80:81], v[100:101], v[16:17], v[84:85] op_sel:[0,1,0]
	v_pk_fma_f32 v[84:85], v[102:103], v[16:17], v[88:89] op_sel:[0,1,0]
	v_pk_fma_f32 v[74:75], v[74:75], v[16:17], v[78:79] op_sel:[0,1,0]
	v_cvt_pk_f32_fp8_e32 v[78:79], v68
	v_cvt_pk_f32_fp8_sdwa v[88:89], v68 src0_sel:WORD_1
	v_cvt_pk_f32_fp8_e32 v[92:93], v69
	v_cvt_pk_f32_fp8_sdwa v[68:69], v69 src0_sel:WORD_1
	v_cvt_pk_f32_fp8_e32 v[94:95], v70
	v_cvt_pk_f32_fp8_sdwa v[96:97], v70 src0_sel:WORD_1
	v_cvt_pk_f32_fp8_e32 v[98:99], v71
	v_cvt_pk_f32_fp8_sdwa v[70:71], v71 src0_sel:WORD_1
	v_pk_fma_f32 v[78:79], v[78:79], v[18:19], v[82:83] op_sel_hi:[1,0,1]
	v_pk_fma_f32 v[82:83], v[88:89], v[18:19], v[86:87] op_sel_hi:[1,0,1]
	v_pk_fma_f32 v[86:87], v[92:93], v[18:19], v[90:91] op_sel_hi:[1,0,1]
	v_pk_fma_f32 v[68:69], v[68:69], v[18:19], v[72:73] op_sel_hi:[1,0,1]
	v_pk_fma_f32 v[72:73], v[94:95], v[18:19], v[76:77] op_sel_hi:[1,0,1]
	v_pk_fma_f32 v[76:77], v[96:97], v[18:19], v[80:81] op_sel_hi:[1,0,1]
	v_pk_fma_f32 v[80:81], v[98:99], v[18:19], v[84:85] op_sel_hi:[1,0,1]
	v_pk_fma_f32 v[70:71], v[70:71], v[18:19], v[74:75] op_sel_hi:[1,0,1]
	v_cvt_pk_f32_fp8_e32 v[74:75], v64
	v_cvt_pk_f32_fp8_sdwa v[84:85], v64 src0_sel:WORD_1
	v_cvt_pk_f32_fp8_e32 v[88:89], v65
	v_cvt_pk_f32_fp8_sdwa v[64:65], v65 src0_sel:WORD_1
	v_cvt_pk_f32_fp8_e32 v[90:91], v66
	v_cvt_pk_f32_fp8_sdwa v[92:93], v66 src0_sel:WORD_1
	v_cvt_pk_f32_fp8_e32 v[94:95], v67
	v_cvt_pk_f32_fp8_sdwa v[66:67], v67 src0_sel:WORD_1
	v_mov_b32_e32 v96, v19
	v_pk_fma_f32 v[74:75], v[74:75], v[96:97], v[78:79] op_sel_hi:[1,0,1]
	v_pk_fma_f32 v[78:79], v[84:85], v[96:97], v[82:83] op_sel_hi:[1,0,1]
	v_pk_fma_f32 v[82:83], v[88:89], v[96:97], v[86:87] op_sel_hi:[1,0,1]
	v_pk_fma_f32 v[64:65], v[64:65], v[96:97], v[68:69] op_sel_hi:[1,0,1]
	v_pk_fma_f32 v[68:69], v[90:91], v[96:97], v[72:73] op_sel_hi:[1,0,1]
	v_pk_fma_f32 v[72:73], v[92:93], v[96:97], v[76:77] op_sel_hi:[1,0,1]
	v_pk_fma_f32 v[76:77], v[94:95], v[96:97], v[80:81] op_sel_hi:[1,0,1]
	v_pk_fma_f32 v[66:67], v[66:67], v[96:97], v[70:71] op_sel_hi:[1,0,1]
	v_permlane32_swap_b32_e32 v74, v68
	v_permlane32_swap_b32_e32 v75, v69
	v_permlane32_swap_b32_e32 v78, v72
	v_permlane32_swap_b32_e32 v79, v73
	v_permlane32_swap_b32_e32 v82, v76
	v_permlane32_swap_b32_e32 v83, v77
	v_permlane32_swap_b32_e32 v64, v66
	v_permlane32_swap_b32_e32 v65, v67
	v_add_f32_e32 v68, v74, v68
	v_add_f32_e32 v69, v75, v69
	v_add_f32_e32 v70, v78, v72
	v_add_f32_e32 v71, v79, v73
	v_add_f32_e32 v72, v82, v76
	v_add_f32_e32 v73, v83, v77
	v_add_f32_e32 v64, v64, v66
	v_add_f32_e32 v65, v65, v67
	v_permlane16_swap_b32_e32 v68, v72
	v_permlane16_swap_b32_e32 v69, v73
	v_permlane16_swap_b32_e32 v70, v64
	v_permlane16_swap_b32_e32 v71, v65
	v_pk_add_f32 v[66:67], v[68:69], v[72:73]
	v_pk_add_f32 v[64:65], v[70:71], v[64:65]
	s_ashr_i32 s9, s8, 31
	v_cndmask_b32_e64 v68, v66, v64, s[0:1]
	v_cndmask_b32_e64 v70, v64, v66, s[0:1]
	v_cndmask_b32_e64 v64, v67, v65, s[0:1]
	v_mov_b32_dpp v68, v68 row_ror:8 row_mask:0xf bank_mask:0xf bound_ctrl:1
	v_cndmask_b32_e64 v71, v65, v67, s[0:1]
	v_mov_b32_dpp v69, v64 row_ror:8 row_mask:0xf bank_mask:0xf bound_ctrl:1
	v_pk_add_f32 v[66:67], v[70:71], v[68:69]
	s_lshl_b64 s[10:11], s[8:9], 11
	v_pk_mul_f32 v[64:65], v[66:67], v[66:67]
	v_cvt_pk_bf16_f32 v68, v66, v67
	v_add_f32_e32 v64, v64, v65
	v_lshl_add_u64 v[66:67], v[130:131], 0, s[10:11]
	global_store_dword v[66:67], v68, off
	v_add_f32_dpp v64, v64, v64 quad_perm:[1,0,3,2] row_mask:0xf bank_mask:0xf bound_ctrl:1
	s_nop 1
	v_add_f32_dpp v64, v64, v64 quad_perm:[2,3,0,1] row_mask:0xf bank_mask:0xf bound_ctrl:1
	s_nop 1
	v_add_f32_dpp v64, v64, v64 row_half_mirror row_mask:0xf bank_mask:0xf bound_ctrl:1
	s_nop 1
	v_add_f32_dpp v64, v64, v64 row_ror:8 row_mask:0xf bank_mask:0xf bound_ctrl:1
	v_mov_b32_e32 v65, v64
	s_nop 1
	v_permlane16_swap_b32_e32 v64, v65
	v_add_f32_e32 v64, v64, v65
	v_mov_b32_e32 v65, v64
	s_nop 1
	v_permlane32_swap_b32_e32 v64, v65
	s_and_saveexec_b64 s[10:11], s[2:3]
	s_lshl_b64 s[16:17], s[8:9], 2
	s_add_u32 s16, s12, s16
	v_add_f32_e32 v64, v64, v65
	s_addc_u32 s17, s13, s17
	global_store_dword v129, v64, s[16:17]
	s_or_b64 exec, exec, s[10:11]
	s_add_u32 s6, s20, 0x100
	s_waitcnt vmcnt(2)
	v_cvt_pk_f32_fp8_e32 v[138:139], v240
	v_cvt_pk_f32_fp8_sdwa v[140:141], v240 src0_sel:WORD_1
	v_cvt_pk_f32_fp8_e32 v[142:143], v241
	v_cvt_pk_f32_fp8_sdwa v[240:241], v241 src0_sel:WORD_1
	v_cvt_pk_f32_fp8_e32 v[144:145], v242
	v_cvt_pk_f32_fp8_sdwa v[146:147], v242 src0_sel:WORD_1
	v_cvt_pk_f32_fp8_e32 v[148:149], v243
	v_cvt_pk_f32_fp8_sdwa v[242:243], v243 src0_sel:WORD_1
	v_cvt_pk_f32_fp8_e32 v[150:151], v236
	v_cvt_pk_f32_fp8_sdwa v[152:153], v236 src0_sel:WORD_1
	v_cvt_pk_f32_fp8_e32 v[154:155], v237
	v_cvt_pk_f32_fp8_sdwa v[236:237], v237 src0_sel:WORD_1
	v_cvt_pk_f32_fp8_e32 v[156:157], v238
	v_cvt_pk_f32_fp8_sdwa v[158:159], v238 src0_sel:WORD_1
	v_cvt_pk_f32_fp8_e32 v[160:161], v239
	v_cvt_pk_f32_fp8_sdwa v[238:239], v239 src0_sel:WORD_1
	v_pk_fma_f32 v[138:139], v[138:139], v[48:49], 0 op_sel_hi:[1,0,0]
	v_pk_fma_f32 v[140:141], v[140:141], v[48:49], 0 op_sel_hi:[1,0,0]
	v_pk_fma_f32 v[142:143], v[142:143], v[48:49], 0 op_sel_hi:[1,0,0]
	v_pk_fma_f32 v[240:241], v[240:241], v[48:49], 0 op_sel_hi:[1,0,0]
	v_pk_fma_f32 v[144:145], v[144:145], v[48:49], 0 op_sel_hi:[1,0,0]
	v_pk_fma_f32 v[146:147], v[146:147], v[48:49], 0 op_sel_hi:[1,0,0]
	v_pk_fma_f32 v[148:149], v[148:149], v[48:49], 0 op_sel_hi:[1,0,0]
	v_pk_fma_f32 v[242:243], v[242:243], v[48:49], 0 op_sel_hi:[1,0,0]
	v_pk_fma_f32 v[138:139], v[150:151], v[48:49], v[138:139] op_sel:[0,1,0]
	v_pk_fma_f32 v[140:141], v[152:153], v[48:49], v[140:141] op_sel:[0,1,0]
	v_pk_fma_f32 v[142:143], v[154:155], v[48:49], v[142:143] op_sel:[0,1,0]
	v_pk_fma_f32 v[236:237], v[236:237], v[48:49], v[240:241] op_sel:[0,1,0]
	v_pk_fma_f32 v[240:241], v[156:157], v[48:49], v[144:145] op_sel:[0,1,0]
	v_pk_fma_f32 v[144:145], v[158:159], v[48:49], v[146:147] op_sel:[0,1,0]
	v_pk_fma_f32 v[146:147], v[160:161], v[48:49], v[148:149] op_sel:[0,1,0]
	v_pk_fma_f32 v[238:239], v[238:239], v[48:49], v[242:243] op_sel:[0,1,0]
	v_cvt_pk_f32_fp8_e32 v[242:243], v232
	v_cvt_pk_f32_fp8_sdwa v[148:149], v232 src0_sel:WORD_1
	v_cvt_pk_f32_fp8_e32 v[150:151], v233
	v_cvt_pk_f32_fp8_sdwa v[232:233], v233 src0_sel:WORD_1
	v_cvt_pk_f32_fp8_e32 v[152:153], v234
	v_cvt_pk_f32_fp8_sdwa v[154:155], v234 src0_sel:WORD_1
	v_cvt_pk_f32_fp8_e32 v[156:157], v235
	v_cvt_pk_f32_fp8_sdwa v[234:235], v235 src0_sel:WORD_1
	v_pk_fma_f32 v[242:243], v[242:243], v[50:51], v[138:139] op_sel_hi:[1,0,1]
	v_pk_fma_f32 v[138:139], v[148:149], v[50:51], v[140:141] op_sel_hi:[1,0,1]
	v_pk_fma_f32 v[140:141], v[150:151], v[50:51], v[142:143] op_sel_hi:[1,0,1]
	v_pk_fma_f32 v[232:233], v[232:233], v[50:51], v[236:237] op_sel_hi:[1,0,1]
	v_pk_fma_f32 v[236:237], v[152:153], v[50:51], v[240:241] op_sel_hi:[1,0,1]
	v_pk_fma_f32 v[240:241], v[154:155], v[50:51], v[144:145] op_sel_hi:[1,0,1]
	v_pk_fma_f32 v[142:143], v[156:157], v[50:51], v[146:147] op_sel_hi:[1,0,1]
	v_pk_fma_f32 v[234:235], v[234:235], v[50:51], v[238:239] op_sel_hi:[1,0,1]
	v_cvt_pk_f32_fp8_e32 v[238:239], v228
	v_cvt_pk_f32_fp8_sdwa v[144:145], v228 src0_sel:WORD_1
	v_cvt_pk_f32_fp8_e32 v[146:147], v229
	v_cvt_pk_f32_fp8_sdwa v[228:229], v229 src0_sel:WORD_1
	v_cvt_pk_f32_fp8_e32 v[148:149], v230
	v_cvt_pk_f32_fp8_sdwa v[150:151], v230 src0_sel:WORD_1
	v_cvt_pk_f32_fp8_e32 v[152:153], v231
	v_cvt_pk_f32_fp8_sdwa v[230:231], v231 src0_sel:WORD_1
	v_mov_b32_e32 v128, v51
	v_pk_fma_f32 v[238:239], v[238:239], v[128:129], v[242:243] op_sel_hi:[1,0,1]
	v_pk_fma_f32 v[242:243], v[144:145], v[128:129], v[138:139] op_sel_hi:[1,0,1]
	v_pk_fma_f32 v[138:139], v[146:147], v[128:129], v[140:141] op_sel_hi:[1,0,1]
	v_pk_fma_f32 v[228:229], v[228:229], v[128:129], v[232:233] op_sel_hi:[1,0,1]
	v_pk_fma_f32 v[232:233], v[148:149], v[128:129], v[236:237] op_sel_hi:[1,0,1]
	v_pk_fma_f32 v[236:237], v[150:151], v[128:129], v[240:241] op_sel_hi:[1,0,1]
	v_pk_fma_f32 v[240:241], v[152:153], v[128:129], v[142:143] op_sel_hi:[1,0,1]
	v_pk_fma_f32 v[230:231], v[230:231], v[128:129], v[234:235] op_sel_hi:[1,0,1]
	v_cvt_pk_f32_fp8_e32 v[234:235], v224
	v_cvt_pk_f32_fp8_sdwa v[140:141], v224 src0_sel:WORD_1
	v_cvt_pk_f32_fp8_e32 v[142:143], v225
	v_cvt_pk_f32_fp8_sdwa v[224:225], v225 src0_sel:WORD_1
	v_cvt_pk_f32_fp8_e32 v[144:145], v226
	v_cvt_pk_f32_fp8_sdwa v[146:147], v226 src0_sel:WORD_1
	v_cvt_pk_f32_fp8_e32 v[148:149], v227
	v_cvt_pk_f32_fp8_sdwa v[226:227], v227 src0_sel:WORD_1
	v_pk_fma_f32 v[234:235], v[234:235], v[52:53], v[238:239] op_sel_hi:[1,0,1]
	v_pk_fma_f32 v[238:239], v[140:141], v[52:53], v[242:243] op_sel_hi:[1,0,1]
	v_pk_fma_f32 v[242:243], v[142:143], v[52:53], v[138:139] op_sel_hi:[1,0,1]
	v_pk_fma_f32 v[224:225], v[224:225], v[52:53], v[228:229] op_sel_hi:[1,0,1]
	v_pk_fma_f32 v[228:229], v[144:145], v[52:53], v[232:233] op_sel_hi:[1,0,1]
	v_pk_fma_f32 v[232:233], v[146:147], v[52:53], v[236:237] op_sel_hi:[1,0,1]
	v_pk_fma_f32 v[236:237], v[148:149], v[52:53], v[240:241] op_sel_hi:[1,0,1]
	v_pk_fma_f32 v[226:227], v[226:227], v[52:53], v[230:231] op_sel_hi:[1,0,1]
	v_cvt_pk_f32_fp8_e32 v[230:231], v220
	v_cvt_pk_f32_fp8_sdwa v[240:241], v220 src0_sel:WORD_1
	v_cvt_pk_f32_fp8_e32 v[138:139], v221
	v_cvt_pk_f32_fp8_sdwa v[220:221], v221 src0_sel:WORD_1
	v_cvt_pk_f32_fp8_e32 v[140:141], v222
	v_cvt_pk_f32_fp8_sdwa v[142:143], v222 src0_sel:WORD_1
	v_cvt_pk_f32_fp8_e32 v[144:145], v223
	v_cvt_pk_f32_fp8_sdwa v[222:223], v223 src0_sel:WORD_1
	v_pk_fma_f32 v[230:231], v[230:231], v[52:53], v[234:235] op_sel:[0,1,0]
	v_pk_fma_f32 v[234:235], v[240:241], v[52:53], v[238:239] op_sel:[0,1,0]
	v_pk_fma_f32 v[238:239], v[138:139], v[52:53], v[242:243] op_sel:[0,1,0]
	v_pk_fma_f32 v[220:221], v[220:221], v[52:53], v[224:225] op_sel:[0,1,0]
	v_pk_fma_f32 v[224:225], v[140:141], v[52:53], v[228:229] op_sel:[0,1,0]
	v_pk_fma_f32 v[228:229], v[142:143], v[52:53], v[232:233] op_sel:[0,1,0]
	v_pk_fma_f32 v[232:233], v[144:145], v[52:53], v[236:237] op_sel:[0,1,0]
	v_pk_fma_f32 v[222:223], v[222:223], v[52:53], v[226:227] op_sel:[0,1,0]
	v_cvt_pk_f32_fp8_e32 v[226:227], v216
	v_cvt_pk_f32_fp8_sdwa v[236:237], v216 src0_sel:WORD_1
	v_cvt_pk_f32_fp8_e32 v[240:241], v217
	v_cvt_pk_f32_fp8_sdwa v[216:217], v217 src0_sel:WORD_1
	v_cvt_pk_f32_fp8_e32 v[242:243], v218
	v_cvt_pk_f32_fp8_sdwa v[138:139], v218 src0_sel:WORD_1
	v_cvt_pk_f32_fp8_e32 v[140:141], v219
	v_cvt_pk_f32_fp8_sdwa v[218:219], v219 src0_sel:WORD_1
	v_pk_fma_f32 v[226:227], v[226:227], v[54:55], v[230:231] op_sel_hi:[1,0,1]
	v_pk_fma_f32 v[230:231], v[236:237], v[54:55], v[234:235] op_sel_hi:[1,0,1]
	v_pk_fma_f32 v[234:235], v[240:241], v[54:55], v[238:239] op_sel_hi:[1,0,1]
	v_pk_fma_f32 v[216:217], v[216:217], v[54:55], v[220:221] op_sel_hi:[1,0,1]
	v_pk_fma_f32 v[220:221], v[242:243], v[54:55], v[224:225] op_sel_hi:[1,0,1]
	v_pk_fma_f32 v[224:225], v[138:139], v[54:55], v[228:229] op_sel_hi:[1,0,1]
	v_pk_fma_f32 v[228:229], v[140:141], v[54:55], v[232:233] op_sel_hi:[1,0,1]
	v_pk_fma_f32 v[218:219], v[218:219], v[54:55], v[222:223] op_sel_hi:[1,0,1]
	v_cvt_pk_f32_fp8_e32 v[222:223], v212
	v_cvt_pk_f32_fp8_sdwa v[232:233], v212 src0_sel:WORD_1
	v_cvt_pk_f32_fp8_e32 v[236:237], v213
	v_cvt_pk_f32_fp8_sdwa v[212:213], v213 src0_sel:WORD_1
	v_cvt_pk_f32_fp8_e32 v[238:239], v214
	v_cvt_pk_f32_fp8_sdwa v[240:241], v214 src0_sel:WORD_1
	v_cvt_pk_f32_fp8_e32 v[242:243], v215
	v_cvt_pk_f32_fp8_sdwa v[214:215], v215 src0_sel:WORD_1
	v_mov_b32_e32 v128, v55
	v_pk_fma_f32 v[222:223], v[222:223], v[128:129], v[226:227] op_sel_hi:[1,0,1]
	v_pk_fma_f32 v[226:227], v[232:233], v[128:129], v[230:231] op_sel_hi:[1,0,1]
	v_pk_fma_f32 v[230:231], v[236:237], v[128:129], v[234:235] op_sel_hi:[1,0,1]
	v_pk_fma_f32 v[212:213], v[212:213], v[128:129], v[216:217] op_sel_hi:[1,0,1]
	v_pk_fma_f32 v[216:217], v[238:239], v[128:129], v[220:221] op_sel_hi:[1,0,1]
	v_pk_fma_f32 v[220:221], v[240:241], v[128:129], v[224:225] op_sel_hi:[1,0,1]
	v_pk_fma_f32 v[224:225], v[242:243], v[128:129], v[228:229] op_sel_hi:[1,0,1]
	v_pk_fma_f32 v[214:215], v[214:215], v[128:129], v[218:219] op_sel_hi:[1,0,1]
	v_cvt_pk_f32_fp8_e32 v[218:219], v200
	v_cvt_pk_f32_fp8_sdwa v[228:229], v200 src0_sel:WORD_1
	v_cvt_pk_f32_fp8_e32 v[232:233], v201
	v_cvt_pk_f32_fp8_sdwa v[200:201], v201 src0_sel:WORD_1
	v_cvt_pk_f32_fp8_e32 v[234:235], v202
	v_cvt_pk_f32_fp8_sdwa v[236:237], v202 src0_sel:WORD_1
	v_cvt_pk_f32_fp8_e32 v[238:239], v203
	v_cvt_pk_f32_fp8_sdwa v[202:203], v203 src0_sel:WORD_1
	v_pk_fma_f32 v[218:219], v[218:219], v[56:57], v[222:223] op_sel_hi:[1,0,1]
	v_pk_fma_f32 v[222:223], v[228:229], v[56:57], v[226:227] op_sel_hi:[1,0,1]
	v_pk_fma_f32 v[226:227], v[232:233], v[56:57], v[230:231] op_sel_hi:[1,0,1]
	v_pk_fma_f32 v[200:201], v[200:201], v[56:57], v[212:213] op_sel_hi:[1,0,1]
	v_pk_fma_f32 v[212:213], v[234:235], v[56:57], v[216:217] op_sel_hi:[1,0,1]
	v_pk_fma_f32 v[216:217], v[236:237], v[56:57], v[220:221] op_sel_hi:[1,0,1]
	v_pk_fma_f32 v[220:221], v[238:239], v[56:57], v[224:225] op_sel_hi:[1,0,1]
	v_pk_fma_f32 v[202:203], v[202:203], v[56:57], v[214:215] op_sel_hi:[1,0,1]
	v_cvt_pk_f32_fp8_e32 v[214:215], v196
	v_cvt_pk_f32_fp8_sdwa v[224:225], v196 src0_sel:WORD_1
	v_cvt_pk_f32_fp8_e32 v[228:229], v197
	v_cvt_pk_f32_fp8_sdwa v[196:197], v197 src0_sel:WORD_1
	v_cvt_pk_f32_fp8_e32 v[230:231], v198
	v_cvt_pk_f32_fp8_sdwa v[232:233], v198 src0_sel:WORD_1
	v_cvt_pk_f32_fp8_e32 v[234:235], v199
	v_cvt_pk_f32_fp8_sdwa v[198:199], v199 src0_sel:WORD_1
	v_pk_fma_f32 v[214:215], v[214:215], v[56:57], v[218:219] op_sel:[0,1,0]
	v_pk_fma_f32 v[218:219], v[224:225], v[56:57], v[222:223] op_sel:[0,1,0]
	v_pk_fma_f32 v[222:223], v[228:229], v[56:57], v[226:227] op_sel:[0,1,0]
	v_pk_fma_f32 v[196:197], v[196:197], v[56:57], v[200:201] op_sel:[0,1,0]
	v_pk_fma_f32 v[200:201], v[230:231], v[56:57], v[212:213] op_sel:[0,1,0]
	v_pk_fma_f32 v[212:213], v[232:233], v[56:57], v[216:217] op_sel:[0,1,0]
	v_pk_fma_f32 v[216:217], v[234:235], v[56:57], v[220:221] op_sel:[0,1,0]
	v_pk_fma_f32 v[198:199], v[198:199], v[56:57], v[202:203] op_sel:[0,1,0]
	v_cvt_pk_f32_fp8_e32 v[202:203], v192
	v_cvt_pk_f32_fp8_sdwa v[220:221], v192 src0_sel:WORD_1
	v_cvt_pk_f32_fp8_e32 v[224:225], v193
	v_cvt_pk_f32_fp8_sdwa v[192:193], v193 src0_sel:WORD_1
	v_cvt_pk_f32_fp8_e32 v[226:227], v194
	v_cvt_pk_f32_fp8_sdwa v[228:229], v194 src0_sel:WORD_1
	v_cvt_pk_f32_fp8_e32 v[230:231], v195
	v_cvt_pk_f32_fp8_sdwa v[194:195], v195 src0_sel:WORD_1
	v_pk_fma_f32 v[202:203], v[202:203], v[58:59], v[214:215] op_sel_hi:[1,0,1]
	v_pk_fma_f32 v[214:215], v[220:221], v[58:59], v[218:219] op_sel_hi:[1,0,1]
	v_pk_fma_f32 v[218:219], v[224:225], v[58:59], v[222:223] op_sel_hi:[1,0,1]
	v_pk_fma_f32 v[192:193], v[192:193], v[58:59], v[196:197] op_sel_hi:[1,0,1]
	v_pk_fma_f32 v[196:197], v[226:227], v[58:59], v[200:201] op_sel_hi:[1,0,1]
	v_pk_fma_f32 v[200:201], v[228:229], v[58:59], v[212:213] op_sel_hi:[1,0,1]
	v_pk_fma_f32 v[212:213], v[230:231], v[58:59], v[216:217] op_sel_hi:[1,0,1]
	v_pk_fma_f32 v[194:195], v[194:195], v[58:59], v[198:199] op_sel_hi:[1,0,1]
	v_cvt_pk_f32_fp8_e32 v[198:199], v184
	v_cvt_pk_f32_fp8_sdwa v[216:217], v184 src0_sel:WORD_1
	v_cvt_pk_f32_fp8_e32 v[220:221], v185
	v_cvt_pk_f32_fp8_sdwa v[184:185], v185 src0_sel:WORD_1
	v_cvt_pk_f32_fp8_e32 v[222:223], v186
	v_cvt_pk_f32_fp8_sdwa v[224:225], v186 src0_sel:WORD_1
	v_cvt_pk_f32_fp8_e32 v[226:227], v187
	v_cvt_pk_f32_fp8_sdwa v[186:187], v187 src0_sel:WORD_1
	v_mov_b32_e32 v228, v59
	v_pk_fma_f32 v[198:199], v[198:199], v[228:229], v[202:203] op_sel_hi:[1,0,1]
	v_pk_fma_f32 v[202:203], v[216:217], v[228:229], v[214:215] op_sel_hi:[1,0,1]
	v_pk_fma_f32 v[214:215], v[220:221], v[228:229], v[218:219] op_sel_hi:[1,0,1]
	v_pk_fma_f32 v[184:185], v[184:185], v[228:229], v[192:193] op_sel_hi:[1,0,1]
	v_pk_fma_f32 v[192:193], v[222:223], v[228:229], v[196:197] op_sel_hi:[1,0,1]
	v_pk_fma_f32 v[196:197], v[224:225], v[228:229], v[200:201] op_sel_hi:[1,0,1]
	v_pk_fma_f32 v[200:201], v[226:227], v[228:229], v[212:213] op_sel_hi:[1,0,1]
	v_pk_fma_f32 v[186:187], v[186:187], v[228:229], v[194:195] op_sel_hi:[1,0,1]
	v_cvt_pk_f32_fp8_e32 v[194:195], v180
	v_cvt_pk_f32_fp8_sdwa v[212:213], v180 src0_sel:WORD_1
	v_cvt_pk_f32_fp8_e32 v[216:217], v181
	v_cvt_pk_f32_fp8_sdwa v[180:181], v181 src0_sel:WORD_1
	v_cvt_pk_f32_fp8_e32 v[218:219], v182
	v_cvt_pk_f32_fp8_sdwa v[220:221], v182 src0_sel:WORD_1
	v_cvt_pk_f32_fp8_e32 v[222:223], v183
	v_cvt_pk_f32_fp8_sdwa v[182:183], v183 src0_sel:WORD_1
	v_pk_fma_f32 v[194:195], v[194:195], v[60:61], v[198:199] op_sel_hi:[1,0,1]
	v_pk_fma_f32 v[198:199], v[212:213], v[60:61], v[202:203] op_sel_hi:[1,0,1]
	v_pk_fma_f32 v[202:203], v[216:217], v[60:61], v[214:215] op_sel_hi:[1,0,1]
	v_pk_fma_f32 v[180:181], v[180:181], v[60:61], v[184:185] op_sel_hi:[1,0,1]
	v_pk_fma_f32 v[184:185], v[218:219], v[60:61], v[192:193] op_sel_hi:[1,0,1]
	v_pk_fma_f32 v[192:193], v[220:221], v[60:61], v[196:197] op_sel_hi:[1,0,1]
	v_pk_fma_f32 v[196:197], v[222:223], v[60:61], v[200:201] op_sel_hi:[1,0,1]
	v_pk_fma_f32 v[182:183], v[182:183], v[60:61], v[186:187] op_sel_hi:[1,0,1]
	v_cvt_pk_f32_fp8_e32 v[186:187], v172
	v_cvt_pk_f32_fp8_sdwa v[200:201], v172 src0_sel:WORD_1
	v_cvt_pk_f32_fp8_e32 v[212:213], v173
	v_cvt_pk_f32_fp8_sdwa v[172:173], v173 src0_sel:WORD_1
	v_cvt_pk_f32_fp8_e32 v[214:215], v174
	v_cvt_pk_f32_fp8_sdwa v[216:217], v174 src0_sel:WORD_1
	v_cvt_pk_f32_fp8_e32 v[218:219], v175
	v_cvt_pk_f32_fp8_sdwa v[174:175], v175 src0_sel:WORD_1
	v_pk_fma_f32 v[186:187], v[186:187], v[60:61], v[194:195] op_sel:[0,1,0]
	v_pk_fma_f32 v[194:195], v[200:201], v[60:61], v[198:199] op_sel:[0,1,0]
	v_pk_fma_f32 v[198:199], v[212:213], v[60:61], v[202:203] op_sel:[0,1,0]
	v_pk_fma_f32 v[172:173], v[172:173], v[60:61], v[180:181] op_sel:[0,1,0]
	v_pk_fma_f32 v[180:181], v[214:215], v[60:61], v[184:185] op_sel:[0,1,0]
	v_pk_fma_f32 v[184:185], v[216:217], v[60:61], v[192:193] op_sel:[0,1,0]
	v_pk_fma_f32 v[192:193], v[218:219], v[60:61], v[196:197] op_sel:[0,1,0]
	v_pk_fma_f32 v[174:175], v[174:175], v[60:61], v[182:183] op_sel:[0,1,0]
	v_cvt_pk_f32_fp8_e32 v[182:183], v168
	v_cvt_pk_f32_fp8_sdwa v[196:197], v168 src0_sel:WORD_1
	v_cvt_pk_f32_fp8_e32 v[200:201], v169
	v_cvt_pk_f32_fp8_sdwa v[168:169], v169 src0_sel:WORD_1
	v_cvt_pk_f32_fp8_e32 v[202:203], v170
	v_cvt_pk_f32_fp8_sdwa v[212:213], v170 src0_sel:WORD_1
	v_cvt_pk_f32_fp8_e32 v[214:215], v171
	v_cvt_pk_f32_fp8_sdwa v[170:171], v171 src0_sel:WORD_1
	v_pk_fma_f32 v[182:183], v[182:183], v[62:63], v[186:187] op_sel_hi:[1,0,1]
	v_pk_fma_f32 v[186:187], v[196:197], v[62:63], v[194:195] op_sel_hi:[1,0,1]
	v_pk_fma_f32 v[194:195], v[200:201], v[62:63], v[198:199] op_sel_hi:[1,0,1]
	v_pk_fma_f32 v[168:169], v[168:169], v[62:63], v[172:173] op_sel_hi:[1,0,1]
	v_pk_fma_f32 v[172:173], v[202:203], v[62:63], v[180:181] op_sel_hi:[1,0,1]
	v_pk_fma_f32 v[180:181], v[212:213], v[62:63], v[184:185] op_sel_hi:[1,0,1]
	v_pk_fma_f32 v[184:185], v[214:215], v[62:63], v[192:193] op_sel_hi:[1,0,1]
	v_pk_fma_f32 v[170:171], v[170:171], v[62:63], v[174:175] op_sel_hi:[1,0,1]
	v_cvt_pk_f32_fp8_e32 v[174:175], v164
	v_cvt_pk_f32_fp8_sdwa v[192:193], v164 src0_sel:WORD_1
	v_cvt_pk_f32_fp8_e32 v[196:197], v165
	v_cvt_pk_f32_fp8_sdwa v[164:165], v165 src0_sel:WORD_1
	v_cvt_pk_f32_fp8_e32 v[198:199], v166
	v_cvt_pk_f32_fp8_sdwa v[200:201], v166 src0_sel:WORD_1
	v_cvt_pk_f32_fp8_e32 v[202:203], v167
	v_cvt_pk_f32_fp8_sdwa v[166:167], v167 src0_sel:WORD_1
	v_mov_b32_e32 v212, v63
	v_pk_fma_f32 v[174:175], v[174:175], v[212:213], v[182:183] op_sel_hi:[1,0,1]
	v_pk_fma_f32 v[182:183], v[192:193], v[212:213], v[186:187] op_sel_hi:[1,0,1]
	v_pk_fma_f32 v[186:187], v[196:197], v[212:213], v[194:195] op_sel_hi:[1,0,1]
	v_pk_fma_f32 v[164:165], v[164:165], v[212:213], v[168:169] op_sel_hi:[1,0,1]
	v_pk_fma_f32 v[168:169], v[198:199], v[212:213], v[172:173] op_sel_hi:[1,0,1]
	v_pk_fma_f32 v[172:173], v[200:201], v[212:213], v[180:181] op_sel_hi:[1,0,1]
	v_pk_fma_f32 v[180:181], v[202:203], v[212:213], v[184:185] op_sel_hi:[1,0,1]
	v_pk_fma_f32 v[166:167], v[166:167], v[212:213], v[170:171] op_sel_hi:[1,0,1]
	v_permlane32_swap_b32_e32 v174, v168
	v_permlane32_swap_b32_e32 v175, v169
	v_permlane32_swap_b32_e32 v182, v172
	v_permlane32_swap_b32_e32 v183, v173
	v_permlane32_swap_b32_e32 v186, v180
	v_permlane32_swap_b32_e32 v187, v181
	v_permlane32_swap_b32_e32 v164, v166
	v_permlane32_swap_b32_e32 v165, v167
	v_add_f32_e32 v168, v174, v168
	v_add_f32_e32 v169, v175, v169
	v_add_f32_e32 v170, v182, v172
	v_add_f32_e32 v171, v183, v173
	v_add_f32_e32 v172, v186, v180
	v_add_f32_e32 v173, v187, v181
	v_add_f32_e32 v164, v164, v166
	v_add_f32_e32 v165, v165, v167
	v_permlane16_swap_b32_e32 v168, v172
	v_permlane16_swap_b32_e32 v169, v173
	v_permlane16_swap_b32_e32 v170, v164
	v_permlane16_swap_b32_e32 v171, v165
	v_pk_add_f32 v[166:167], v[168:169], v[172:173]
	v_pk_add_f32 v[164:165], v[170:171], v[164:165]
	s_ashr_i32 s7, s6, 31
	v_cndmask_b32_e64 v168, v166, v164, s[0:1]
	v_cndmask_b32_e64 v170, v164, v166, s[0:1]
	v_cndmask_b32_e64 v164, v167, v165, s[0:1]
	v_mov_b32_dpp v168, v168 row_ror:8 row_mask:0xf bank_mask:0xf bound_ctrl:1
	v_cndmask_b32_e64 v171, v165, v167, s[0:1]
	v_mov_b32_dpp v169, v164 row_ror:8 row_mask:0xf bank_mask:0xf bound_ctrl:1
	v_pk_add_f32 v[166:167], v[170:171], v[168:169]
	s_lshl_b64 s[8:9], s[6:7], 11
	v_pk_mul_f32 v[164:165], v[166:167], v[166:167]
	v_cvt_pk_bf16_f32 v168, v166, v167
	v_add_f32_e32 v164, v164, v165
	v_lshl_add_u64 v[166:167], v[130:131], 0, s[8:9]
	global_store_dword v[166:167], v168, off
	v_add_f32_dpp v164, v164, v164 quad_perm:[1,0,3,2] row_mask:0xf bank_mask:0xf bound_ctrl:1
	s_nop 1
	v_add_f32_dpp v164, v164, v164 quad_perm:[2,3,0,1] row_mask:0xf bank_mask:0xf bound_ctrl:1
	s_nop 1
	v_add_f32_dpp v164, v164, v164 row_half_mirror row_mask:0xf bank_mask:0xf bound_ctrl:1
	s_nop 1
	v_add_f32_dpp v164, v164, v164 row_ror:8 row_mask:0xf bank_mask:0xf bound_ctrl:1
	v_mov_b32_e32 v165, v164
	s_nop 1
	v_permlane16_swap_b32_e32 v164, v165
	v_add_f32_e32 v164, v164, v165
	v_mov_b32_e32 v165, v164
	s_nop 1
	v_permlane32_swap_b32_e32 v164, v165
	s_and_saveexec_b64 s[8:9], s[2:3]
	s_lshl_b64 s[10:11], s[6:7], 2
	s_add_u32 s10, s12, s10
	v_add_f32_e32 v164, v164, v165
	s_addc_u32 s11, s13, s11
	global_store_dword v129, v164, s[10:11]
	s_or_b64 exec, exec, s[8:9]
